# P1 S5 tap-table (KT) loop re-emitted: Bbar rows fetched once per half and broadcast by v_readlane, C/abar operands double-buffered; same f32 ops per output
# speedup vs baseline: 1.0166x; 1.0123x over previous
; __device__ __forceinline__ void ph1_small(const Args& a, int tid, int wave, int lane, int G, int bid) {
;     ...
;     {
;         const float* cre = a.in[I_CRE]; const float* cim = a.in[I_CIM]; const float* BBAR = (const float*)(a.ws + WS_BBAR); const float* POW = (const float*)(a.ws + WS_POW); float* KT = (float*)(a.ws + WS_KT);
;         for (int idx = (tid < 128 ? bid * 128 + tid : SSMG * SL * 16); idx < SSMG * SL * 16; idx += G * 128) {
;             const int g = idx >> 9, tau = (idx >> 4) & 31, p = idx & 15; float s[16];
; #pragma unroll
;             for (int q = 0; q < 16; ++q) s[q] = 0.f;
; #pragma unroll 8
;             for (int n = 0; n < 64; ++n) { const float cr = cre[((size_t)g * 16 + p) * 64 + n], ci = cim[((size_t)g * 16 + p) * 64 + n];
;                 const float pr = POW[(((size_t)g * 65 + tau) * 64 + n) * 2], pi = POW[(((size_t)g * 65 + tau) * 64 + n) * 2 + 1];
;                 const float er = cr * pr - ci * pi, ei = cr * pi + ci * pr;
;                 const f32x4* bp = (const f32x4*)(BBAR + ((size_t)g * 64 + n) * 32);
; #pragma unroll
;                 for (int q = 0; q < 8; ++q) { const f32x4 bb = bp[q]; s[2 * q] += er * bb[0] - ei * bb[1]; s[2 * q + 1] += er * bb[2] - ei * bb[3]; } }
;             { const float dv = (tau == 0) ? a.in[I_SD][g * 16 + p] : 0.0f;
; #pragma unroll
;               for (int q = 0; q < 16; ++q) s[q] += (q == p) ? dv : 0.0f; }
;             float* kp = KT + (((size_t)g * 64 + tau) * 16 + p) * 16;
; #pragma unroll
;             for (int q = 0; q < 4; ++q) *(f32x4*)(kp + 4 * q) = (f32x4){s[4 * q], s[4 * q + 1], s[4 * q + 2], s[4 * q + 3]}; }
;     }
.LBB0_104:
	v_readlane_b32 s0, v251, 15
	v_readlane_b32 s1, v251, 16
	s_and_saveexec_b64 s[44:45], s[0:1]
	s_cbranch_execz .LBB0_111
	v_writelane_b32 v249, s16, 0
	v_writelane_b32 v249, s17, 1
	v_writelane_b32 v249, s36, 2
	v_writelane_b32 v249, s37, 3
	v_writelane_b32 v249, s38, 4
	v_writelane_b32 v249, s39, 5
	v_writelane_b32 v249, s40, 6
	v_writelane_b32 v249, s41, 7
	v_writelane_b32 v249, s42, 8
	v_writelane_b32 v249, s43, 9
	v_writelane_b32 v249, s52, 10
	v_writelane_b32 v249, s53, 11
	v_writelane_b32 v249, s54, 12
	v_writelane_b32 v249, s55, 13
	v_writelane_b32 v249, s56, 14
	v_writelane_b32 v249, s57, 15
	v_writelane_b32 v249, s58, 16
	v_writelane_b32 v249, s59, 17
	v_writelane_b32 v249, s62, 18
	v_writelane_b32 v249, s63, 19
	v_writelane_b32 v249, s64, 20
	v_writelane_b32 v249, s65, 21
	v_writelane_b32 v249, s80, 22
	v_writelane_b32 v249, s81, 23
	v_writelane_b32 v249, s82, 24
	v_writelane_b32 v249, s83, 25
	v_writelane_b32 v249, s84, 26
	v_writelane_b32 v249, s85, 27
	v_writelane_b32 v249, s86, 28
	v_writelane_b32 v249, s87, 29
	v_writelane_b32 v249, s88, 30
	v_writelane_b32 v249, s89, 31
	v_readlane_b32 s0, v250, 33
	v_lshlrev_b32_e32 v30, 8, v160
	v_mov_b32_e32 v31, 0
	v_readlane_b32 s10, v250, 43
	v_readlane_b32 s11, v250, 44
	v_readlane_b32 s12, v250, 45
	v_readlane_b32 s13, v250, 46
	v_lshl_add_u64 v[34:35], s[10:11], 0, v[30:31]
	s_mov_b64 s[46:47], 0
	v_lshl_add_u64 v[32:33], s[12:13], 0, v[30:31]
	v_mov_b32_e32 v68, v159
	v_readlane_b32 s1, v250, 34
	v_readlane_b32 s2, v250, 35
	v_readlane_b32 s3, v250, 36
	v_readlane_b32 s4, v250, 37
	v_readlane_b32 s5, v250, 38
	v_readlane_b32 s6, v250, 39
	v_readlane_b32 s7, v250, 40
	v_readlane_b32 s8, v250, 41
	v_readlane_b32 s9, v250, 42
	v_readlane_b32 s14, v250, 47
	v_readlane_b32 s15, v250, 48
	s_branch .LBB0_107

; __device__ __forceinline__ void ph1_small(const Args& a, int tid, int wave, int lane, int G, int bid) {
;     ...
;     {
;         const float* cre = a.in[I_CRE]; const float* cim = a.in[I_CIM]; const float* BBAR = (const float*)(a.ws + WS_BBAR); const float* POW = (const float*)(a.ws + WS_POW); float* KT = (float*)(a.ws + WS_KT);
;         for (int idx = (tid < 128 ? bid * 128 + tid : SSMG * SL * 16); idx < SSMG * SL * 16; idx += G * 128) {
;             const int g = idx >> 9, tau = (idx >> 4) & 31, p = idx & 15; float s[16];
; #pragma unroll
;             for (int q = 0; q < 16; ++q) s[q] = 0.f;
; #pragma unroll 8
;             for (int n = 0; n < 64; ++n) { const float cr = cre[((size_t)g * 16 + p) * 64 + n], ci = cim[((size_t)g * 16 + p) * 64 + n];
;                 const float pr = POW[(((size_t)g * 65 + tau) * 64 + n) * 2], pi = POW[(((size_t)g * 65 + tau) * 64 + n) * 2 + 1];
;                 const float er = cr * pr - ci * pi, ei = cr * pi + ci * pr;
;                 const f32x4* bp = (const f32x4*)(BBAR + ((size_t)g * 64 + n) * 32);
; #pragma unroll
;                 for (int q = 0; q < 8; ++q) { const f32x4 bb = bp[q]; s[2 * q] += er * bb[0] - ei * bb[1]; s[2 * q + 1] += er * bb[2] - ei * bb[3]; } }
.LBB0_107:
	v_ashrrev_i32_e32 v36, 9, v68
	v_bfe_u32 v30, v68, 4, 5
	v_mul_hi_i32_i24_e32 v3, 0x41, v36
	s_waitcnt vmcnt(1)
	v_mul_i32_i24_e32 v2, 0x41, v36
	v_ashrrev_i32_e32 v37, 31, v36
	v_lshl_add_u64 v[2:3], v[2:3], 0, v[30:31]
	v_lshlrev_b64 v[40:41], 9, v[2:3]
	v_lshlrev_b64 v[2:3], 12, v[36:37]
	v_readlane_b32 s72, v250, 51
	v_lshrrev_b32_e32 v69, 4, v68
	v_lshlrev_b64 v[38:39], 13, v[36:37]
	v_lshl_add_u64 v[42:43], v[32:33], 0, v[2:3]
	v_lshl_add_u64 v[44:45], v[34:35], 0, v[2:3]
	s_mov_b64 s[48:49], 0
	v_mov_b32_e32 v62, 0
	v_mov_b32_e32 v63, v31
	v_mov_b32_e32 v56, 0
	v_mov_b32_e32 v57, v31
	v_mov_b32_e32 v54, 0
	v_mov_b32_e32 v55, v31
	v_mov_b32_e32 v52, 0
	v_mov_b32_e32 v53, v31
	v_mov_b32_e32 v50, 0
	v_mov_b32_e32 v51, v31
	v_mov_b32_e32 v58, 0
	v_mov_b32_e32 v59, v31
	v_mov_b32_e32 v60, 0
	v_mov_b32_e32 v61, v31
	v_mov_b32_e32 v64, 0
	v_mov_b32_e32 v65, v31
	v_readlane_b32 s74, v250, 53
	v_readlane_b32 s75, v250, 54
	v_readlane_b32 s73, v250, 52
	v_readlane_b32 s98, v250, 53
	v_readlane_b32 s99, v250, 54
	v_readfirstlane_b32 s16, v38
	v_readlane_b32 s100, v250, 53
	v_readlane_b32 s101, v250, 54
	s_add_u32 s98, s98, s16
	s_addc_u32 s99, s99, 0
	s_add_u32 s98, s98, 0x500000
	s_addc_u32 s99, s99, 0
	s_add_u32 s100, s100, 0x600000
	s_addc_u32 s101, s101, 0
	v_mbcnt_lo_u32_b32 v246, -1, 0
	v_mbcnt_hi_u32_b32 v246, -1, v246
	v_lshlrev_b32_e32 v246, 2, v246
	s_mov_b32 s32, 2
.Lkta_half:
	global_load_dword v2, v246, s[98:99] offset:0
	global_load_dword v3, v246, s[98:99] offset:256
	global_load_dword v4, v246, s[98:99] offset:512
	global_load_dword v5, v246, s[98:99] offset:768
	global_load_dword v6, v246, s[98:99] offset:1024
	global_load_dword v7, v246, s[98:99] offset:1280
	global_load_dword v8, v246, s[98:99] offset:1536
	global_load_dword v9, v246, s[98:99] offset:1792
	global_load_dword v10, v246, s[98:99] offset:2048
	global_load_dword v11, v246, s[98:99] offset:2304
	global_load_dword v12, v246, s[98:99] offset:2560
	global_load_dword v13, v246, s[98:99] offset:2816
	global_load_dword v14, v246, s[98:99] offset:3072
	global_load_dword v15, v246, s[98:99] offset:3328
	global_load_dword v16, v246, s[98:99] offset:3584
	global_load_dword v17, v246, s[98:99] offset:3840
	global_load_dwordx4 v[18:21], v[44:45], off offset:0
	global_load_dwordx4 v[22:25], v[42:43], off offset:0
	global_load_dwordx4 v[26:29], v40, s[100:101] offset:0
	global_load_dwordx4 v[46:49], v40, s[100:101] offset:16
	global_load_dwordx4 v[70:73], v[44:45], off offset:16
	global_load_dwordx4 v[74:77], v[42:43], off offset:16
	global_load_dwordx4 v[78:81], v40, s[100:101] offset:32
	global_load_dwordx4 v[82:85], v40, s[100:101] offset:48
	s_waitcnt vmcnt(4)
	v_readlane_b32 s16, v2, 0
	v_readlane_b32 s17, v2, 2
	v_readlane_b32 s36, v2, 1
	v_readlane_b32 s37, v2, 3
	v_readlane_b32 s38, v2, 4
	v_readlane_b32 s39, v2, 6
	v_readlane_b32 s40, v2, 5
	v_readlane_b32 s41, v2, 7
	v_readlane_b32 s42, v2, 8
	v_readlane_b32 s43, v2, 10
	v_readlane_b32 s52, v2, 9
	v_readlane_b32 s53, v2, 11
	v_readlane_b32 s54, v2, 12
	v_readlane_b32 s55, v2, 14
	v_readlane_b32 s56, v2, 13
	v_readlane_b32 s57, v2, 15
	v_readlane_b32 s58, v2, 16
	v_readlane_b32 s59, v2, 18
	v_readlane_b32 s62, v2, 17
	v_readlane_b32 s63, v2, 19
	v_readlane_b32 s64, v2, 20
	v_readlane_b32 s65, v2, 22
	v_readlane_b32 s80, v2, 21
	v_readlane_b32 s81, v2, 23
	v_readlane_b32 s82, v2, 24
	v_readlane_b32 s83, v2, 26
	v_readlane_b32 s84, v2, 25
	v_readlane_b32 s85, v2, 27
	v_readlane_b32 s86, v2, 28
	v_readlane_b32 s87, v2, 30
	v_readlane_b32 s88, v2, 29
	v_readlane_b32 s89, v2, 31
	v_mul_f32_e32 v244, v18, v26
	v_mul_f32_e32 v245, v22, v27
	v_sub_f32_e32 v86, v244, v245
	v_mul_f32_e32 v244, v22, v26
	v_mul_f32_e32 v245, v18, v27
	v_add_f32_e32 v88, v244, v245
	v_pk_mul_f32 v[90:91], v[88:89], s[36:37] op_sel_hi:[0,1]
	v_pk_fma_f32 v[90:91], v[86:87], s[16:17], v[90:91] op_sel_hi:[0,1,1] neg_lo:[0,0,1] neg_hi:[0,0,1]
	v_pk_add_f32 v[56:57], v[56:57], v[90:91]
	v_pk_mul_f32 v[90:91], v[88:89], s[40:41] op_sel_hi:[0,1]
	v_pk_fma_f32 v[90:91], v[86:87], s[38:39], v[90:91] op_sel_hi:[0,1,1] neg_lo:[0,0,1] neg_hi:[0,0,1]
	v_pk_add_f32 v[54:55], v[54:55], v[90:91]
	v_pk_mul_f32 v[90:91], v[88:89], s[52:53] op_sel_hi:[0,1]
	v_pk_fma_f32 v[90:91], v[86:87], s[42:43], v[90:91] op_sel_hi:[0,1,1] neg_lo:[0,0,1] neg_hi:[0,0,1]
	v_pk_add_f32 v[52:53], v[52:53], v[90:91]
	v_pk_mul_f32 v[90:91], v[88:89], s[56:57] op_sel_hi:[0,1]
	v_pk_fma_f32 v[90:91], v[86:87], s[54:55], v[90:91] op_sel_hi:[0,1,1] neg_lo:[0,0,1] neg_hi:[0,0,1]
	v_pk_add_f32 v[50:51], v[50:51], v[90:91]
	v_pk_mul_f32 v[90:91], v[88:89], s[62:63] op_sel_hi:[0,1]
	v_pk_fma_f32 v[90:91], v[86:87], s[58:59], v[90:91] op_sel_hi:[0,1,1] neg_lo:[0,0,1] neg_hi:[0,0,1]
	v_pk_add_f32 v[58:59], v[58:59], v[90:91]
	v_pk_mul_f32 v[90:91], v[88:89], s[80:81] op_sel_hi:[0,1]
	v_pk_fma_f32 v[90:91], v[86:87], s[64:65], v[90:91] op_sel_hi:[0,1,1] neg_lo:[0,0,1] neg_hi:[0,0,1]
	v_pk_add_f32 v[60:61], v[60:61], v[90:91]
	v_pk_mul_f32 v[90:91], v[88:89], s[84:85] op_sel_hi:[0,1]
	v_pk_fma_f32 v[90:91], v[86:87], s[82:83], v[90:91] op_sel_hi:[0,1,1] neg_lo:[0,0,1] neg_hi:[0,0,1]
	v_pk_add_f32 v[64:65], v[64:65], v[90:91]
	v_pk_mul_f32 v[90:91], v[88:89], s[88:89] op_sel_hi:[0,1]
	v_pk_fma_f32 v[90:91], v[86:87], s[86:87], v[90:91] op_sel_hi:[0,1,1] neg_lo:[0,0,1] neg_hi:[0,0,1]
	v_pk_add_f32 v[62:63], v[62:63], v[90:91]
	v_readlane_b32 s16, v2, 32
	v_readlane_b32 s17, v2, 34
	v_readlane_b32 s36, v2, 33
	v_readlane_b32 s37, v2, 35
	v_readlane_b32 s38, v2, 36
	v_readlane_b32 s39, v2, 38
	v_readlane_b32 s40, v2, 37
	v_readlane_b32 s41, v2, 39
	v_readlane_b32 s42, v2, 40
; __device__ __forceinline__ void ph1_small(const Args& a, int tid, int wave, int lane, int G, int bid) {
;     ...
; #pragma unroll 8
;             for (int n = 0; n < 64; ++n) { const float cr = cre[((size_t)g * 16 + p) * 64 + n], ci = cim[((size_t)g * 16 + p) * 64 + n];
;                 const float pr = POW[(((size_t)g * 65 + tau) * 64 + n) * 2], pi = POW[(((size_t)g * 65 + tau) * 64 + n) * 2 + 1];
;                 const float er = cr * pr - ci * pi, ei = cr * pi + ci * pr;
;                 const f32x4* bp = (const f32x4*)(BBAR + ((size_t)g * 64 + n) * 32);
; #pragma unroll
;                 for (int q = 0; q < 8; ++q) { const f32x4 bb = bp[q]; s[2 * q] += er * bb[0] - ei * bb[1]; s[2 * q + 1] += er * bb[2] - ei * bb[3]; } }
	v_readlane_b32 s43, v2, 42
	v_readlane_b32 s52, v2, 41
	v_readlane_b32 s53, v2, 43
	v_readlane_b32 s54, v2, 44
	v_readlane_b32 s55, v2, 46
	v_readlane_b32 s56, v2, 45
	v_readlane_b32 s57, v2, 47
	v_readlane_b32 s58, v2, 48
	v_readlane_b32 s59, v2, 50
	v_readlane_b32 s62, v2, 49
	v_readlane_b32 s63, v2, 51
	v_readlane_b32 s64, v2, 52
	v_readlane_b32 s65, v2, 54
	v_readlane_b32 s80, v2, 53
	v_readlane_b32 s81, v2, 55
	v_readlane_b32 s82, v2, 56
	v_readlane_b32 s83, v2, 58
	v_readlane_b32 s84, v2, 57
	v_readlane_b32 s85, v2, 59
	v_readlane_b32 s86, v2, 60
	v_readlane_b32 s87, v2, 62
	v_readlane_b32 s88, v2, 61
	v_readlane_b32 s89, v2, 63
	v_mul_f32_e32 v244, v19, v28
	v_mul_f32_e32 v245, v23, v29
	v_sub_f32_e32 v86, v244, v245
	v_mul_f32_e32 v244, v23, v28
	v_mul_f32_e32 v245, v19, v29
	v_add_f32_e32 v88, v244, v245
	v_pk_mul_f32 v[90:91], v[88:89], s[36:37] op_sel_hi:[0,1]
	v_pk_fma_f32 v[90:91], v[86:87], s[16:17], v[90:91] op_sel_hi:[0,1,1] neg_lo:[0,0,1] neg_hi:[0,0,1]
	v_pk_add_f32 v[56:57], v[56:57], v[90:91]
	v_pk_mul_f32 v[90:91], v[88:89], s[40:41] op_sel_hi:[0,1]
	v_pk_fma_f32 v[90:91], v[86:87], s[38:39], v[90:91] op_sel_hi:[0,1,1] neg_lo:[0,0,1] neg_hi:[0,0,1]
	v_pk_add_f32 v[54:55], v[54:55], v[90:91]
	v_pk_mul_f32 v[90:91], v[88:89], s[52:53] op_sel_hi:[0,1]
	v_pk_fma_f32 v[90:91], v[86:87], s[42:43], v[90:91] op_sel_hi:[0,1,1] neg_lo:[0,0,1] neg_hi:[0,0,1]
	v_pk_add_f32 v[52:53], v[52:53], v[90:91]
	v_pk_mul_f32 v[90:91], v[88:89], s[56:57] op_sel_hi:[0,1]
	v_pk_fma_f32 v[90:91], v[86:87], s[54:55], v[90:91] op_sel_hi:[0,1,1] neg_lo:[0,0,1] neg_hi:[0,0,1]
	v_pk_add_f32 v[50:51], v[50:51], v[90:91]
	v_pk_mul_f32 v[90:91], v[88:89], s[62:63] op_sel_hi:[0,1]
	v_pk_fma_f32 v[90:91], v[86:87], s[58:59], v[90:91] op_sel_hi:[0,1,1] neg_lo:[0,0,1] neg_hi:[0,0,1]
	v_pk_add_f32 v[58:59], v[58:59], v[90:91]
	v_pk_mul_f32 v[90:91], v[88:89], s[80:81] op_sel_hi:[0,1]
	v_pk_fma_f32 v[90:91], v[86:87], s[64:65], v[90:91] op_sel_hi:[0,1,1] neg_lo:[0,0,1] neg_hi:[0,0,1]
	v_pk_add_f32 v[60:61], v[60:61], v[90:91]
	v_pk_mul_f32 v[90:91], v[88:89], s[84:85] op_sel_hi:[0,1]
	v_pk_fma_f32 v[90:91], v[86:87], s[82:83], v[90:91] op_sel_hi:[0,1,1] neg_lo:[0,0,1] neg_hi:[0,0,1]
	v_pk_add_f32 v[64:65], v[64:65], v[90:91]
	v_pk_mul_f32 v[90:91], v[88:89], s[88:89] op_sel_hi:[0,1]
	v_pk_fma_f32 v[90:91], v[86:87], s[86:87], v[90:91] op_sel_hi:[0,1,1] neg_lo:[0,0,1] neg_hi:[0,0,1]
	v_pk_add_f32 v[62:63], v[62:63], v[90:91]
	v_readlane_b32 s16, v3, 0
	v_readlane_b32 s17, v3, 2
	v_readlane_b32 s36, v3, 1
	v_readlane_b32 s37, v3, 3
	v_readlane_b32 s38, v3, 4
	v_readlane_b32 s39, v3, 6
	v_readlane_b32 s40, v3, 5
	v_readlane_b32 s41, v3, 7
	v_readlane_b32 s42, v3, 8
	v_readlane_b32 s43, v3, 10
	v_readlane_b32 s52, v3, 9
	v_readlane_b32 s53, v3, 11
	v_readlane_b32 s54, v3, 12
	v_readlane_b32 s55, v3, 14
	v_readlane_b32 s56, v3, 13
	v_readlane_b32 s57, v3, 15
	v_readlane_b32 s58, v3, 16
	v_readlane_b32 s59, v3, 18
	v_readlane_b32 s62, v3, 17
	v_readlane_b32 s63, v3, 19
	v_readlane_b32 s64, v3, 20
	v_readlane_b32 s65, v3, 22
	v_readlane_b32 s80, v3, 21
	v_readlane_b32 s81, v3, 23
	v_readlane_b32 s82, v3, 24
	v_readlane_b32 s83, v3, 26
	v_readlane_b32 s84, v3, 25
	v_readlane_b32 s85, v3, 27
	v_readlane_b32 s86, v3, 28
	v_readlane_b32 s87, v3, 30
	v_readlane_b32 s88, v3, 29
	v_readlane_b32 s89, v3, 31
	v_mul_f32_e32 v244, v20, v46
	v_mul_f32_e32 v245, v24, v47
	v_sub_f32_e32 v86, v244, v245
	v_mul_f32_e32 v244, v24, v46
	v_mul_f32_e32 v245, v20, v47
	v_add_f32_e32 v88, v244, v245
	v_pk_mul_f32 v[90:91], v[88:89], s[36:37] op_sel_hi:[0,1]
	v_pk_fma_f32 v[90:91], v[86:87], s[16:17], v[90:91] op_sel_hi:[0,1,1] neg_lo:[0,0,1] neg_hi:[0,0,1]
	v_pk_add_f32 v[56:57], v[56:57], v[90:91]
	v_pk_mul_f32 v[90:91], v[88:89], s[40:41] op_sel_hi:[0,1]
	v_pk_fma_f32 v[90:91], v[86:87], s[38:39], v[90:91] op_sel_hi:[0,1,1] neg_lo:[0,0,1] neg_hi:[0,0,1]
	v_pk_add_f32 v[54:55], v[54:55], v[90:91]
	v_pk_mul_f32 v[90:91], v[88:89], s[52:53] op_sel_hi:[0,1]
	v_pk_fma_f32 v[90:91], v[86:87], s[42:43], v[90:91] op_sel_hi:[0,1,1] neg_lo:[0,0,1] neg_hi:[0,0,1]
	v_pk_add_f32 v[52:53], v[52:53], v[90:91]
	v_pk_mul_f32 v[90:91], v[88:89], s[56:57] op_sel_hi:[0,1]
	v_pk_fma_f32 v[90:91], v[86:87], s[54:55], v[90:91] op_sel_hi:[0,1,1] neg_lo:[0,0,1] neg_hi:[0,0,1]
	v_pk_add_f32 v[50:51], v[50:51], v[90:91]
	v_pk_mul_f32 v[90:91], v[88:89], s[62:63] op_sel_hi:[0,1]
	v_pk_fma_f32 v[90:91], v[86:87], s[58:59], v[90:91] op_sel_hi:[0,1,1] neg_lo:[0,0,1] neg_hi:[0,0,1]
	v_pk_add_f32 v[58:59], v[58:59], v[90:91]
	v_pk_mul_f32 v[90:91], v[88:89], s[80:81] op_sel_hi:[0,1]
	v_pk_fma_f32 v[90:91], v[86:87], s[64:65], v[90:91] op_sel_hi:[0,1,1] neg_lo:[0,0,1] neg_hi:[0,0,1]
	v_pk_add_f32 v[60:61], v[60:61], v[90:91]
	v_pk_mul_f32 v[90:91], v[88:89], s[84:85] op_sel_hi:[0,1]
	v_pk_fma_f32 v[90:91], v[86:87], s[82:83], v[90:91] op_sel_hi:[0,1,1] neg_lo:[0,0,1] neg_hi:[0,0,1]
	v_pk_add_f32 v[64:65], v[64:65], v[90:91]
	v_pk_mul_f32 v[90:91], v[88:89], s[88:89] op_sel_hi:[0,1]
	v_pk_fma_f32 v[90:91], v[86:87], s[86:87], v[90:91] op_sel_hi:[0,1,1] neg_lo:[0,0,1] neg_hi:[0,0,1]
	v_pk_add_f32 v[62:63], v[62:63], v[90:91]
	v_readlane_b32 s16, v3, 32
	v_readlane_b32 s17, v3, 34
	v_readlane_b32 s36, v3, 33
	v_readlane_b32 s37, v3, 35
	v_readlane_b32 s38, v3, 36
	v_readlane_b32 s39, v3, 38
	v_readlane_b32 s40, v3, 37
	v_readlane_b32 s41, v3, 39
	v_readlane_b32 s42, v3, 40
	v_readlane_b32 s43, v3, 42
	v_readlane_b32 s52, v3, 41
	v_readlane_b32 s53, v3, 43
	v_readlane_b32 s54, v3, 44
	v_readlane_b32 s55, v3, 46
	v_readlane_b32 s56, v3, 45
	v_readlane_b32 s57, v3, 47
	v_readlane_b32 s58, v3, 48
	v_readlane_b32 s59, v3, 50
; __device__ __forceinline__ void ph1_small(const Args& a, int tid, int wave, int lane, int G, int bid) {
;     ...
; #pragma unroll 8
;             for (int n = 0; n < 64; ++n) { const float cr = cre[((size_t)g * 16 + p) * 64 + n], ci = cim[((size_t)g * 16 + p) * 64 + n];
;                 const float pr = POW[(((size_t)g * 65 + tau) * 64 + n) * 2], pi = POW[(((size_t)g * 65 + tau) * 64 + n) * 2 + 1];
;                 const float er = cr * pr - ci * pi, ei = cr * pi + ci * pr;
;                 const f32x4* bp = (const f32x4*)(BBAR + ((size_t)g * 64 + n) * 32);
; #pragma unroll
;                 for (int q = 0; q < 8; ++q) { const f32x4 bb = bp[q]; s[2 * q] += er * bb[0] - ei * bb[1]; s[2 * q + 1] += er * bb[2] - ei * bb[3]; } }
	v_readlane_b32 s62, v3, 49
	v_readlane_b32 s63, v3, 51
	v_readlane_b32 s64, v3, 52
	v_readlane_b32 s65, v3, 54
	v_readlane_b32 s80, v3, 53
	v_readlane_b32 s81, v3, 55
	v_readlane_b32 s82, v3, 56
	v_readlane_b32 s83, v3, 58
	v_readlane_b32 s84, v3, 57
	v_readlane_b32 s85, v3, 59
	v_readlane_b32 s86, v3, 60
	v_readlane_b32 s87, v3, 62
	v_readlane_b32 s88, v3, 61
	v_readlane_b32 s89, v3, 63
	v_mul_f32_e32 v244, v21, v48
	v_mul_f32_e32 v245, v25, v49
	v_sub_f32_e32 v86, v244, v245
	v_mul_f32_e32 v244, v25, v48
	v_mul_f32_e32 v245, v21, v49
	v_add_f32_e32 v88, v244, v245
	v_pk_mul_f32 v[90:91], v[88:89], s[36:37] op_sel_hi:[0,1]
	v_pk_fma_f32 v[90:91], v[86:87], s[16:17], v[90:91] op_sel_hi:[0,1,1] neg_lo:[0,0,1] neg_hi:[0,0,1]
	v_pk_add_f32 v[56:57], v[56:57], v[90:91]
	v_pk_mul_f32 v[90:91], v[88:89], s[40:41] op_sel_hi:[0,1]
	v_pk_fma_f32 v[90:91], v[86:87], s[38:39], v[90:91] op_sel_hi:[0,1,1] neg_lo:[0,0,1] neg_hi:[0,0,1]
	v_pk_add_f32 v[54:55], v[54:55], v[90:91]
	v_pk_mul_f32 v[90:91], v[88:89], s[52:53] op_sel_hi:[0,1]
	v_pk_fma_f32 v[90:91], v[86:87], s[42:43], v[90:91] op_sel_hi:[0,1,1] neg_lo:[0,0,1] neg_hi:[0,0,1]
	v_pk_add_f32 v[52:53], v[52:53], v[90:91]
	v_pk_mul_f32 v[90:91], v[88:89], s[56:57] op_sel_hi:[0,1]
	v_pk_fma_f32 v[90:91], v[86:87], s[54:55], v[90:91] op_sel_hi:[0,1,1] neg_lo:[0,0,1] neg_hi:[0,0,1]
	v_pk_add_f32 v[50:51], v[50:51], v[90:91]
	v_pk_mul_f32 v[90:91], v[88:89], s[62:63] op_sel_hi:[0,1]
	v_pk_fma_f32 v[90:91], v[86:87], s[58:59], v[90:91] op_sel_hi:[0,1,1] neg_lo:[0,0,1] neg_hi:[0,0,1]
	v_pk_add_f32 v[58:59], v[58:59], v[90:91]
	v_pk_mul_f32 v[90:91], v[88:89], s[80:81] op_sel_hi:[0,1]
	v_pk_fma_f32 v[90:91], v[86:87], s[64:65], v[90:91] op_sel_hi:[0,1,1] neg_lo:[0,0,1] neg_hi:[0,0,1]
	v_pk_add_f32 v[60:61], v[60:61], v[90:91]
	v_pk_mul_f32 v[90:91], v[88:89], s[84:85] op_sel_hi:[0,1]
	v_pk_fma_f32 v[90:91], v[86:87], s[82:83], v[90:91] op_sel_hi:[0,1,1] neg_lo:[0,0,1] neg_hi:[0,0,1]
	v_pk_add_f32 v[64:65], v[64:65], v[90:91]
	v_pk_mul_f32 v[90:91], v[88:89], s[88:89] op_sel_hi:[0,1]
	v_pk_fma_f32 v[90:91], v[86:87], s[86:87], v[90:91] op_sel_hi:[0,1,1] neg_lo:[0,0,1] neg_hi:[0,0,1]
	v_pk_add_f32 v[62:63], v[62:63], v[90:91]
	global_load_dwordx4 v[18:21], v[44:45], off offset:32
	global_load_dwordx4 v[22:25], v[42:43], off offset:32
	global_load_dwordx4 v[26:29], v40, s[100:101] offset:64
	global_load_dwordx4 v[46:49], v40, s[100:101] offset:80
	s_waitcnt vmcnt(4)
	v_readlane_b32 s16, v4, 0
	v_readlane_b32 s17, v4, 2
	v_readlane_b32 s36, v4, 1
	v_readlane_b32 s37, v4, 3
	v_readlane_b32 s38, v4, 4
	v_readlane_b32 s39, v4, 6
	v_readlane_b32 s40, v4, 5
	v_readlane_b32 s41, v4, 7
	v_readlane_b32 s42, v4, 8
	v_readlane_b32 s43, v4, 10
	v_readlane_b32 s52, v4, 9
	v_readlane_b32 s53, v4, 11
	v_readlane_b32 s54, v4, 12
	v_readlane_b32 s55, v4, 14
	v_readlane_b32 s56, v4, 13
	v_readlane_b32 s57, v4, 15
	v_readlane_b32 s58, v4, 16
	v_readlane_b32 s59, v4, 18
	v_readlane_b32 s62, v4, 17
	v_readlane_b32 s63, v4, 19
	v_readlane_b32 s64, v4, 20
	v_readlane_b32 s65, v4, 22
	v_readlane_b32 s80, v4, 21
	v_readlane_b32 s81, v4, 23
	v_readlane_b32 s82, v4, 24
	v_readlane_b32 s83, v4, 26
	v_readlane_b32 s84, v4, 25
	v_readlane_b32 s85, v4, 27
	v_readlane_b32 s86, v4, 28
	v_readlane_b32 s87, v4, 30
	v_readlane_b32 s88, v4, 29
	v_readlane_b32 s89, v4, 31
	v_mul_f32_e32 v244, v70, v78
	v_mul_f32_e32 v245, v74, v79
	v_sub_f32_e32 v86, v244, v245
	v_mul_f32_e32 v244, v74, v78
	v_mul_f32_e32 v245, v70, v79
	v_add_f32_e32 v88, v244, v245
	v_pk_mul_f32 v[90:91], v[88:89], s[36:37] op_sel_hi:[0,1]
	v_pk_fma_f32 v[90:91], v[86:87], s[16:17], v[90:91] op_sel_hi:[0,1,1] neg_lo:[0,0,1] neg_hi:[0,0,1]
	v_pk_add_f32 v[56:57], v[56:57], v[90:91]
	v_pk_mul_f32 v[90:91], v[88:89], s[40:41] op_sel_hi:[0,1]
	v_pk_fma_f32 v[90:91], v[86:87], s[38:39], v[90:91] op_sel_hi:[0,1,1] neg_lo:[0,0,1] neg_hi:[0,0,1]
	v_pk_add_f32 v[54:55], v[54:55], v[90:91]
	v_pk_mul_f32 v[90:91], v[88:89], s[52:53] op_sel_hi:[0,1]
	v_pk_fma_f32 v[90:91], v[86:87], s[42:43], v[90:91] op_sel_hi:[0,1,1] neg_lo:[0,0,1] neg_hi:[0,0,1]
	v_pk_add_f32 v[52:53], v[52:53], v[90:91]
	v_pk_mul_f32 v[90:91], v[88:89], s[56:57] op_sel_hi:[0,1]
	v_pk_fma_f32 v[90:91], v[86:87], s[54:55], v[90:91] op_sel_hi:[0,1,1] neg_lo:[0,0,1] neg_hi:[0,0,1]
	v_pk_add_f32 v[50:51], v[50:51], v[90:91]
	v_pk_mul_f32 v[90:91], v[88:89], s[62:63] op_sel_hi:[0,1]
	v_pk_fma_f32 v[90:91], v[86:87], s[58:59], v[90:91] op_sel_hi:[0,1,1] neg_lo:[0,0,1] neg_hi:[0,0,1]
	v_pk_add_f32 v[58:59], v[58:59], v[90:91]
	v_pk_mul_f32 v[90:91], v[88:89], s[80:81] op_sel_hi:[0,1]
	v_pk_fma_f32 v[90:91], v[86:87], s[64:65], v[90:91] op_sel_hi:[0,1,1] neg_lo:[0,0,1] neg_hi:[0,0,1]
	v_pk_add_f32 v[60:61], v[60:61], v[90:91]
	v_pk_mul_f32 v[90:91], v[88:89], s[84:85] op_sel_hi:[0,1]
	v_pk_fma_f32 v[90:91], v[86:87], s[82:83], v[90:91] op_sel_hi:[0,1,1] neg_lo:[0,0,1] neg_hi:[0,0,1]
	v_pk_add_f32 v[64:65], v[64:65], v[90:91]
	v_pk_mul_f32 v[90:91], v[88:89], s[88:89] op_sel_hi:[0,1]
	v_pk_fma_f32 v[90:91], v[86:87], s[86:87], v[90:91] op_sel_hi:[0,1,1] neg_lo:[0,0,1] neg_hi:[0,0,1]
	v_pk_add_f32 v[62:63], v[62:63], v[90:91]
	v_readlane_b32 s16, v4, 32
	v_readlane_b32 s17, v4, 34
	v_readlane_b32 s36, v4, 33
	v_readlane_b32 s37, v4, 35
	v_readlane_b32 s38, v4, 36
	v_readlane_b32 s39, v4, 38
	v_readlane_b32 s40, v4, 37
	v_readlane_b32 s41, v4, 39
	v_readlane_b32 s42, v4, 40
	v_readlane_b32 s43, v4, 42
	v_readlane_b32 s52, v4, 41
	v_readlane_b32 s53, v4, 43
	v_readlane_b32 s54, v4, 44
	v_readlane_b32 s55, v4, 46
	v_readlane_b32 s56, v4, 45
	v_readlane_b32 s57, v4, 47
	v_readlane_b32 s58, v4, 48
	v_readlane_b32 s59, v4, 50
; __device__ __forceinline__ void ph1_small(const Args& a, int tid, int wave, int lane, int G, int bid) {
;     ...
; #pragma unroll 8
;             for (int n = 0; n < 64; ++n) { const float cr = cre[((size_t)g * 16 + p) * 64 + n], ci = cim[((size_t)g * 16 + p) * 64 + n];
;                 const float pr = POW[(((size_t)g * 65 + tau) * 64 + n) * 2], pi = POW[(((size_t)g * 65 + tau) * 64 + n) * 2 + 1];
;                 const float er = cr * pr - ci * pi, ei = cr * pi + ci * pr;
;                 const f32x4* bp = (const f32x4*)(BBAR + ((size_t)g * 64 + n) * 32);
; #pragma unroll
;                 for (int q = 0; q < 8; ++q) { const f32x4 bb = bp[q]; s[2 * q] += er * bb[0] - ei * bb[1]; s[2 * q + 1] += er * bb[2] - ei * bb[3]; } }
	v_readlane_b32 s62, v4, 49
	v_readlane_b32 s63, v4, 51
	v_readlane_b32 s64, v4, 52
	v_readlane_b32 s65, v4, 54
	v_readlane_b32 s80, v4, 53
	v_readlane_b32 s81, v4, 55
	v_readlane_b32 s82, v4, 56
	v_readlane_b32 s83, v4, 58
	v_readlane_b32 s84, v4, 57
	v_readlane_b32 s85, v4, 59
	v_readlane_b32 s86, v4, 60
	v_readlane_b32 s87, v4, 62
	v_readlane_b32 s88, v4, 61
	v_readlane_b32 s89, v4, 63
	v_mul_f32_e32 v244, v71, v80
	v_mul_f32_e32 v245, v75, v81
	v_sub_f32_e32 v86, v244, v245
	v_mul_f32_e32 v244, v75, v80
	v_mul_f32_e32 v245, v71, v81
	v_add_f32_e32 v88, v244, v245
	v_pk_mul_f32 v[90:91], v[88:89], s[36:37] op_sel_hi:[0,1]
	v_pk_fma_f32 v[90:91], v[86:87], s[16:17], v[90:91] op_sel_hi:[0,1,1] neg_lo:[0,0,1] neg_hi:[0,0,1]
	v_pk_add_f32 v[56:57], v[56:57], v[90:91]
	v_pk_mul_f32 v[90:91], v[88:89], s[40:41] op_sel_hi:[0,1]
	v_pk_fma_f32 v[90:91], v[86:87], s[38:39], v[90:91] op_sel_hi:[0,1,1] neg_lo:[0,0,1] neg_hi:[0,0,1]
	v_pk_add_f32 v[54:55], v[54:55], v[90:91]
	v_pk_mul_f32 v[90:91], v[88:89], s[52:53] op_sel_hi:[0,1]
	v_pk_fma_f32 v[90:91], v[86:87], s[42:43], v[90:91] op_sel_hi:[0,1,1] neg_lo:[0,0,1] neg_hi:[0,0,1]
	v_pk_add_f32 v[52:53], v[52:53], v[90:91]
	v_pk_mul_f32 v[90:91], v[88:89], s[56:57] op_sel_hi:[0,1]
	v_pk_fma_f32 v[90:91], v[86:87], s[54:55], v[90:91] op_sel_hi:[0,1,1] neg_lo:[0,0,1] neg_hi:[0,0,1]
	v_pk_add_f32 v[50:51], v[50:51], v[90:91]
	v_pk_mul_f32 v[90:91], v[88:89], s[62:63] op_sel_hi:[0,1]
	v_pk_fma_f32 v[90:91], v[86:87], s[58:59], v[90:91] op_sel_hi:[0,1,1] neg_lo:[0,0,1] neg_hi:[0,0,1]
	v_pk_add_f32 v[58:59], v[58:59], v[90:91]
	v_pk_mul_f32 v[90:91], v[88:89], s[80:81] op_sel_hi:[0,1]
	v_pk_fma_f32 v[90:91], v[86:87], s[64:65], v[90:91] op_sel_hi:[0,1,1] neg_lo:[0,0,1] neg_hi:[0,0,1]
	v_pk_add_f32 v[60:61], v[60:61], v[90:91]
	v_pk_mul_f32 v[90:91], v[88:89], s[84:85] op_sel_hi:[0,1]
	v_pk_fma_f32 v[90:91], v[86:87], s[82:83], v[90:91] op_sel_hi:[0,1,1] neg_lo:[0,0,1] neg_hi:[0,0,1]
	v_pk_add_f32 v[64:65], v[64:65], v[90:91]
	v_pk_mul_f32 v[90:91], v[88:89], s[88:89] op_sel_hi:[0,1]
	v_pk_fma_f32 v[90:91], v[86:87], s[86:87], v[90:91] op_sel_hi:[0,1,1] neg_lo:[0,0,1] neg_hi:[0,0,1]
	v_pk_add_f32 v[62:63], v[62:63], v[90:91]
	v_readlane_b32 s16, v5, 0
	v_readlane_b32 s17, v5, 2
	v_readlane_b32 s36, v5, 1
	v_readlane_b32 s37, v5, 3
	v_readlane_b32 s38, v5, 4
	v_readlane_b32 s39, v5, 6
	v_readlane_b32 s40, v5, 5
	v_readlane_b32 s41, v5, 7
	v_readlane_b32 s42, v5, 8
	v_readlane_b32 s43, v5, 10
	v_readlane_b32 s52, v5, 9
	v_readlane_b32 s53, v5, 11
	v_readlane_b32 s54, v5, 12
	v_readlane_b32 s55, v5, 14
	v_readlane_b32 s56, v5, 13
	v_readlane_b32 s57, v5, 15
	v_readlane_b32 s58, v5, 16
	v_readlane_b32 s59, v5, 18
	v_readlane_b32 s62, v5, 17
	v_readlane_b32 s63, v5, 19
	v_readlane_b32 s64, v5, 20
	v_readlane_b32 s65, v5, 22
	v_readlane_b32 s80, v5, 21
	v_readlane_b32 s81, v5, 23
	v_readlane_b32 s82, v5, 24
	v_readlane_b32 s83, v5, 26
	v_readlane_b32 s84, v5, 25
	v_readlane_b32 s85, v5, 27
	v_readlane_b32 s86, v5, 28
	v_readlane_b32 s87, v5, 30
	v_readlane_b32 s88, v5, 29
	v_readlane_b32 s89, v5, 31
	v_mul_f32_e32 v244, v72, v82
	v_mul_f32_e32 v245, v76, v83
	v_sub_f32_e32 v86, v244, v245
	v_mul_f32_e32 v244, v76, v82
	v_mul_f32_e32 v245, v72, v83
	v_add_f32_e32 v88, v244, v245
	v_pk_mul_f32 v[90:91], v[88:89], s[36:37] op_sel_hi:[0,1]
	v_pk_fma_f32 v[90:91], v[86:87], s[16:17], v[90:91] op_sel_hi:[0,1,1] neg_lo:[0,0,1] neg_hi:[0,0,1]
	v_pk_add_f32 v[56:57], v[56:57], v[90:91]
	v_pk_mul_f32 v[90:91], v[88:89], s[40:41] op_sel_hi:[0,1]
	v_pk_fma_f32 v[90:91], v[86:87], s[38:39], v[90:91] op_sel_hi:[0,1,1] neg_lo:[0,0,1] neg_hi:[0,0,1]
	v_pk_add_f32 v[54:55], v[54:55], v[90:91]
	v_pk_mul_f32 v[90:91], v[88:89], s[52:53] op_sel_hi:[0,1]
	v_pk_fma_f32 v[90:91], v[86:87], s[42:43], v[90:91] op_sel_hi:[0,1,1] neg_lo:[0,0,1] neg_hi:[0,0,1]
	v_pk_add_f32 v[52:53], v[52:53], v[90:91]
	v_pk_mul_f32 v[90:91], v[88:89], s[56:57] op_sel_hi:[0,1]
	v_pk_fma_f32 v[90:91], v[86:87], s[54:55], v[90:91] op_sel_hi:[0,1,1] neg_lo:[0,0,1] neg_hi:[0,0,1]
	v_pk_add_f32 v[50:51], v[50:51], v[90:91]
	v_pk_mul_f32 v[90:91], v[88:89], s[62:63] op_sel_hi:[0,1]
	v_pk_fma_f32 v[90:91], v[86:87], s[58:59], v[90:91] op_sel_hi:[0,1,1] neg_lo:[0,0,1] neg_hi:[0,0,1]
	v_pk_add_f32 v[58:59], v[58:59], v[90:91]
	v_pk_mul_f32 v[90:91], v[88:89], s[80:81] op_sel_hi:[0,1]
	v_pk_fma_f32 v[90:91], v[86:87], s[64:65], v[90:91] op_sel_hi:[0,1,1] neg_lo:[0,0,1] neg_hi:[0,0,1]
	v_pk_add_f32 v[60:61], v[60:61], v[90:91]
	v_pk_mul_f32 v[90:91], v[88:89], s[84:85] op_sel_hi:[0,1]
	v_pk_fma_f32 v[90:91], v[86:87], s[82:83], v[90:91] op_sel_hi:[0,1,1] neg_lo:[0,0,1] neg_hi:[0,0,1]
	v_pk_add_f32 v[64:65], v[64:65], v[90:91]
	v_pk_mul_f32 v[90:91], v[88:89], s[88:89] op_sel_hi:[0,1]
	v_pk_fma_f32 v[90:91], v[86:87], s[86:87], v[90:91] op_sel_hi:[0,1,1] neg_lo:[0,0,1] neg_hi:[0,0,1]
	v_pk_add_f32 v[62:63], v[62:63], v[90:91]
	v_readlane_b32 s16, v5, 32
	v_readlane_b32 s17, v5, 34
	v_readlane_b32 s36, v5, 33
	v_readlane_b32 s37, v5, 35
	v_readlane_b32 s38, v5, 36
	v_readlane_b32 s39, v5, 38
	v_readlane_b32 s40, v5, 37
	v_readlane_b32 s41, v5, 39
	v_readlane_b32 s42, v5, 40
	v_readlane_b32 s43, v5, 42
	v_readlane_b32 s52, v5, 41
	v_readlane_b32 s53, v5, 43
	v_readlane_b32 s54, v5, 44
	v_readlane_b32 s55, v5, 46
	v_readlane_b32 s56, v5, 45
	v_readlane_b32 s57, v5, 47
	v_readlane_b32 s58, v5, 48
	v_readlane_b32 s59, v5, 50
	v_readlane_b32 s62, v5, 49
	v_readlane_b32 s63, v5, 51
	v_readlane_b32 s64, v5, 52
	v_readlane_b32 s65, v5, 54
	v_readlane_b32 s80, v5, 53
	v_readlane_b32 s81, v5, 55
	v_readlane_b32 s82, v5, 56
	v_readlane_b32 s83, v5, 58
	v_readlane_b32 s84, v5, 57
; __device__ __forceinline__ void ph1_small(const Args& a, int tid, int wave, int lane, int G, int bid) {
;     ...
; #pragma unroll 8
;             for (int n = 0; n < 64; ++n) { const float cr = cre[((size_t)g * 16 + p) * 64 + n], ci = cim[((size_t)g * 16 + p) * 64 + n];
;                 const float pr = POW[(((size_t)g * 65 + tau) * 64 + n) * 2], pi = POW[(((size_t)g * 65 + tau) * 64 + n) * 2 + 1];
;                 const float er = cr * pr - ci * pi, ei = cr * pi + ci * pr;
;                 const f32x4* bp = (const f32x4*)(BBAR + ((size_t)g * 64 + n) * 32);
; #pragma unroll
;                 for (int q = 0; q < 8; ++q) { const f32x4 bb = bp[q]; s[2 * q] += er * bb[0] - ei * bb[1]; s[2 * q + 1] += er * bb[2] - ei * bb[3]; } }
	v_readlane_b32 s85, v5, 59
	v_readlane_b32 s86, v5, 60
	v_readlane_b32 s87, v5, 62
	v_readlane_b32 s88, v5, 61
	v_readlane_b32 s89, v5, 63
	v_mul_f32_e32 v244, v73, v84
	v_mul_f32_e32 v245, v77, v85
	v_sub_f32_e32 v86, v244, v245
	v_mul_f32_e32 v244, v77, v84
	v_mul_f32_e32 v245, v73, v85
	v_add_f32_e32 v88, v244, v245
	v_pk_mul_f32 v[90:91], v[88:89], s[36:37] op_sel_hi:[0,1]
	v_pk_fma_f32 v[90:91], v[86:87], s[16:17], v[90:91] op_sel_hi:[0,1,1] neg_lo:[0,0,1] neg_hi:[0,0,1]
	v_pk_add_f32 v[56:57], v[56:57], v[90:91]
	v_pk_mul_f32 v[90:91], v[88:89], s[40:41] op_sel_hi:[0,1]
	v_pk_fma_f32 v[90:91], v[86:87], s[38:39], v[90:91] op_sel_hi:[0,1,1] neg_lo:[0,0,1] neg_hi:[0,0,1]
	v_pk_add_f32 v[54:55], v[54:55], v[90:91]
	v_pk_mul_f32 v[90:91], v[88:89], s[52:53] op_sel_hi:[0,1]
	v_pk_fma_f32 v[90:91], v[86:87], s[42:43], v[90:91] op_sel_hi:[0,1,1] neg_lo:[0,0,1] neg_hi:[0,0,1]
	v_pk_add_f32 v[52:53], v[52:53], v[90:91]
	v_pk_mul_f32 v[90:91], v[88:89], s[56:57] op_sel_hi:[0,1]
	v_pk_fma_f32 v[90:91], v[86:87], s[54:55], v[90:91] op_sel_hi:[0,1,1] neg_lo:[0,0,1] neg_hi:[0,0,1]
	v_pk_add_f32 v[50:51], v[50:51], v[90:91]
	v_pk_mul_f32 v[90:91], v[88:89], s[62:63] op_sel_hi:[0,1]
	v_pk_fma_f32 v[90:91], v[86:87], s[58:59], v[90:91] op_sel_hi:[0,1,1] neg_lo:[0,0,1] neg_hi:[0,0,1]
	v_pk_add_f32 v[58:59], v[58:59], v[90:91]
	v_pk_mul_f32 v[90:91], v[88:89], s[80:81] op_sel_hi:[0,1]
	v_pk_fma_f32 v[90:91], v[86:87], s[64:65], v[90:91] op_sel_hi:[0,1,1] neg_lo:[0,0,1] neg_hi:[0,0,1]
	v_pk_add_f32 v[60:61], v[60:61], v[90:91]
	v_pk_mul_f32 v[90:91], v[88:89], s[84:85] op_sel_hi:[0,1]
	v_pk_fma_f32 v[90:91], v[86:87], s[82:83], v[90:91] op_sel_hi:[0,1,1] neg_lo:[0,0,1] neg_hi:[0,0,1]
	v_pk_add_f32 v[64:65], v[64:65], v[90:91]
	v_pk_mul_f32 v[90:91], v[88:89], s[88:89] op_sel_hi:[0,1]
	v_pk_fma_f32 v[90:91], v[86:87], s[86:87], v[90:91] op_sel_hi:[0,1,1] neg_lo:[0,0,1] neg_hi:[0,0,1]
	v_pk_add_f32 v[62:63], v[62:63], v[90:91]
	global_load_dwordx4 v[70:73], v[44:45], off offset:48
	global_load_dwordx4 v[74:77], v[42:43], off offset:48
	global_load_dwordx4 v[78:81], v40, s[100:101] offset:96
	global_load_dwordx4 v[82:85], v40, s[100:101] offset:112
	s_waitcnt vmcnt(4)
	v_readlane_b32 s16, v6, 0
	v_readlane_b32 s17, v6, 2
	v_readlane_b32 s36, v6, 1
	v_readlane_b32 s37, v6, 3
	v_readlane_b32 s38, v6, 4
	v_readlane_b32 s39, v6, 6
	v_readlane_b32 s40, v6, 5
	v_readlane_b32 s41, v6, 7
	v_readlane_b32 s42, v6, 8
	v_readlane_b32 s43, v6, 10
	v_readlane_b32 s52, v6, 9
	v_readlane_b32 s53, v6, 11
	v_readlane_b32 s54, v6, 12
	v_readlane_b32 s55, v6, 14
	v_readlane_b32 s56, v6, 13
	v_readlane_b32 s57, v6, 15
	v_readlane_b32 s58, v6, 16
	v_readlane_b32 s59, v6, 18
	v_readlane_b32 s62, v6, 17
	v_readlane_b32 s63, v6, 19
	v_readlane_b32 s64, v6, 20
	v_readlane_b32 s65, v6, 22
	v_readlane_b32 s80, v6, 21
	v_readlane_b32 s81, v6, 23
	v_readlane_b32 s82, v6, 24
	v_readlane_b32 s83, v6, 26
	v_readlane_b32 s84, v6, 25
	v_readlane_b32 s85, v6, 27
	v_readlane_b32 s86, v6, 28
	v_readlane_b32 s87, v6, 30
	v_readlane_b32 s88, v6, 29
	v_readlane_b32 s89, v6, 31
	v_mul_f32_e32 v244, v18, v26
	v_mul_f32_e32 v245, v22, v27
	v_sub_f32_e32 v86, v244, v245
	v_mul_f32_e32 v244, v22, v26
	v_mul_f32_e32 v245, v18, v27
	v_add_f32_e32 v88, v244, v245
	v_pk_mul_f32 v[90:91], v[88:89], s[36:37] op_sel_hi:[0,1]
	v_pk_fma_f32 v[90:91], v[86:87], s[16:17], v[90:91] op_sel_hi:[0,1,1] neg_lo:[0,0,1] neg_hi:[0,0,1]
	v_pk_add_f32 v[56:57], v[56:57], v[90:91]
	v_pk_mul_f32 v[90:91], v[88:89], s[40:41] op_sel_hi:[0,1]
	v_pk_fma_f32 v[90:91], v[86:87], s[38:39], v[90:91] op_sel_hi:[0,1,1] neg_lo:[0,0,1] neg_hi:[0,0,1]
	v_pk_add_f32 v[54:55], v[54:55], v[90:91]
	v_pk_mul_f32 v[90:91], v[88:89], s[52:53] op_sel_hi:[0,1]
	v_pk_fma_f32 v[90:91], v[86:87], s[42:43], v[90:91] op_sel_hi:[0,1,1] neg_lo:[0,0,1] neg_hi:[0,0,1]
	v_pk_add_f32 v[52:53], v[52:53], v[90:91]
	v_pk_mul_f32 v[90:91], v[88:89], s[56:57] op_sel_hi:[0,1]
	v_pk_fma_f32 v[90:91], v[86:87], s[54:55], v[90:91] op_sel_hi:[0,1,1] neg_lo:[0,0,1] neg_hi:[0,0,1]
	v_pk_add_f32 v[50:51], v[50:51], v[90:91]
	v_pk_mul_f32 v[90:91], v[88:89], s[62:63] op_sel_hi:[0,1]
	v_pk_fma_f32 v[90:91], v[86:87], s[58:59], v[90:91] op_sel_hi:[0,1,1] neg_lo:[0,0,1] neg_hi:[0,0,1]
	v_pk_add_f32 v[58:59], v[58:59], v[90:91]
	v_pk_mul_f32 v[90:91], v[88:89], s[80:81] op_sel_hi:[0,1]
	v_pk_fma_f32 v[90:91], v[86:87], s[64:65], v[90:91] op_sel_hi:[0,1,1] neg_lo:[0,0,1] neg_hi:[0,0,1]
	v_pk_add_f32 v[60:61], v[60:61], v[90:91]
	v_pk_mul_f32 v[90:91], v[88:89], s[84:85] op_sel_hi:[0,1]
	v_pk_fma_f32 v[90:91], v[86:87], s[82:83], v[90:91] op_sel_hi:[0,1,1] neg_lo:[0,0,1] neg_hi:[0,0,1]
	v_pk_add_f32 v[64:65], v[64:65], v[90:91]
	v_pk_mul_f32 v[90:91], v[88:89], s[88:89] op_sel_hi:[0,1]
	v_pk_fma_f32 v[90:91], v[86:87], s[86:87], v[90:91] op_sel_hi:[0,1,1] neg_lo:[0,0,1] neg_hi:[0,0,1]
	v_pk_add_f32 v[62:63], v[62:63], v[90:91]
	v_readlane_b32 s16, v6, 32
	v_readlane_b32 s17, v6, 34
	v_readlane_b32 s36, v6, 33
	v_readlane_b32 s37, v6, 35
	v_readlane_b32 s38, v6, 36
	v_readlane_b32 s39, v6, 38
	v_readlane_b32 s40, v6, 37
	v_readlane_b32 s41, v6, 39
	v_readlane_b32 s42, v6, 40
	v_readlane_b32 s43, v6, 42
	v_readlane_b32 s52, v6, 41
	v_readlane_b32 s53, v6, 43
	v_readlane_b32 s54, v6, 44
	v_readlane_b32 s55, v6, 46
	v_readlane_b32 s56, v6, 45
	v_readlane_b32 s57, v6, 47
	v_readlane_b32 s58, v6, 48
	v_readlane_b32 s59, v6, 50
	v_readlane_b32 s62, v6, 49
	v_readlane_b32 s63, v6, 51
	v_readlane_b32 s64, v6, 52
	v_readlane_b32 s65, v6, 54
	v_readlane_b32 s80, v6, 53
	v_readlane_b32 s81, v6, 55
	v_readlane_b32 s82, v6, 56
	v_readlane_b32 s83, v6, 58
	v_readlane_b32 s84, v6, 57
; __device__ __forceinline__ void ph1_small(const Args& a, int tid, int wave, int lane, int G, int bid) {
;     ...
; #pragma unroll 8
;             for (int n = 0; n < 64; ++n) { const float cr = cre[((size_t)g * 16 + p) * 64 + n], ci = cim[((size_t)g * 16 + p) * 64 + n];
;                 const float pr = POW[(((size_t)g * 65 + tau) * 64 + n) * 2], pi = POW[(((size_t)g * 65 + tau) * 64 + n) * 2 + 1];
;                 const float er = cr * pr - ci * pi, ei = cr * pi + ci * pr;
;                 const f32x4* bp = (const f32x4*)(BBAR + ((size_t)g * 64 + n) * 32);
; #pragma unroll
;                 for (int q = 0; q < 8; ++q) { const f32x4 bb = bp[q]; s[2 * q] += er * bb[0] - ei * bb[1]; s[2 * q + 1] += er * bb[2] - ei * bb[3]; } }
	v_readlane_b32 s85, v6, 59
	v_readlane_b32 s86, v6, 60
	v_readlane_b32 s87, v6, 62
	v_readlane_b32 s88, v6, 61
	v_readlane_b32 s89, v6, 63
	v_mul_f32_e32 v244, v19, v28
	v_mul_f32_e32 v245, v23, v29
	v_sub_f32_e32 v86, v244, v245
	v_mul_f32_e32 v244, v23, v28
	v_mul_f32_e32 v245, v19, v29
	v_add_f32_e32 v88, v244, v245
	v_pk_mul_f32 v[90:91], v[88:89], s[36:37] op_sel_hi:[0,1]
	v_pk_fma_f32 v[90:91], v[86:87], s[16:17], v[90:91] op_sel_hi:[0,1,1] neg_lo:[0,0,1] neg_hi:[0,0,1]
	v_pk_add_f32 v[56:57], v[56:57], v[90:91]
	v_pk_mul_f32 v[90:91], v[88:89], s[40:41] op_sel_hi:[0,1]
	v_pk_fma_f32 v[90:91], v[86:87], s[38:39], v[90:91] op_sel_hi:[0,1,1] neg_lo:[0,0,1] neg_hi:[0,0,1]
	v_pk_add_f32 v[54:55], v[54:55], v[90:91]
	v_pk_mul_f32 v[90:91], v[88:89], s[52:53] op_sel_hi:[0,1]
	v_pk_fma_f32 v[90:91], v[86:87], s[42:43], v[90:91] op_sel_hi:[0,1,1] neg_lo:[0,0,1] neg_hi:[0,0,1]
	v_pk_add_f32 v[52:53], v[52:53], v[90:91]
	v_pk_mul_f32 v[90:91], v[88:89], s[56:57] op_sel_hi:[0,1]
	v_pk_fma_f32 v[90:91], v[86:87], s[54:55], v[90:91] op_sel_hi:[0,1,1] neg_lo:[0,0,1] neg_hi:[0,0,1]
	v_pk_add_f32 v[50:51], v[50:51], v[90:91]
	v_pk_mul_f32 v[90:91], v[88:89], s[62:63] op_sel_hi:[0,1]
	v_pk_fma_f32 v[90:91], v[86:87], s[58:59], v[90:91] op_sel_hi:[0,1,1] neg_lo:[0,0,1] neg_hi:[0,0,1]
	v_pk_add_f32 v[58:59], v[58:59], v[90:91]
	v_pk_mul_f32 v[90:91], v[88:89], s[80:81] op_sel_hi:[0,1]
	v_pk_fma_f32 v[90:91], v[86:87], s[64:65], v[90:91] op_sel_hi:[0,1,1] neg_lo:[0,0,1] neg_hi:[0,0,1]
	v_pk_add_f32 v[60:61], v[60:61], v[90:91]
	v_pk_mul_f32 v[90:91], v[88:89], s[84:85] op_sel_hi:[0,1]
	v_pk_fma_f32 v[90:91], v[86:87], s[82:83], v[90:91] op_sel_hi:[0,1,1] neg_lo:[0,0,1] neg_hi:[0,0,1]
	v_pk_add_f32 v[64:65], v[64:65], v[90:91]
	v_pk_mul_f32 v[90:91], v[88:89], s[88:89] op_sel_hi:[0,1]
	v_pk_fma_f32 v[90:91], v[86:87], s[86:87], v[90:91] op_sel_hi:[0,1,1] neg_lo:[0,0,1] neg_hi:[0,0,1]
	v_pk_add_f32 v[62:63], v[62:63], v[90:91]
	v_readlane_b32 s16, v7, 0
	v_readlane_b32 s17, v7, 2
	v_readlane_b32 s36, v7, 1
	v_readlane_b32 s37, v7, 3
	v_readlane_b32 s38, v7, 4
	v_readlane_b32 s39, v7, 6
	v_readlane_b32 s40, v7, 5
	v_readlane_b32 s41, v7, 7
	v_readlane_b32 s42, v7, 8
	v_readlane_b32 s43, v7, 10
	v_readlane_b32 s52, v7, 9
	v_readlane_b32 s53, v7, 11
	v_readlane_b32 s54, v7, 12
	v_readlane_b32 s55, v7, 14
	v_readlane_b32 s56, v7, 13
	v_readlane_b32 s57, v7, 15
	v_readlane_b32 s58, v7, 16
	v_readlane_b32 s59, v7, 18
	v_readlane_b32 s62, v7, 17
	v_readlane_b32 s63, v7, 19
	v_readlane_b32 s64, v7, 20
	v_readlane_b32 s65, v7, 22
	v_readlane_b32 s80, v7, 21
	v_readlane_b32 s81, v7, 23
	v_readlane_b32 s82, v7, 24
	v_readlane_b32 s83, v7, 26
	v_readlane_b32 s84, v7, 25
	v_readlane_b32 s85, v7, 27
	v_readlane_b32 s86, v7, 28
	v_readlane_b32 s87, v7, 30
	v_readlane_b32 s88, v7, 29
	v_readlane_b32 s89, v7, 31
	v_mul_f32_e32 v244, v20, v46
	v_mul_f32_e32 v245, v24, v47
	v_sub_f32_e32 v86, v244, v245
	v_mul_f32_e32 v244, v24, v46
	v_mul_f32_e32 v245, v20, v47
	v_add_f32_e32 v88, v244, v245
	v_pk_mul_f32 v[90:91], v[88:89], s[36:37] op_sel_hi:[0,1]
	v_pk_fma_f32 v[90:91], v[86:87], s[16:17], v[90:91] op_sel_hi:[0,1,1] neg_lo:[0,0,1] neg_hi:[0,0,1]
	v_pk_add_f32 v[56:57], v[56:57], v[90:91]
	v_pk_mul_f32 v[90:91], v[88:89], s[40:41] op_sel_hi:[0,1]
	v_pk_fma_f32 v[90:91], v[86:87], s[38:39], v[90:91] op_sel_hi:[0,1,1] neg_lo:[0,0,1] neg_hi:[0,0,1]
	v_pk_add_f32 v[54:55], v[54:55], v[90:91]
	v_pk_mul_f32 v[90:91], v[88:89], s[52:53] op_sel_hi:[0,1]
	v_pk_fma_f32 v[90:91], v[86:87], s[42:43], v[90:91] op_sel_hi:[0,1,1] neg_lo:[0,0,1] neg_hi:[0,0,1]
	v_pk_add_f32 v[52:53], v[52:53], v[90:91]
	v_pk_mul_f32 v[90:91], v[88:89], s[56:57] op_sel_hi:[0,1]
	v_pk_fma_f32 v[90:91], v[86:87], s[54:55], v[90:91] op_sel_hi:[0,1,1] neg_lo:[0,0,1] neg_hi:[0,0,1]
	v_pk_add_f32 v[50:51], v[50:51], v[90:91]
	v_pk_mul_f32 v[90:91], v[88:89], s[62:63] op_sel_hi:[0,1]
	v_pk_fma_f32 v[90:91], v[86:87], s[58:59], v[90:91] op_sel_hi:[0,1,1] neg_lo:[0,0,1] neg_hi:[0,0,1]
	v_pk_add_f32 v[58:59], v[58:59], v[90:91]
	v_pk_mul_f32 v[90:91], v[88:89], s[80:81] op_sel_hi:[0,1]
	v_pk_fma_f32 v[90:91], v[86:87], s[64:65], v[90:91] op_sel_hi:[0,1,1] neg_lo:[0,0,1] neg_hi:[0,0,1]
	v_pk_add_f32 v[60:61], v[60:61], v[90:91]
	v_pk_mul_f32 v[90:91], v[88:89], s[84:85] op_sel_hi:[0,1]
	v_pk_fma_f32 v[90:91], v[86:87], s[82:83], v[90:91] op_sel_hi:[0,1,1] neg_lo:[0,0,1] neg_hi:[0,0,1]
	v_pk_add_f32 v[64:65], v[64:65], v[90:91]
	v_pk_mul_f32 v[90:91], v[88:89], s[88:89] op_sel_hi:[0,1]
	v_pk_fma_f32 v[90:91], v[86:87], s[86:87], v[90:91] op_sel_hi:[0,1,1] neg_lo:[0,0,1] neg_hi:[0,0,1]
	v_pk_add_f32 v[62:63], v[62:63], v[90:91]
	v_readlane_b32 s16, v7, 32
	v_readlane_b32 s17, v7, 34
	v_readlane_b32 s36, v7, 33
	v_readlane_b32 s37, v7, 35
	v_readlane_b32 s38, v7, 36
	v_readlane_b32 s39, v7, 38
	v_readlane_b32 s40, v7, 37
	v_readlane_b32 s41, v7, 39
	v_readlane_b32 s42, v7, 40
	v_readlane_b32 s43, v7, 42
	v_readlane_b32 s52, v7, 41
	v_readlane_b32 s53, v7, 43
	v_readlane_b32 s54, v7, 44
	v_readlane_b32 s55, v7, 46
	v_readlane_b32 s56, v7, 45
	v_readlane_b32 s57, v7, 47
	v_readlane_b32 s58, v7, 48
	v_readlane_b32 s59, v7, 50
	v_readlane_b32 s62, v7, 49
	v_readlane_b32 s63, v7, 51
	v_readlane_b32 s64, v7, 52
	v_readlane_b32 s65, v7, 54
	v_readlane_b32 s80, v7, 53
	v_readlane_b32 s81, v7, 55
	v_readlane_b32 s82, v7, 56
	v_readlane_b32 s83, v7, 58
	v_readlane_b32 s84, v7, 57
	v_readlane_b32 s85, v7, 59
	v_readlane_b32 s86, v7, 60
	v_readlane_b32 s87, v7, 62
	v_readlane_b32 s88, v7, 61
	v_readlane_b32 s89, v7, 63
	v_mul_f32_e32 v244, v21, v48
	v_mul_f32_e32 v245, v25, v49
	v_sub_f32_e32 v86, v244, v245
; __device__ __forceinline__ void ph1_small(const Args& a, int tid, int wave, int lane, int G, int bid) {
;     ...
; #pragma unroll 8
;             for (int n = 0; n < 64; ++n) { const float cr = cre[((size_t)g * 16 + p) * 64 + n], ci = cim[((size_t)g * 16 + p) * 64 + n];
;                 const float pr = POW[(((size_t)g * 65 + tau) * 64 + n) * 2], pi = POW[(((size_t)g * 65 + tau) * 64 + n) * 2 + 1];
;                 const float er = cr * pr - ci * pi, ei = cr * pi + ci * pr;
;                 const f32x4* bp = (const f32x4*)(BBAR + ((size_t)g * 64 + n) * 32);
; #pragma unroll
;                 for (int q = 0; q < 8; ++q) { const f32x4 bb = bp[q]; s[2 * q] += er * bb[0] - ei * bb[1]; s[2 * q + 1] += er * bb[2] - ei * bb[3]; } }
	v_mul_f32_e32 v244, v25, v48
	v_mul_f32_e32 v245, v21, v49
	v_add_f32_e32 v88, v244, v245
	v_pk_mul_f32 v[90:91], v[88:89], s[36:37] op_sel_hi:[0,1]
	v_pk_fma_f32 v[90:91], v[86:87], s[16:17], v[90:91] op_sel_hi:[0,1,1] neg_lo:[0,0,1] neg_hi:[0,0,1]
	v_pk_add_f32 v[56:57], v[56:57], v[90:91]
	v_pk_mul_f32 v[90:91], v[88:89], s[40:41] op_sel_hi:[0,1]
	v_pk_fma_f32 v[90:91], v[86:87], s[38:39], v[90:91] op_sel_hi:[0,1,1] neg_lo:[0,0,1] neg_hi:[0,0,1]
	v_pk_add_f32 v[54:55], v[54:55], v[90:91]
	v_pk_mul_f32 v[90:91], v[88:89], s[52:53] op_sel_hi:[0,1]
	v_pk_fma_f32 v[90:91], v[86:87], s[42:43], v[90:91] op_sel_hi:[0,1,1] neg_lo:[0,0,1] neg_hi:[0,0,1]
	v_pk_add_f32 v[52:53], v[52:53], v[90:91]
	v_pk_mul_f32 v[90:91], v[88:89], s[56:57] op_sel_hi:[0,1]
	v_pk_fma_f32 v[90:91], v[86:87], s[54:55], v[90:91] op_sel_hi:[0,1,1] neg_lo:[0,0,1] neg_hi:[0,0,1]
	v_pk_add_f32 v[50:51], v[50:51], v[90:91]
	v_pk_mul_f32 v[90:91], v[88:89], s[62:63] op_sel_hi:[0,1]
	v_pk_fma_f32 v[90:91], v[86:87], s[58:59], v[90:91] op_sel_hi:[0,1,1] neg_lo:[0,0,1] neg_hi:[0,0,1]
	v_pk_add_f32 v[58:59], v[58:59], v[90:91]
	v_pk_mul_f32 v[90:91], v[88:89], s[80:81] op_sel_hi:[0,1]
	v_pk_fma_f32 v[90:91], v[86:87], s[64:65], v[90:91] op_sel_hi:[0,1,1] neg_lo:[0,0,1] neg_hi:[0,0,1]
	v_pk_add_f32 v[60:61], v[60:61], v[90:91]
	v_pk_mul_f32 v[90:91], v[88:89], s[84:85] op_sel_hi:[0,1]
	v_pk_fma_f32 v[90:91], v[86:87], s[82:83], v[90:91] op_sel_hi:[0,1,1] neg_lo:[0,0,1] neg_hi:[0,0,1]
	v_pk_add_f32 v[64:65], v[64:65], v[90:91]
	v_pk_mul_f32 v[90:91], v[88:89], s[88:89] op_sel_hi:[0,1]
	v_pk_fma_f32 v[90:91], v[86:87], s[86:87], v[90:91] op_sel_hi:[0,1,1] neg_lo:[0,0,1] neg_hi:[0,0,1]
	v_pk_add_f32 v[62:63], v[62:63], v[90:91]
	global_load_dwordx4 v[18:21], v[44:45], off offset:64
	global_load_dwordx4 v[22:25], v[42:43], off offset:64
	global_load_dwordx4 v[26:29], v40, s[100:101] offset:128
	global_load_dwordx4 v[46:49], v40, s[100:101] offset:144
	s_waitcnt vmcnt(4)
	v_readlane_b32 s16, v8, 0
	v_readlane_b32 s17, v8, 2
	v_readlane_b32 s36, v8, 1
	v_readlane_b32 s37, v8, 3
	v_readlane_b32 s38, v8, 4
	v_readlane_b32 s39, v8, 6
	v_readlane_b32 s40, v8, 5
	v_readlane_b32 s41, v8, 7
	v_readlane_b32 s42, v8, 8
	v_readlane_b32 s43, v8, 10
	v_readlane_b32 s52, v8, 9
	v_readlane_b32 s53, v8, 11
	v_readlane_b32 s54, v8, 12
	v_readlane_b32 s55, v8, 14
	v_readlane_b32 s56, v8, 13
	v_readlane_b32 s57, v8, 15
	v_readlane_b32 s58, v8, 16
	v_readlane_b32 s59, v8, 18
	v_readlane_b32 s62, v8, 17
	v_readlane_b32 s63, v8, 19
	v_readlane_b32 s64, v8, 20
	v_readlane_b32 s65, v8, 22
	v_readlane_b32 s80, v8, 21
	v_readlane_b32 s81, v8, 23
	v_readlane_b32 s82, v8, 24
	v_readlane_b32 s83, v8, 26
	v_readlane_b32 s84, v8, 25
	v_readlane_b32 s85, v8, 27
	v_readlane_b32 s86, v8, 28
	v_readlane_b32 s87, v8, 30
	v_readlane_b32 s88, v8, 29
	v_readlane_b32 s89, v8, 31
	v_mul_f32_e32 v244, v70, v78
	v_mul_f32_e32 v245, v74, v79
	v_sub_f32_e32 v86, v244, v245
	v_mul_f32_e32 v244, v74, v78
	v_mul_f32_e32 v245, v70, v79
	v_add_f32_e32 v88, v244, v245
	v_pk_mul_f32 v[90:91], v[88:89], s[36:37] op_sel_hi:[0,1]
	v_pk_fma_f32 v[90:91], v[86:87], s[16:17], v[90:91] op_sel_hi:[0,1,1] neg_lo:[0,0,1] neg_hi:[0,0,1]
	v_pk_add_f32 v[56:57], v[56:57], v[90:91]
	v_pk_mul_f32 v[90:91], v[88:89], s[40:41] op_sel_hi:[0,1]
	v_pk_fma_f32 v[90:91], v[86:87], s[38:39], v[90:91] op_sel_hi:[0,1,1] neg_lo:[0,0,1] neg_hi:[0,0,1]
	v_pk_add_f32 v[54:55], v[54:55], v[90:91]
	v_pk_mul_f32 v[90:91], v[88:89], s[52:53] op_sel_hi:[0,1]
	v_pk_fma_f32 v[90:91], v[86:87], s[42:43], v[90:91] op_sel_hi:[0,1,1] neg_lo:[0,0,1] neg_hi:[0,0,1]
	v_pk_add_f32 v[52:53], v[52:53], v[90:91]
	v_pk_mul_f32 v[90:91], v[88:89], s[56:57] op_sel_hi:[0,1]
	v_pk_fma_f32 v[90:91], v[86:87], s[54:55], v[90:91] op_sel_hi:[0,1,1] neg_lo:[0,0,1] neg_hi:[0,0,1]
	v_pk_add_f32 v[50:51], v[50:51], v[90:91]
	v_pk_mul_f32 v[90:91], v[88:89], s[62:63] op_sel_hi:[0,1]
	v_pk_fma_f32 v[90:91], v[86:87], s[58:59], v[90:91] op_sel_hi:[0,1,1] neg_lo:[0,0,1] neg_hi:[0,0,1]
	v_pk_add_f32 v[58:59], v[58:59], v[90:91]
	v_pk_mul_f32 v[90:91], v[88:89], s[80:81] op_sel_hi:[0,1]
	v_pk_fma_f32 v[90:91], v[86:87], s[64:65], v[90:91] op_sel_hi:[0,1,1] neg_lo:[0,0,1] neg_hi:[0,0,1]
	v_pk_add_f32 v[60:61], v[60:61], v[90:91]
	v_pk_mul_f32 v[90:91], v[88:89], s[84:85] op_sel_hi:[0,1]
	v_pk_fma_f32 v[90:91], v[86:87], s[82:83], v[90:91] op_sel_hi:[0,1,1] neg_lo:[0,0,1] neg_hi:[0,0,1]
	v_pk_add_f32 v[64:65], v[64:65], v[90:91]
	v_pk_mul_f32 v[90:91], v[88:89], s[88:89] op_sel_hi:[0,1]
	v_pk_fma_f32 v[90:91], v[86:87], s[86:87], v[90:91] op_sel_hi:[0,1,1] neg_lo:[0,0,1] neg_hi:[0,0,1]
	v_pk_add_f32 v[62:63], v[62:63], v[90:91]
	v_readlane_b32 s16, v8, 32
	v_readlane_b32 s17, v8, 34
	v_readlane_b32 s36, v8, 33
	v_readlane_b32 s37, v8, 35
	v_readlane_b32 s38, v8, 36
	v_readlane_b32 s39, v8, 38
	v_readlane_b32 s40, v8, 37
	v_readlane_b32 s41, v8, 39
	v_readlane_b32 s42, v8, 40
	v_readlane_b32 s43, v8, 42
	v_readlane_b32 s52, v8, 41
	v_readlane_b32 s53, v8, 43
	v_readlane_b32 s54, v8, 44
	v_readlane_b32 s55, v8, 46
	v_readlane_b32 s56, v8, 45
	v_readlane_b32 s57, v8, 47
	v_readlane_b32 s58, v8, 48
	v_readlane_b32 s59, v8, 50
	v_readlane_b32 s62, v8, 49
	v_readlane_b32 s63, v8, 51
	v_readlane_b32 s64, v8, 52
	v_readlane_b32 s65, v8, 54
	v_readlane_b32 s80, v8, 53
	v_readlane_b32 s81, v8, 55
	v_readlane_b32 s82, v8, 56
	v_readlane_b32 s83, v8, 58
	v_readlane_b32 s84, v8, 57
	v_readlane_b32 s85, v8, 59
	v_readlane_b32 s86, v8, 60
	v_readlane_b32 s87, v8, 62
	v_readlane_b32 s88, v8, 61
	v_readlane_b32 s89, v8, 63
	v_mul_f32_e32 v244, v71, v80
	v_mul_f32_e32 v245, v75, v81
	v_sub_f32_e32 v86, v244, v245
; __device__ __forceinline__ void ph1_small(const Args& a, int tid, int wave, int lane, int G, int bid) {
;     ...
; #pragma unroll 8
;             for (int n = 0; n < 64; ++n) { const float cr = cre[((size_t)g * 16 + p) * 64 + n], ci = cim[((size_t)g * 16 + p) * 64 + n];
;                 const float pr = POW[(((size_t)g * 65 + tau) * 64 + n) * 2], pi = POW[(((size_t)g * 65 + tau) * 64 + n) * 2 + 1];
;                 const float er = cr * pr - ci * pi, ei = cr * pi + ci * pr;
;                 const f32x4* bp = (const f32x4*)(BBAR + ((size_t)g * 64 + n) * 32);
; #pragma unroll
;                 for (int q = 0; q < 8; ++q) { const f32x4 bb = bp[q]; s[2 * q] += er * bb[0] - ei * bb[1]; s[2 * q + 1] += er * bb[2] - ei * bb[3]; } }
	v_mul_f32_e32 v244, v75, v80
	v_mul_f32_e32 v245, v71, v81
	v_add_f32_e32 v88, v244, v245
	v_pk_mul_f32 v[90:91], v[88:89], s[36:37] op_sel_hi:[0,1]
	v_pk_fma_f32 v[90:91], v[86:87], s[16:17], v[90:91] op_sel_hi:[0,1,1] neg_lo:[0,0,1] neg_hi:[0,0,1]
	v_pk_add_f32 v[56:57], v[56:57], v[90:91]
	v_pk_mul_f32 v[90:91], v[88:89], s[40:41] op_sel_hi:[0,1]
	v_pk_fma_f32 v[90:91], v[86:87], s[38:39], v[90:91] op_sel_hi:[0,1,1] neg_lo:[0,0,1] neg_hi:[0,0,1]
	v_pk_add_f32 v[54:55], v[54:55], v[90:91]
	v_pk_mul_f32 v[90:91], v[88:89], s[52:53] op_sel_hi:[0,1]
	v_pk_fma_f32 v[90:91], v[86:87], s[42:43], v[90:91] op_sel_hi:[0,1,1] neg_lo:[0,0,1] neg_hi:[0,0,1]
	v_pk_add_f32 v[52:53], v[52:53], v[90:91]
	v_pk_mul_f32 v[90:91], v[88:89], s[56:57] op_sel_hi:[0,1]
	v_pk_fma_f32 v[90:91], v[86:87], s[54:55], v[90:91] op_sel_hi:[0,1,1] neg_lo:[0,0,1] neg_hi:[0,0,1]
	v_pk_add_f32 v[50:51], v[50:51], v[90:91]
	v_pk_mul_f32 v[90:91], v[88:89], s[62:63] op_sel_hi:[0,1]
	v_pk_fma_f32 v[90:91], v[86:87], s[58:59], v[90:91] op_sel_hi:[0,1,1] neg_lo:[0,0,1] neg_hi:[0,0,1]
	v_pk_add_f32 v[58:59], v[58:59], v[90:91]
	v_pk_mul_f32 v[90:91], v[88:89], s[80:81] op_sel_hi:[0,1]
	v_pk_fma_f32 v[90:91], v[86:87], s[64:65], v[90:91] op_sel_hi:[0,1,1] neg_lo:[0,0,1] neg_hi:[0,0,1]
	v_pk_add_f32 v[60:61], v[60:61], v[90:91]
	v_pk_mul_f32 v[90:91], v[88:89], s[84:85] op_sel_hi:[0,1]
	v_pk_fma_f32 v[90:91], v[86:87], s[82:83], v[90:91] op_sel_hi:[0,1,1] neg_lo:[0,0,1] neg_hi:[0,0,1]
	v_pk_add_f32 v[64:65], v[64:65], v[90:91]
	v_pk_mul_f32 v[90:91], v[88:89], s[88:89] op_sel_hi:[0,1]
	v_pk_fma_f32 v[90:91], v[86:87], s[86:87], v[90:91] op_sel_hi:[0,1,1] neg_lo:[0,0,1] neg_hi:[0,0,1]
	v_pk_add_f32 v[62:63], v[62:63], v[90:91]
	v_readlane_b32 s16, v9, 0
	v_readlane_b32 s17, v9, 2
	v_readlane_b32 s36, v9, 1
	v_readlane_b32 s37, v9, 3
	v_readlane_b32 s38, v9, 4
	v_readlane_b32 s39, v9, 6
	v_readlane_b32 s40, v9, 5
	v_readlane_b32 s41, v9, 7
	v_readlane_b32 s42, v9, 8
	v_readlane_b32 s43, v9, 10
	v_readlane_b32 s52, v9, 9
	v_readlane_b32 s53, v9, 11
	v_readlane_b32 s54, v9, 12
	v_readlane_b32 s55, v9, 14
	v_readlane_b32 s56, v9, 13
	v_readlane_b32 s57, v9, 15
	v_readlane_b32 s58, v9, 16
	v_readlane_b32 s59, v9, 18
	v_readlane_b32 s62, v9, 17
	v_readlane_b32 s63, v9, 19
	v_readlane_b32 s64, v9, 20
	v_readlane_b32 s65, v9, 22
	v_readlane_b32 s80, v9, 21
	v_readlane_b32 s81, v9, 23
	v_readlane_b32 s82, v9, 24
	v_readlane_b32 s83, v9, 26
	v_readlane_b32 s84, v9, 25
	v_readlane_b32 s85, v9, 27
	v_readlane_b32 s86, v9, 28
	v_readlane_b32 s87, v9, 30
	v_readlane_b32 s88, v9, 29
	v_readlane_b32 s89, v9, 31
	v_mul_f32_e32 v244, v72, v82
	v_mul_f32_e32 v245, v76, v83
	v_sub_f32_e32 v86, v244, v245
	v_mul_f32_e32 v244, v76, v82
	v_mul_f32_e32 v245, v72, v83
	v_add_f32_e32 v88, v244, v245
	v_pk_mul_f32 v[90:91], v[88:89], s[36:37] op_sel_hi:[0,1]
	v_pk_fma_f32 v[90:91], v[86:87], s[16:17], v[90:91] op_sel_hi:[0,1,1] neg_lo:[0,0,1] neg_hi:[0,0,1]
	v_pk_add_f32 v[56:57], v[56:57], v[90:91]
	v_pk_mul_f32 v[90:91], v[88:89], s[40:41] op_sel_hi:[0,1]
	v_pk_fma_f32 v[90:91], v[86:87], s[38:39], v[90:91] op_sel_hi:[0,1,1] neg_lo:[0,0,1] neg_hi:[0,0,1]
	v_pk_add_f32 v[54:55], v[54:55], v[90:91]
	v_pk_mul_f32 v[90:91], v[88:89], s[52:53] op_sel_hi:[0,1]
	v_pk_fma_f32 v[90:91], v[86:87], s[42:43], v[90:91] op_sel_hi:[0,1,1] neg_lo:[0,0,1] neg_hi:[0,0,1]
	v_pk_add_f32 v[52:53], v[52:53], v[90:91]
	v_pk_mul_f32 v[90:91], v[88:89], s[56:57] op_sel_hi:[0,1]
	v_pk_fma_f32 v[90:91], v[86:87], s[54:55], v[90:91] op_sel_hi:[0,1,1] neg_lo:[0,0,1] neg_hi:[0,0,1]
	v_pk_add_f32 v[50:51], v[50:51], v[90:91]
	v_pk_mul_f32 v[90:91], v[88:89], s[62:63] op_sel_hi:[0,1]
	v_pk_fma_f32 v[90:91], v[86:87], s[58:59], v[90:91] op_sel_hi:[0,1,1] neg_lo:[0,0,1] neg_hi:[0,0,1]
	v_pk_add_f32 v[58:59], v[58:59], v[90:91]
	v_pk_mul_f32 v[90:91], v[88:89], s[80:81] op_sel_hi:[0,1]
	v_pk_fma_f32 v[90:91], v[86:87], s[64:65], v[90:91] op_sel_hi:[0,1,1] neg_lo:[0,0,1] neg_hi:[0,0,1]
	v_pk_add_f32 v[60:61], v[60:61], v[90:91]
	v_pk_mul_f32 v[90:91], v[88:89], s[84:85] op_sel_hi:[0,1]
	v_pk_fma_f32 v[90:91], v[86:87], s[82:83], v[90:91] op_sel_hi:[0,1,1] neg_lo:[0,0,1] neg_hi:[0,0,1]
	v_pk_add_f32 v[64:65], v[64:65], v[90:91]
	v_pk_mul_f32 v[90:91], v[88:89], s[88:89] op_sel_hi:[0,1]
	v_pk_fma_f32 v[90:91], v[86:87], s[86:87], v[90:91] op_sel_hi:[0,1,1] neg_lo:[0,0,1] neg_hi:[0,0,1]
	v_pk_add_f32 v[62:63], v[62:63], v[90:91]
	v_readlane_b32 s16, v9, 32
	v_readlane_b32 s17, v9, 34
	v_readlane_b32 s36, v9, 33
	v_readlane_b32 s37, v9, 35
	v_readlane_b32 s38, v9, 36
	v_readlane_b32 s39, v9, 38
	v_readlane_b32 s40, v9, 37
	v_readlane_b32 s41, v9, 39
	v_readlane_b32 s42, v9, 40
	v_readlane_b32 s43, v9, 42
	v_readlane_b32 s52, v9, 41
	v_readlane_b32 s53, v9, 43
	v_readlane_b32 s54, v9, 44
	v_readlane_b32 s55, v9, 46
	v_readlane_b32 s56, v9, 45
	v_readlane_b32 s57, v9, 47
	v_readlane_b32 s58, v9, 48
	v_readlane_b32 s59, v9, 50
	v_readlane_b32 s62, v9, 49
	v_readlane_b32 s63, v9, 51
	v_readlane_b32 s64, v9, 52
	v_readlane_b32 s65, v9, 54
	v_readlane_b32 s80, v9, 53
	v_readlane_b32 s81, v9, 55
	v_readlane_b32 s82, v9, 56
	v_readlane_b32 s83, v9, 58
	v_readlane_b32 s84, v9, 57
	v_readlane_b32 s85, v9, 59
	v_readlane_b32 s86, v9, 60
	v_readlane_b32 s87, v9, 62
	v_readlane_b32 s88, v9, 61
	v_readlane_b32 s89, v9, 63
	v_mul_f32_e32 v244, v73, v84
	v_mul_f32_e32 v245, v77, v85
	v_sub_f32_e32 v86, v244, v245
	v_mul_f32_e32 v244, v77, v84
	v_mul_f32_e32 v245, v73, v85
	v_add_f32_e32 v88, v244, v245
	v_pk_mul_f32 v[90:91], v[88:89], s[36:37] op_sel_hi:[0,1]
	v_pk_fma_f32 v[90:91], v[86:87], s[16:17], v[90:91] op_sel_hi:[0,1,1] neg_lo:[0,0,1] neg_hi:[0,0,1]
; __device__ __forceinline__ void ph1_small(const Args& a, int tid, int wave, int lane, int G, int bid) {
;     ...
; #pragma unroll 8
;             for (int n = 0; n < 64; ++n) { const float cr = cre[((size_t)g * 16 + p) * 64 + n], ci = cim[((size_t)g * 16 + p) * 64 + n];
;                 const float pr = POW[(((size_t)g * 65 + tau) * 64 + n) * 2], pi = POW[(((size_t)g * 65 + tau) * 64 + n) * 2 + 1];
;                 const float er = cr * pr - ci * pi, ei = cr * pi + ci * pr;
;                 const f32x4* bp = (const f32x4*)(BBAR + ((size_t)g * 64 + n) * 32);
; #pragma unroll
;                 for (int q = 0; q < 8; ++q) { const f32x4 bb = bp[q]; s[2 * q] += er * bb[0] - ei * bb[1]; s[2 * q + 1] += er * bb[2] - ei * bb[3]; } }
	v_pk_add_f32 v[56:57], v[56:57], v[90:91]
	v_pk_mul_f32 v[90:91], v[88:89], s[40:41] op_sel_hi:[0,1]
	v_pk_fma_f32 v[90:91], v[86:87], s[38:39], v[90:91] op_sel_hi:[0,1,1] neg_lo:[0,0,1] neg_hi:[0,0,1]
	v_pk_add_f32 v[54:55], v[54:55], v[90:91]
	v_pk_mul_f32 v[90:91], v[88:89], s[52:53] op_sel_hi:[0,1]
	v_pk_fma_f32 v[90:91], v[86:87], s[42:43], v[90:91] op_sel_hi:[0,1,1] neg_lo:[0,0,1] neg_hi:[0,0,1]
	v_pk_add_f32 v[52:53], v[52:53], v[90:91]
	v_pk_mul_f32 v[90:91], v[88:89], s[56:57] op_sel_hi:[0,1]
	v_pk_fma_f32 v[90:91], v[86:87], s[54:55], v[90:91] op_sel_hi:[0,1,1] neg_lo:[0,0,1] neg_hi:[0,0,1]
	v_pk_add_f32 v[50:51], v[50:51], v[90:91]
	v_pk_mul_f32 v[90:91], v[88:89], s[62:63] op_sel_hi:[0,1]
	v_pk_fma_f32 v[90:91], v[86:87], s[58:59], v[90:91] op_sel_hi:[0,1,1] neg_lo:[0,0,1] neg_hi:[0,0,1]
	v_pk_add_f32 v[58:59], v[58:59], v[90:91]
	v_pk_mul_f32 v[90:91], v[88:89], s[80:81] op_sel_hi:[0,1]
	v_pk_fma_f32 v[90:91], v[86:87], s[64:65], v[90:91] op_sel_hi:[0,1,1] neg_lo:[0,0,1] neg_hi:[0,0,1]
	v_pk_add_f32 v[60:61], v[60:61], v[90:91]
	v_pk_mul_f32 v[90:91], v[88:89], s[84:85] op_sel_hi:[0,1]
	v_pk_fma_f32 v[90:91], v[86:87], s[82:83], v[90:91] op_sel_hi:[0,1,1] neg_lo:[0,0,1] neg_hi:[0,0,1]
	v_pk_add_f32 v[64:65], v[64:65], v[90:91]
	v_pk_mul_f32 v[90:91], v[88:89], s[88:89] op_sel_hi:[0,1]
	v_pk_fma_f32 v[90:91], v[86:87], s[86:87], v[90:91] op_sel_hi:[0,1,1] neg_lo:[0,0,1] neg_hi:[0,0,1]
	v_pk_add_f32 v[62:63], v[62:63], v[90:91]
	global_load_dwordx4 v[70:73], v[44:45], off offset:80
	global_load_dwordx4 v[74:77], v[42:43], off offset:80
	global_load_dwordx4 v[78:81], v40, s[100:101] offset:160
	global_load_dwordx4 v[82:85], v40, s[100:101] offset:176
	s_waitcnt vmcnt(4)
	v_readlane_b32 s16, v10, 0
	v_readlane_b32 s17, v10, 2
	v_readlane_b32 s36, v10, 1
	v_readlane_b32 s37, v10, 3
	v_readlane_b32 s38, v10, 4
	v_readlane_b32 s39, v10, 6
	v_readlane_b32 s40, v10, 5
	v_readlane_b32 s41, v10, 7
	v_readlane_b32 s42, v10, 8
	v_readlane_b32 s43, v10, 10
	v_readlane_b32 s52, v10, 9
	v_readlane_b32 s53, v10, 11
	v_readlane_b32 s54, v10, 12
	v_readlane_b32 s55, v10, 14
	v_readlane_b32 s56, v10, 13
	v_readlane_b32 s57, v10, 15
	v_readlane_b32 s58, v10, 16
	v_readlane_b32 s59, v10, 18
	v_readlane_b32 s62, v10, 17
	v_readlane_b32 s63, v10, 19
	v_readlane_b32 s64, v10, 20
	v_readlane_b32 s65, v10, 22
	v_readlane_b32 s80, v10, 21
	v_readlane_b32 s81, v10, 23
	v_readlane_b32 s82, v10, 24
	v_readlane_b32 s83, v10, 26
	v_readlane_b32 s84, v10, 25
	v_readlane_b32 s85, v10, 27
	v_readlane_b32 s86, v10, 28
	v_readlane_b32 s87, v10, 30
	v_readlane_b32 s88, v10, 29
	v_readlane_b32 s89, v10, 31
	v_mul_f32_e32 v244, v18, v26
	v_mul_f32_e32 v245, v22, v27
	v_sub_f32_e32 v86, v244, v245
	v_mul_f32_e32 v244, v22, v26
	v_mul_f32_e32 v245, v18, v27
	v_add_f32_e32 v88, v244, v245
	v_pk_mul_f32 v[90:91], v[88:89], s[36:37] op_sel_hi:[0,1]
	v_pk_fma_f32 v[90:91], v[86:87], s[16:17], v[90:91] op_sel_hi:[0,1,1] neg_lo:[0,0,1] neg_hi:[0,0,1]
	v_pk_add_f32 v[56:57], v[56:57], v[90:91]
	v_pk_mul_f32 v[90:91], v[88:89], s[40:41] op_sel_hi:[0,1]
	v_pk_fma_f32 v[90:91], v[86:87], s[38:39], v[90:91] op_sel_hi:[0,1,1] neg_lo:[0,0,1] neg_hi:[0,0,1]
	v_pk_add_f32 v[54:55], v[54:55], v[90:91]
	v_pk_mul_f32 v[90:91], v[88:89], s[52:53] op_sel_hi:[0,1]
	v_pk_fma_f32 v[90:91], v[86:87], s[42:43], v[90:91] op_sel_hi:[0,1,1] neg_lo:[0,0,1] neg_hi:[0,0,1]
	v_pk_add_f32 v[52:53], v[52:53], v[90:91]
	v_pk_mul_f32 v[90:91], v[88:89], s[56:57] op_sel_hi:[0,1]
	v_pk_fma_f32 v[90:91], v[86:87], s[54:55], v[90:91] op_sel_hi:[0,1,1] neg_lo:[0,0,1] neg_hi:[0,0,1]
	v_pk_add_f32 v[50:51], v[50:51], v[90:91]
	v_pk_mul_f32 v[90:91], v[88:89], s[62:63] op_sel_hi:[0,1]
	v_pk_fma_f32 v[90:91], v[86:87], s[58:59], v[90:91] op_sel_hi:[0,1,1] neg_lo:[0,0,1] neg_hi:[0,0,1]
	v_pk_add_f32 v[58:59], v[58:59], v[90:91]
	v_pk_mul_f32 v[90:91], v[88:89], s[80:81] op_sel_hi:[0,1]
	v_pk_fma_f32 v[90:91], v[86:87], s[64:65], v[90:91] op_sel_hi:[0,1,1] neg_lo:[0,0,1] neg_hi:[0,0,1]
	v_pk_add_f32 v[60:61], v[60:61], v[90:91]
	v_pk_mul_f32 v[90:91], v[88:89], s[84:85] op_sel_hi:[0,1]
	v_pk_fma_f32 v[90:91], v[86:87], s[82:83], v[90:91] op_sel_hi:[0,1,1] neg_lo:[0,0,1] neg_hi:[0,0,1]
	v_pk_add_f32 v[64:65], v[64:65], v[90:91]
	v_pk_mul_f32 v[90:91], v[88:89], s[88:89] op_sel_hi:[0,1]
	v_pk_fma_f32 v[90:91], v[86:87], s[86:87], v[90:91] op_sel_hi:[0,1,1] neg_lo:[0,0,1] neg_hi:[0,0,1]
	v_pk_add_f32 v[62:63], v[62:63], v[90:91]
	v_readlane_b32 s16, v10, 32
	v_readlane_b32 s17, v10, 34
	v_readlane_b32 s36, v10, 33
	v_readlane_b32 s37, v10, 35
	v_readlane_b32 s38, v10, 36
	v_readlane_b32 s39, v10, 38
	v_readlane_b32 s40, v10, 37
	v_readlane_b32 s41, v10, 39
	v_readlane_b32 s42, v10, 40
	v_readlane_b32 s43, v10, 42
	v_readlane_b32 s52, v10, 41
	v_readlane_b32 s53, v10, 43
	v_readlane_b32 s54, v10, 44
	v_readlane_b32 s55, v10, 46
	v_readlane_b32 s56, v10, 45
	v_readlane_b32 s57, v10, 47
	v_readlane_b32 s58, v10, 48
	v_readlane_b32 s59, v10, 50
	v_readlane_b32 s62, v10, 49
	v_readlane_b32 s63, v10, 51
	v_readlane_b32 s64, v10, 52
	v_readlane_b32 s65, v10, 54
	v_readlane_b32 s80, v10, 53
	v_readlane_b32 s81, v10, 55
	v_readlane_b32 s82, v10, 56
	v_readlane_b32 s83, v10, 58
	v_readlane_b32 s84, v10, 57
	v_readlane_b32 s85, v10, 59
	v_readlane_b32 s86, v10, 60
	v_readlane_b32 s87, v10, 62
	v_readlane_b32 s88, v10, 61
	v_readlane_b32 s89, v10, 63
	v_mul_f32_e32 v244, v19, v28
	v_mul_f32_e32 v245, v23, v29
	v_sub_f32_e32 v86, v244, v245
	v_mul_f32_e32 v244, v23, v28
	v_mul_f32_e32 v245, v19, v29
	v_add_f32_e32 v88, v244, v245
	v_pk_mul_f32 v[90:91], v[88:89], s[36:37] op_sel_hi:[0,1]
; __device__ __forceinline__ void ph1_small(const Args& a, int tid, int wave, int lane, int G, int bid) {
;     ...
; #pragma unroll 8
;             for (int n = 0; n < 64; ++n) { const float cr = cre[((size_t)g * 16 + p) * 64 + n], ci = cim[((size_t)g * 16 + p) * 64 + n];
;                 const float pr = POW[(((size_t)g * 65 + tau) * 64 + n) * 2], pi = POW[(((size_t)g * 65 + tau) * 64 + n) * 2 + 1];
;                 const float er = cr * pr - ci * pi, ei = cr * pi + ci * pr;
;                 const f32x4* bp = (const f32x4*)(BBAR + ((size_t)g * 64 + n) * 32);
; #pragma unroll
;                 for (int q = 0; q < 8; ++q) { const f32x4 bb = bp[q]; s[2 * q] += er * bb[0] - ei * bb[1]; s[2 * q + 1] += er * bb[2] - ei * bb[3]; } }
	v_pk_fma_f32 v[90:91], v[86:87], s[16:17], v[90:91] op_sel_hi:[0,1,1] neg_lo:[0,0,1] neg_hi:[0,0,1]
	v_pk_add_f32 v[56:57], v[56:57], v[90:91]
	v_pk_mul_f32 v[90:91], v[88:89], s[40:41] op_sel_hi:[0,1]
	v_pk_fma_f32 v[90:91], v[86:87], s[38:39], v[90:91] op_sel_hi:[0,1,1] neg_lo:[0,0,1] neg_hi:[0,0,1]
	v_pk_add_f32 v[54:55], v[54:55], v[90:91]
	v_pk_mul_f32 v[90:91], v[88:89], s[52:53] op_sel_hi:[0,1]
	v_pk_fma_f32 v[90:91], v[86:87], s[42:43], v[90:91] op_sel_hi:[0,1,1] neg_lo:[0,0,1] neg_hi:[0,0,1]
	v_pk_add_f32 v[52:53], v[52:53], v[90:91]
	v_pk_mul_f32 v[90:91], v[88:89], s[56:57] op_sel_hi:[0,1]
	v_pk_fma_f32 v[90:91], v[86:87], s[54:55], v[90:91] op_sel_hi:[0,1,1] neg_lo:[0,0,1] neg_hi:[0,0,1]
	v_pk_add_f32 v[50:51], v[50:51], v[90:91]
	v_pk_mul_f32 v[90:91], v[88:89], s[62:63] op_sel_hi:[0,1]
	v_pk_fma_f32 v[90:91], v[86:87], s[58:59], v[90:91] op_sel_hi:[0,1,1] neg_lo:[0,0,1] neg_hi:[0,0,1]
	v_pk_add_f32 v[58:59], v[58:59], v[90:91]
	v_pk_mul_f32 v[90:91], v[88:89], s[80:81] op_sel_hi:[0,1]
	v_pk_fma_f32 v[90:91], v[86:87], s[64:65], v[90:91] op_sel_hi:[0,1,1] neg_lo:[0,0,1] neg_hi:[0,0,1]
	v_pk_add_f32 v[60:61], v[60:61], v[90:91]
	v_pk_mul_f32 v[90:91], v[88:89], s[84:85] op_sel_hi:[0,1]
	v_pk_fma_f32 v[90:91], v[86:87], s[82:83], v[90:91] op_sel_hi:[0,1,1] neg_lo:[0,0,1] neg_hi:[0,0,1]
	v_pk_add_f32 v[64:65], v[64:65], v[90:91]
	v_pk_mul_f32 v[90:91], v[88:89], s[88:89] op_sel_hi:[0,1]
	v_pk_fma_f32 v[90:91], v[86:87], s[86:87], v[90:91] op_sel_hi:[0,1,1] neg_lo:[0,0,1] neg_hi:[0,0,1]
	v_pk_add_f32 v[62:63], v[62:63], v[90:91]
	v_readlane_b32 s16, v11, 0
	v_readlane_b32 s17, v11, 2
	v_readlane_b32 s36, v11, 1
	v_readlane_b32 s37, v11, 3
	v_readlane_b32 s38, v11, 4
	v_readlane_b32 s39, v11, 6
	v_readlane_b32 s40, v11, 5
	v_readlane_b32 s41, v11, 7
	v_readlane_b32 s42, v11, 8
	v_readlane_b32 s43, v11, 10
	v_readlane_b32 s52, v11, 9
	v_readlane_b32 s53, v11, 11
	v_readlane_b32 s54, v11, 12
	v_readlane_b32 s55, v11, 14
	v_readlane_b32 s56, v11, 13
	v_readlane_b32 s57, v11, 15
	v_readlane_b32 s58, v11, 16
	v_readlane_b32 s59, v11, 18
	v_readlane_b32 s62, v11, 17
	v_readlane_b32 s63, v11, 19
	v_readlane_b32 s64, v11, 20
	v_readlane_b32 s65, v11, 22
	v_readlane_b32 s80, v11, 21
	v_readlane_b32 s81, v11, 23
	v_readlane_b32 s82, v11, 24
	v_readlane_b32 s83, v11, 26
	v_readlane_b32 s84, v11, 25
	v_readlane_b32 s85, v11, 27
	v_readlane_b32 s86, v11, 28
	v_readlane_b32 s87, v11, 30
	v_readlane_b32 s88, v11, 29
	v_readlane_b32 s89, v11, 31
	v_mul_f32_e32 v244, v20, v46
	v_mul_f32_e32 v245, v24, v47
	v_sub_f32_e32 v86, v244, v245
	v_mul_f32_e32 v244, v24, v46
	v_mul_f32_e32 v245, v20, v47
	v_add_f32_e32 v88, v244, v245
	v_pk_mul_f32 v[90:91], v[88:89], s[36:37] op_sel_hi:[0,1]
	v_pk_fma_f32 v[90:91], v[86:87], s[16:17], v[90:91] op_sel_hi:[0,1,1] neg_lo:[0,0,1] neg_hi:[0,0,1]
	v_pk_add_f32 v[56:57], v[56:57], v[90:91]
	v_pk_mul_f32 v[90:91], v[88:89], s[40:41] op_sel_hi:[0,1]
	v_pk_fma_f32 v[90:91], v[86:87], s[38:39], v[90:91] op_sel_hi:[0,1,1] neg_lo:[0,0,1] neg_hi:[0,0,1]
	v_pk_add_f32 v[54:55], v[54:55], v[90:91]
	v_pk_mul_f32 v[90:91], v[88:89], s[52:53] op_sel_hi:[0,1]
	v_pk_fma_f32 v[90:91], v[86:87], s[42:43], v[90:91] op_sel_hi:[0,1,1] neg_lo:[0,0,1] neg_hi:[0,0,1]
	v_pk_add_f32 v[52:53], v[52:53], v[90:91]
	v_pk_mul_f32 v[90:91], v[88:89], s[56:57] op_sel_hi:[0,1]
	v_pk_fma_f32 v[90:91], v[86:87], s[54:55], v[90:91] op_sel_hi:[0,1,1] neg_lo:[0,0,1] neg_hi:[0,0,1]
	v_pk_add_f32 v[50:51], v[50:51], v[90:91]
	v_pk_mul_f32 v[90:91], v[88:89], s[62:63] op_sel_hi:[0,1]
	v_pk_fma_f32 v[90:91], v[86:87], s[58:59], v[90:91] op_sel_hi:[0,1,1] neg_lo:[0,0,1] neg_hi:[0,0,1]
	v_pk_add_f32 v[58:59], v[58:59], v[90:91]
	v_pk_mul_f32 v[90:91], v[88:89], s[80:81] op_sel_hi:[0,1]
	v_pk_fma_f32 v[90:91], v[86:87], s[64:65], v[90:91] op_sel_hi:[0,1,1] neg_lo:[0,0,1] neg_hi:[0,0,1]
	v_pk_add_f32 v[60:61], v[60:61], v[90:91]
	v_pk_mul_f32 v[90:91], v[88:89], s[84:85] op_sel_hi:[0,1]
	v_pk_fma_f32 v[90:91], v[86:87], s[82:83], v[90:91] op_sel_hi:[0,1,1] neg_lo:[0,0,1] neg_hi:[0,0,1]
	v_pk_add_f32 v[64:65], v[64:65], v[90:91]
	v_pk_mul_f32 v[90:91], v[88:89], s[88:89] op_sel_hi:[0,1]
	v_pk_fma_f32 v[90:91], v[86:87], s[86:87], v[90:91] op_sel_hi:[0,1,1] neg_lo:[0,0,1] neg_hi:[0,0,1]
	v_pk_add_f32 v[62:63], v[62:63], v[90:91]
	v_readlane_b32 s16, v11, 32
	v_readlane_b32 s17, v11, 34
	v_readlane_b32 s36, v11, 33
	v_readlane_b32 s37, v11, 35
	v_readlane_b32 s38, v11, 36
	v_readlane_b32 s39, v11, 38
	v_readlane_b32 s40, v11, 37
	v_readlane_b32 s41, v11, 39
	v_readlane_b32 s42, v11, 40
	v_readlane_b32 s43, v11, 42
	v_readlane_b32 s52, v11, 41
	v_readlane_b32 s53, v11, 43
	v_readlane_b32 s54, v11, 44
	v_readlane_b32 s55, v11, 46
	v_readlane_b32 s56, v11, 45
	v_readlane_b32 s57, v11, 47
	v_readlane_b32 s58, v11, 48
	v_readlane_b32 s59, v11, 50
	v_readlane_b32 s62, v11, 49
	v_readlane_b32 s63, v11, 51
	v_readlane_b32 s64, v11, 52
	v_readlane_b32 s65, v11, 54
	v_readlane_b32 s80, v11, 53
	v_readlane_b32 s81, v11, 55
	v_readlane_b32 s82, v11, 56
	v_readlane_b32 s83, v11, 58
	v_readlane_b32 s84, v11, 57
	v_readlane_b32 s85, v11, 59
	v_readlane_b32 s86, v11, 60
	v_readlane_b32 s87, v11, 62
	v_readlane_b32 s88, v11, 61
	v_readlane_b32 s89, v11, 63
	v_mul_f32_e32 v244, v21, v48
	v_mul_f32_e32 v245, v25, v49
	v_sub_f32_e32 v86, v244, v245
	v_mul_f32_e32 v244, v25, v48
	v_mul_f32_e32 v245, v21, v49
	v_add_f32_e32 v88, v244, v245
	v_pk_mul_f32 v[90:91], v[88:89], s[36:37] op_sel_hi:[0,1]
	v_pk_fma_f32 v[90:91], v[86:87], s[16:17], v[90:91] op_sel_hi:[0,1,1] neg_lo:[0,0,1] neg_hi:[0,0,1]
	v_pk_add_f32 v[56:57], v[56:57], v[90:91]
	v_pk_mul_f32 v[90:91], v[88:89], s[40:41] op_sel_hi:[0,1]
; __device__ __forceinline__ void ph1_small(const Args& a, int tid, int wave, int lane, int G, int bid) {
;     ...
; #pragma unroll 8
;             for (int n = 0; n < 64; ++n) { const float cr = cre[((size_t)g * 16 + p) * 64 + n], ci = cim[((size_t)g * 16 + p) * 64 + n];
;                 const float pr = POW[(((size_t)g * 65 + tau) * 64 + n) * 2], pi = POW[(((size_t)g * 65 + tau) * 64 + n) * 2 + 1];
;                 const float er = cr * pr - ci * pi, ei = cr * pi + ci * pr;
;                 const f32x4* bp = (const f32x4*)(BBAR + ((size_t)g * 64 + n) * 32);
; #pragma unroll
;                 for (int q = 0; q < 8; ++q) { const f32x4 bb = bp[q]; s[2 * q] += er * bb[0] - ei * bb[1]; s[2 * q + 1] += er * bb[2] - ei * bb[3]; } }
	v_pk_fma_f32 v[90:91], v[86:87], s[38:39], v[90:91] op_sel_hi:[0,1,1] neg_lo:[0,0,1] neg_hi:[0,0,1]
	v_pk_add_f32 v[54:55], v[54:55], v[90:91]
	v_pk_mul_f32 v[90:91], v[88:89], s[52:53] op_sel_hi:[0,1]
	v_pk_fma_f32 v[90:91], v[86:87], s[42:43], v[90:91] op_sel_hi:[0,1,1] neg_lo:[0,0,1] neg_hi:[0,0,1]
	v_pk_add_f32 v[52:53], v[52:53], v[90:91]
	v_pk_mul_f32 v[90:91], v[88:89], s[56:57] op_sel_hi:[0,1]
	v_pk_fma_f32 v[90:91], v[86:87], s[54:55], v[90:91] op_sel_hi:[0,1,1] neg_lo:[0,0,1] neg_hi:[0,0,1]
	v_pk_add_f32 v[50:51], v[50:51], v[90:91]
	v_pk_mul_f32 v[90:91], v[88:89], s[62:63] op_sel_hi:[0,1]
	v_pk_fma_f32 v[90:91], v[86:87], s[58:59], v[90:91] op_sel_hi:[0,1,1] neg_lo:[0,0,1] neg_hi:[0,0,1]
	v_pk_add_f32 v[58:59], v[58:59], v[90:91]
	v_pk_mul_f32 v[90:91], v[88:89], s[80:81] op_sel_hi:[0,1]
	v_pk_fma_f32 v[90:91], v[86:87], s[64:65], v[90:91] op_sel_hi:[0,1,1] neg_lo:[0,0,1] neg_hi:[0,0,1]
	v_pk_add_f32 v[60:61], v[60:61], v[90:91]
	v_pk_mul_f32 v[90:91], v[88:89], s[84:85] op_sel_hi:[0,1]
	v_pk_fma_f32 v[90:91], v[86:87], s[82:83], v[90:91] op_sel_hi:[0,1,1] neg_lo:[0,0,1] neg_hi:[0,0,1]
	v_pk_add_f32 v[64:65], v[64:65], v[90:91]
	v_pk_mul_f32 v[90:91], v[88:89], s[88:89] op_sel_hi:[0,1]
	v_pk_fma_f32 v[90:91], v[86:87], s[86:87], v[90:91] op_sel_hi:[0,1,1] neg_lo:[0,0,1] neg_hi:[0,0,1]
	v_pk_add_f32 v[62:63], v[62:63], v[90:91]
	global_load_dwordx4 v[18:21], v[44:45], off offset:96
	global_load_dwordx4 v[22:25], v[42:43], off offset:96
	global_load_dwordx4 v[26:29], v40, s[100:101] offset:192
	global_load_dwordx4 v[46:49], v40, s[100:101] offset:208
	s_waitcnt vmcnt(4)
	v_readlane_b32 s16, v12, 0
	v_readlane_b32 s17, v12, 2
	v_readlane_b32 s36, v12, 1
	v_readlane_b32 s37, v12, 3
	v_readlane_b32 s38, v12, 4
	v_readlane_b32 s39, v12, 6
	v_readlane_b32 s40, v12, 5
	v_readlane_b32 s41, v12, 7
	v_readlane_b32 s42, v12, 8
	v_readlane_b32 s43, v12, 10
	v_readlane_b32 s52, v12, 9
	v_readlane_b32 s53, v12, 11
	v_readlane_b32 s54, v12, 12
	v_readlane_b32 s55, v12, 14
	v_readlane_b32 s56, v12, 13
	v_readlane_b32 s57, v12, 15
	v_readlane_b32 s58, v12, 16
	v_readlane_b32 s59, v12, 18
	v_readlane_b32 s62, v12, 17
	v_readlane_b32 s63, v12, 19
	v_readlane_b32 s64, v12, 20
	v_readlane_b32 s65, v12, 22
	v_readlane_b32 s80, v12, 21
	v_readlane_b32 s81, v12, 23
	v_readlane_b32 s82, v12, 24
	v_readlane_b32 s83, v12, 26
	v_readlane_b32 s84, v12, 25
	v_readlane_b32 s85, v12, 27
	v_readlane_b32 s86, v12, 28
	v_readlane_b32 s87, v12, 30
	v_readlane_b32 s88, v12, 29
	v_readlane_b32 s89, v12, 31
	v_mul_f32_e32 v244, v70, v78
	v_mul_f32_e32 v245, v74, v79
	v_sub_f32_e32 v86, v244, v245
	v_mul_f32_e32 v244, v74, v78
	v_mul_f32_e32 v245, v70, v79
	v_add_f32_e32 v88, v244, v245
	v_pk_mul_f32 v[90:91], v[88:89], s[36:37] op_sel_hi:[0,1]
	v_pk_fma_f32 v[90:91], v[86:87], s[16:17], v[90:91] op_sel_hi:[0,1,1] neg_lo:[0,0,1] neg_hi:[0,0,1]
	v_pk_add_f32 v[56:57], v[56:57], v[90:91]
	v_pk_mul_f32 v[90:91], v[88:89], s[40:41] op_sel_hi:[0,1]
	v_pk_fma_f32 v[90:91], v[86:87], s[38:39], v[90:91] op_sel_hi:[0,1,1] neg_lo:[0,0,1] neg_hi:[0,0,1]
	v_pk_add_f32 v[54:55], v[54:55], v[90:91]
	v_pk_mul_f32 v[90:91], v[88:89], s[52:53] op_sel_hi:[0,1]
	v_pk_fma_f32 v[90:91], v[86:87], s[42:43], v[90:91] op_sel_hi:[0,1,1] neg_lo:[0,0,1] neg_hi:[0,0,1]
	v_pk_add_f32 v[52:53], v[52:53], v[90:91]
	v_pk_mul_f32 v[90:91], v[88:89], s[56:57] op_sel_hi:[0,1]
	v_pk_fma_f32 v[90:91], v[86:87], s[54:55], v[90:91] op_sel_hi:[0,1,1] neg_lo:[0,0,1] neg_hi:[0,0,1]
	v_pk_add_f32 v[50:51], v[50:51], v[90:91]
	v_pk_mul_f32 v[90:91], v[88:89], s[62:63] op_sel_hi:[0,1]
	v_pk_fma_f32 v[90:91], v[86:87], s[58:59], v[90:91] op_sel_hi:[0,1,1] neg_lo:[0,0,1] neg_hi:[0,0,1]
	v_pk_add_f32 v[58:59], v[58:59], v[90:91]
	v_pk_mul_f32 v[90:91], v[88:89], s[80:81] op_sel_hi:[0,1]
	v_pk_fma_f32 v[90:91], v[86:87], s[64:65], v[90:91] op_sel_hi:[0,1,1] neg_lo:[0,0,1] neg_hi:[0,0,1]
	v_pk_add_f32 v[60:61], v[60:61], v[90:91]
	v_pk_mul_f32 v[90:91], v[88:89], s[84:85] op_sel_hi:[0,1]
	v_pk_fma_f32 v[90:91], v[86:87], s[82:83], v[90:91] op_sel_hi:[0,1,1] neg_lo:[0,0,1] neg_hi:[0,0,1]
	v_pk_add_f32 v[64:65], v[64:65], v[90:91]
	v_pk_mul_f32 v[90:91], v[88:89], s[88:89] op_sel_hi:[0,1]
	v_pk_fma_f32 v[90:91], v[86:87], s[86:87], v[90:91] op_sel_hi:[0,1,1] neg_lo:[0,0,1] neg_hi:[0,0,1]
	v_pk_add_f32 v[62:63], v[62:63], v[90:91]
	v_readlane_b32 s16, v12, 32
	v_readlane_b32 s17, v12, 34
	v_readlane_b32 s36, v12, 33
	v_readlane_b32 s37, v12, 35
	v_readlane_b32 s38, v12, 36
	v_readlane_b32 s39, v12, 38
	v_readlane_b32 s40, v12, 37
	v_readlane_b32 s41, v12, 39
	v_readlane_b32 s42, v12, 40
	v_readlane_b32 s43, v12, 42
	v_readlane_b32 s52, v12, 41
	v_readlane_b32 s53, v12, 43
	v_readlane_b32 s54, v12, 44
	v_readlane_b32 s55, v12, 46
	v_readlane_b32 s56, v12, 45
	v_readlane_b32 s57, v12, 47
	v_readlane_b32 s58, v12, 48
	v_readlane_b32 s59, v12, 50
	v_readlane_b32 s62, v12, 49
	v_readlane_b32 s63, v12, 51
	v_readlane_b32 s64, v12, 52
	v_readlane_b32 s65, v12, 54
	v_readlane_b32 s80, v12, 53
	v_readlane_b32 s81, v12, 55
	v_readlane_b32 s82, v12, 56
	v_readlane_b32 s83, v12, 58
	v_readlane_b32 s84, v12, 57
	v_readlane_b32 s85, v12, 59
	v_readlane_b32 s86, v12, 60
	v_readlane_b32 s87, v12, 62
	v_readlane_b32 s88, v12, 61
	v_readlane_b32 s89, v12, 63
	v_mul_f32_e32 v244, v71, v80
	v_mul_f32_e32 v245, v75, v81
	v_sub_f32_e32 v86, v244, v245
	v_mul_f32_e32 v244, v75, v80
	v_mul_f32_e32 v245, v71, v81
	v_add_f32_e32 v88, v244, v245
	v_pk_mul_f32 v[90:91], v[88:89], s[36:37] op_sel_hi:[0,1]
	v_pk_fma_f32 v[90:91], v[86:87], s[16:17], v[90:91] op_sel_hi:[0,1,1] neg_lo:[0,0,1] neg_hi:[0,0,1]
	v_pk_add_f32 v[56:57], v[56:57], v[90:91]
; __device__ __forceinline__ void ph1_small(const Args& a, int tid, int wave, int lane, int G, int bid) {
;     ...
; #pragma unroll 8
;             for (int n = 0; n < 64; ++n) { const float cr = cre[((size_t)g * 16 + p) * 64 + n], ci = cim[((size_t)g * 16 + p) * 64 + n];
;                 const float pr = POW[(((size_t)g * 65 + tau) * 64 + n) * 2], pi = POW[(((size_t)g * 65 + tau) * 64 + n) * 2 + 1];
;                 const float er = cr * pr - ci * pi, ei = cr * pi + ci * pr;
;                 const f32x4* bp = (const f32x4*)(BBAR + ((size_t)g * 64 + n) * 32);
; #pragma unroll
;                 for (int q = 0; q < 8; ++q) { const f32x4 bb = bp[q]; s[2 * q] += er * bb[0] - ei * bb[1]; s[2 * q + 1] += er * bb[2] - ei * bb[3]; } }
	v_pk_mul_f32 v[90:91], v[88:89], s[40:41] op_sel_hi:[0,1]
	v_pk_fma_f32 v[90:91], v[86:87], s[38:39], v[90:91] op_sel_hi:[0,1,1] neg_lo:[0,0,1] neg_hi:[0,0,1]
	v_pk_add_f32 v[54:55], v[54:55], v[90:91]
	v_pk_mul_f32 v[90:91], v[88:89], s[52:53] op_sel_hi:[0,1]
	v_pk_fma_f32 v[90:91], v[86:87], s[42:43], v[90:91] op_sel_hi:[0,1,1] neg_lo:[0,0,1] neg_hi:[0,0,1]
	v_pk_add_f32 v[52:53], v[52:53], v[90:91]
	v_pk_mul_f32 v[90:91], v[88:89], s[56:57] op_sel_hi:[0,1]
	v_pk_fma_f32 v[90:91], v[86:87], s[54:55], v[90:91] op_sel_hi:[0,1,1] neg_lo:[0,0,1] neg_hi:[0,0,1]
	v_pk_add_f32 v[50:51], v[50:51], v[90:91]
	v_pk_mul_f32 v[90:91], v[88:89], s[62:63] op_sel_hi:[0,1]
	v_pk_fma_f32 v[90:91], v[86:87], s[58:59], v[90:91] op_sel_hi:[0,1,1] neg_lo:[0,0,1] neg_hi:[0,0,1]
	v_pk_add_f32 v[58:59], v[58:59], v[90:91]
	v_pk_mul_f32 v[90:91], v[88:89], s[80:81] op_sel_hi:[0,1]
	v_pk_fma_f32 v[90:91], v[86:87], s[64:65], v[90:91] op_sel_hi:[0,1,1] neg_lo:[0,0,1] neg_hi:[0,0,1]
	v_pk_add_f32 v[60:61], v[60:61], v[90:91]
	v_pk_mul_f32 v[90:91], v[88:89], s[84:85] op_sel_hi:[0,1]
	v_pk_fma_f32 v[90:91], v[86:87], s[82:83], v[90:91] op_sel_hi:[0,1,1] neg_lo:[0,0,1] neg_hi:[0,0,1]
	v_pk_add_f32 v[64:65], v[64:65], v[90:91]
	v_pk_mul_f32 v[90:91], v[88:89], s[88:89] op_sel_hi:[0,1]
	v_pk_fma_f32 v[90:91], v[86:87], s[86:87], v[90:91] op_sel_hi:[0,1,1] neg_lo:[0,0,1] neg_hi:[0,0,1]
	v_pk_add_f32 v[62:63], v[62:63], v[90:91]
	v_readlane_b32 s16, v13, 0
	v_readlane_b32 s17, v13, 2
	v_readlane_b32 s36, v13, 1
	v_readlane_b32 s37, v13, 3
	v_readlane_b32 s38, v13, 4
	v_readlane_b32 s39, v13, 6
	v_readlane_b32 s40, v13, 5
	v_readlane_b32 s41, v13, 7
	v_readlane_b32 s42, v13, 8
	v_readlane_b32 s43, v13, 10
	v_readlane_b32 s52, v13, 9
	v_readlane_b32 s53, v13, 11
	v_readlane_b32 s54, v13, 12
	v_readlane_b32 s55, v13, 14
	v_readlane_b32 s56, v13, 13
	v_readlane_b32 s57, v13, 15
	v_readlane_b32 s58, v13, 16
	v_readlane_b32 s59, v13, 18
	v_readlane_b32 s62, v13, 17
	v_readlane_b32 s63, v13, 19
	v_readlane_b32 s64, v13, 20
	v_readlane_b32 s65, v13, 22
	v_readlane_b32 s80, v13, 21
	v_readlane_b32 s81, v13, 23
	v_readlane_b32 s82, v13, 24
	v_readlane_b32 s83, v13, 26
	v_readlane_b32 s84, v13, 25
	v_readlane_b32 s85, v13, 27
	v_readlane_b32 s86, v13, 28
	v_readlane_b32 s87, v13, 30
	v_readlane_b32 s88, v13, 29
	v_readlane_b32 s89, v13, 31
	v_mul_f32_e32 v244, v72, v82
	v_mul_f32_e32 v245, v76, v83
	v_sub_f32_e32 v86, v244, v245
	v_mul_f32_e32 v244, v76, v82
	v_mul_f32_e32 v245, v72, v83
	v_add_f32_e32 v88, v244, v245
	v_pk_mul_f32 v[90:91], v[88:89], s[36:37] op_sel_hi:[0,1]
	v_pk_fma_f32 v[90:91], v[86:87], s[16:17], v[90:91] op_sel_hi:[0,1,1] neg_lo:[0,0,1] neg_hi:[0,0,1]
	v_pk_add_f32 v[56:57], v[56:57], v[90:91]
	v_pk_mul_f32 v[90:91], v[88:89], s[40:41] op_sel_hi:[0,1]
	v_pk_fma_f32 v[90:91], v[86:87], s[38:39], v[90:91] op_sel_hi:[0,1,1] neg_lo:[0,0,1] neg_hi:[0,0,1]
	v_pk_add_f32 v[54:55], v[54:55], v[90:91]
	v_pk_mul_f32 v[90:91], v[88:89], s[52:53] op_sel_hi:[0,1]
	v_pk_fma_f32 v[90:91], v[86:87], s[42:43], v[90:91] op_sel_hi:[0,1,1] neg_lo:[0,0,1] neg_hi:[0,0,1]
	v_pk_add_f32 v[52:53], v[52:53], v[90:91]
	v_pk_mul_f32 v[90:91], v[88:89], s[56:57] op_sel_hi:[0,1]
	v_pk_fma_f32 v[90:91], v[86:87], s[54:55], v[90:91] op_sel_hi:[0,1,1] neg_lo:[0,0,1] neg_hi:[0,0,1]
	v_pk_add_f32 v[50:51], v[50:51], v[90:91]
	v_pk_mul_f32 v[90:91], v[88:89], s[62:63] op_sel_hi:[0,1]
	v_pk_fma_f32 v[90:91], v[86:87], s[58:59], v[90:91] op_sel_hi:[0,1,1] neg_lo:[0,0,1] neg_hi:[0,0,1]
	v_pk_add_f32 v[58:59], v[58:59], v[90:91]
	v_pk_mul_f32 v[90:91], v[88:89], s[80:81] op_sel_hi:[0,1]
	v_pk_fma_f32 v[90:91], v[86:87], s[64:65], v[90:91] op_sel_hi:[0,1,1] neg_lo:[0,0,1] neg_hi:[0,0,1]
	v_pk_add_f32 v[60:61], v[60:61], v[90:91]
	v_pk_mul_f32 v[90:91], v[88:89], s[84:85] op_sel_hi:[0,1]
	v_pk_fma_f32 v[90:91], v[86:87], s[82:83], v[90:91] op_sel_hi:[0,1,1] neg_lo:[0,0,1] neg_hi:[0,0,1]
	v_pk_add_f32 v[64:65], v[64:65], v[90:91]
	v_pk_mul_f32 v[90:91], v[88:89], s[88:89] op_sel_hi:[0,1]
	v_pk_fma_f32 v[90:91], v[86:87], s[86:87], v[90:91] op_sel_hi:[0,1,1] neg_lo:[0,0,1] neg_hi:[0,0,1]
	v_pk_add_f32 v[62:63], v[62:63], v[90:91]
	v_readlane_b32 s16, v13, 32
	v_readlane_b32 s17, v13, 34
	v_readlane_b32 s36, v13, 33
	v_readlane_b32 s37, v13, 35
	v_readlane_b32 s38, v13, 36
	v_readlane_b32 s39, v13, 38
	v_readlane_b32 s40, v13, 37
	v_readlane_b32 s41, v13, 39
	v_readlane_b32 s42, v13, 40
	v_readlane_b32 s43, v13, 42
	v_readlane_b32 s52, v13, 41
	v_readlane_b32 s53, v13, 43
	v_readlane_b32 s54, v13, 44
	v_readlane_b32 s55, v13, 46
	v_readlane_b32 s56, v13, 45
	v_readlane_b32 s57, v13, 47
	v_readlane_b32 s58, v13, 48
	v_readlane_b32 s59, v13, 50
	v_readlane_b32 s62, v13, 49
	v_readlane_b32 s63, v13, 51
	v_readlane_b32 s64, v13, 52
	v_readlane_b32 s65, v13, 54
	v_readlane_b32 s80, v13, 53
	v_readlane_b32 s81, v13, 55
	v_readlane_b32 s82, v13, 56
	v_readlane_b32 s83, v13, 58
	v_readlane_b32 s84, v13, 57
	v_readlane_b32 s85, v13, 59
	v_readlane_b32 s86, v13, 60
	v_readlane_b32 s87, v13, 62
	v_readlane_b32 s88, v13, 61
	v_readlane_b32 s89, v13, 63
	v_mul_f32_e32 v244, v73, v84
	v_mul_f32_e32 v245, v77, v85
	v_sub_f32_e32 v86, v244, v245
	v_mul_f32_e32 v244, v77, v84
	v_mul_f32_e32 v245, v73, v85
	v_add_f32_e32 v88, v244, v245
	v_pk_mul_f32 v[90:91], v[88:89], s[36:37] op_sel_hi:[0,1]
	v_pk_fma_f32 v[90:91], v[86:87], s[16:17], v[90:91] op_sel_hi:[0,1,1] neg_lo:[0,0,1] neg_hi:[0,0,1]
	v_pk_add_f32 v[56:57], v[56:57], v[90:91]
	v_pk_mul_f32 v[90:91], v[88:89], s[40:41] op_sel_hi:[0,1]
	v_pk_fma_f32 v[90:91], v[86:87], s[38:39], v[90:91] op_sel_hi:[0,1,1] neg_lo:[0,0,1] neg_hi:[0,0,1]
	v_pk_add_f32 v[54:55], v[54:55], v[90:91]
; __device__ __forceinline__ void ph1_small(const Args& a, int tid, int wave, int lane, int G, int bid) {
;     ...
; #pragma unroll 8
;             for (int n = 0; n < 64; ++n) { const float cr = cre[((size_t)g * 16 + p) * 64 + n], ci = cim[((size_t)g * 16 + p) * 64 + n];
;                 const float pr = POW[(((size_t)g * 65 + tau) * 64 + n) * 2], pi = POW[(((size_t)g * 65 + tau) * 64 + n) * 2 + 1];
;                 const float er = cr * pr - ci * pi, ei = cr * pi + ci * pr;
;                 const f32x4* bp = (const f32x4*)(BBAR + ((size_t)g * 64 + n) * 32);
; #pragma unroll
;                 for (int q = 0; q < 8; ++q) { const f32x4 bb = bp[q]; s[2 * q] += er * bb[0] - ei * bb[1]; s[2 * q + 1] += er * bb[2] - ei * bb[3]; } }
	v_pk_mul_f32 v[90:91], v[88:89], s[52:53] op_sel_hi:[0,1]
	v_pk_fma_f32 v[90:91], v[86:87], s[42:43], v[90:91] op_sel_hi:[0,1,1] neg_lo:[0,0,1] neg_hi:[0,0,1]
	v_pk_add_f32 v[52:53], v[52:53], v[90:91]
	v_pk_mul_f32 v[90:91], v[88:89], s[56:57] op_sel_hi:[0,1]
	v_pk_fma_f32 v[90:91], v[86:87], s[54:55], v[90:91] op_sel_hi:[0,1,1] neg_lo:[0,0,1] neg_hi:[0,0,1]
	v_pk_add_f32 v[50:51], v[50:51], v[90:91]
	v_pk_mul_f32 v[90:91], v[88:89], s[62:63] op_sel_hi:[0,1]
	v_pk_fma_f32 v[90:91], v[86:87], s[58:59], v[90:91] op_sel_hi:[0,1,1] neg_lo:[0,0,1] neg_hi:[0,0,1]
	v_pk_add_f32 v[58:59], v[58:59], v[90:91]
	v_pk_mul_f32 v[90:91], v[88:89], s[80:81] op_sel_hi:[0,1]
	v_pk_fma_f32 v[90:91], v[86:87], s[64:65], v[90:91] op_sel_hi:[0,1,1] neg_lo:[0,0,1] neg_hi:[0,0,1]
	v_pk_add_f32 v[60:61], v[60:61], v[90:91]
	v_pk_mul_f32 v[90:91], v[88:89], s[84:85] op_sel_hi:[0,1]
	v_pk_fma_f32 v[90:91], v[86:87], s[82:83], v[90:91] op_sel_hi:[0,1,1] neg_lo:[0,0,1] neg_hi:[0,0,1]
	v_pk_add_f32 v[64:65], v[64:65], v[90:91]
	v_pk_mul_f32 v[90:91], v[88:89], s[88:89] op_sel_hi:[0,1]
	v_pk_fma_f32 v[90:91], v[86:87], s[86:87], v[90:91] op_sel_hi:[0,1,1] neg_lo:[0,0,1] neg_hi:[0,0,1]
	v_pk_add_f32 v[62:63], v[62:63], v[90:91]
	global_load_dwordx4 v[70:73], v[44:45], off offset:112
	global_load_dwordx4 v[74:77], v[42:43], off offset:112
	global_load_dwordx4 v[78:81], v40, s[100:101] offset:224
	global_load_dwordx4 v[82:85], v40, s[100:101] offset:240
	s_waitcnt vmcnt(4)
	v_readlane_b32 s16, v14, 0
	v_readlane_b32 s17, v14, 2
	v_readlane_b32 s36, v14, 1
	v_readlane_b32 s37, v14, 3
	v_readlane_b32 s38, v14, 4
	v_readlane_b32 s39, v14, 6
	v_readlane_b32 s40, v14, 5
	v_readlane_b32 s41, v14, 7
	v_readlane_b32 s42, v14, 8
	v_readlane_b32 s43, v14, 10
	v_readlane_b32 s52, v14, 9
	v_readlane_b32 s53, v14, 11
	v_readlane_b32 s54, v14, 12
	v_readlane_b32 s55, v14, 14
	v_readlane_b32 s56, v14, 13
	v_readlane_b32 s57, v14, 15
	v_readlane_b32 s58, v14, 16
	v_readlane_b32 s59, v14, 18
	v_readlane_b32 s62, v14, 17
	v_readlane_b32 s63, v14, 19
	v_readlane_b32 s64, v14, 20
	v_readlane_b32 s65, v14, 22
	v_readlane_b32 s80, v14, 21
	v_readlane_b32 s81, v14, 23
	v_readlane_b32 s82, v14, 24
	v_readlane_b32 s83, v14, 26
	v_readlane_b32 s84, v14, 25
	v_readlane_b32 s85, v14, 27
	v_readlane_b32 s86, v14, 28
	v_readlane_b32 s87, v14, 30
	v_readlane_b32 s88, v14, 29
	v_readlane_b32 s89, v14, 31
	v_mul_f32_e32 v244, v18, v26
	v_mul_f32_e32 v245, v22, v27
	v_sub_f32_e32 v86, v244, v245
	v_mul_f32_e32 v244, v22, v26
	v_mul_f32_e32 v245, v18, v27
	v_add_f32_e32 v88, v244, v245
	v_pk_mul_f32 v[90:91], v[88:89], s[36:37] op_sel_hi:[0,1]
	v_pk_fma_f32 v[90:91], v[86:87], s[16:17], v[90:91] op_sel_hi:[0,1,1] neg_lo:[0,0,1] neg_hi:[0,0,1]
	v_pk_add_f32 v[56:57], v[56:57], v[90:91]
	v_pk_mul_f32 v[90:91], v[88:89], s[40:41] op_sel_hi:[0,1]
	v_pk_fma_f32 v[90:91], v[86:87], s[38:39], v[90:91] op_sel_hi:[0,1,1] neg_lo:[0,0,1] neg_hi:[0,0,1]
	v_pk_add_f32 v[54:55], v[54:55], v[90:91]
	v_pk_mul_f32 v[90:91], v[88:89], s[52:53] op_sel_hi:[0,1]
	v_pk_fma_f32 v[90:91], v[86:87], s[42:43], v[90:91] op_sel_hi:[0,1,1] neg_lo:[0,0,1] neg_hi:[0,0,1]
	v_pk_add_f32 v[52:53], v[52:53], v[90:91]
	v_pk_mul_f32 v[90:91], v[88:89], s[56:57] op_sel_hi:[0,1]
	v_pk_fma_f32 v[90:91], v[86:87], s[54:55], v[90:91] op_sel_hi:[0,1,1] neg_lo:[0,0,1] neg_hi:[0,0,1]
	v_pk_add_f32 v[50:51], v[50:51], v[90:91]
	v_pk_mul_f32 v[90:91], v[88:89], s[62:63] op_sel_hi:[0,1]
	v_pk_fma_f32 v[90:91], v[86:87], s[58:59], v[90:91] op_sel_hi:[0,1,1] neg_lo:[0,0,1] neg_hi:[0,0,1]
	v_pk_add_f32 v[58:59], v[58:59], v[90:91]
	v_pk_mul_f32 v[90:91], v[88:89], s[80:81] op_sel_hi:[0,1]
	v_pk_fma_f32 v[90:91], v[86:87], s[64:65], v[90:91] op_sel_hi:[0,1,1] neg_lo:[0,0,1] neg_hi:[0,0,1]
	v_pk_add_f32 v[60:61], v[60:61], v[90:91]
	v_pk_mul_f32 v[90:91], v[88:89], s[84:85] op_sel_hi:[0,1]
	v_pk_fma_f32 v[90:91], v[86:87], s[82:83], v[90:91] op_sel_hi:[0,1,1] neg_lo:[0,0,1] neg_hi:[0,0,1]
	v_pk_add_f32 v[64:65], v[64:65], v[90:91]
	v_pk_mul_f32 v[90:91], v[88:89], s[88:89] op_sel_hi:[0,1]
	v_pk_fma_f32 v[90:91], v[86:87], s[86:87], v[90:91] op_sel_hi:[0,1,1] neg_lo:[0,0,1] neg_hi:[0,0,1]
	v_pk_add_f32 v[62:63], v[62:63], v[90:91]
	v_readlane_b32 s16, v14, 32
	v_readlane_b32 s17, v14, 34
	v_readlane_b32 s36, v14, 33
	v_readlane_b32 s37, v14, 35
	v_readlane_b32 s38, v14, 36
	v_readlane_b32 s39, v14, 38
	v_readlane_b32 s40, v14, 37
	v_readlane_b32 s41, v14, 39
	v_readlane_b32 s42, v14, 40
	v_readlane_b32 s43, v14, 42
	v_readlane_b32 s52, v14, 41
	v_readlane_b32 s53, v14, 43
	v_readlane_b32 s54, v14, 44
	v_readlane_b32 s55, v14, 46
	v_readlane_b32 s56, v14, 45
	v_readlane_b32 s57, v14, 47
	v_readlane_b32 s58, v14, 48
	v_readlane_b32 s59, v14, 50
	v_readlane_b32 s62, v14, 49
	v_readlane_b32 s63, v14, 51
	v_readlane_b32 s64, v14, 52
	v_readlane_b32 s65, v14, 54
	v_readlane_b32 s80, v14, 53
	v_readlane_b32 s81, v14, 55
	v_readlane_b32 s82, v14, 56
	v_readlane_b32 s83, v14, 58
	v_readlane_b32 s84, v14, 57
	v_readlane_b32 s85, v14, 59
	v_readlane_b32 s86, v14, 60
	v_readlane_b32 s87, v14, 62
	v_readlane_b32 s88, v14, 61
	v_readlane_b32 s89, v14, 63
	v_mul_f32_e32 v244, v19, v28
	v_mul_f32_e32 v245, v23, v29
	v_sub_f32_e32 v86, v244, v245
	v_mul_f32_e32 v244, v23, v28
	v_mul_f32_e32 v245, v19, v29
	v_add_f32_e32 v88, v244, v245
	v_pk_mul_f32 v[90:91], v[88:89], s[36:37] op_sel_hi:[0,1]
	v_pk_fma_f32 v[90:91], v[86:87], s[16:17], v[90:91] op_sel_hi:[0,1,1] neg_lo:[0,0,1] neg_hi:[0,0,1]
	v_pk_add_f32 v[56:57], v[56:57], v[90:91]
	v_pk_mul_f32 v[90:91], v[88:89], s[40:41] op_sel_hi:[0,1]
	v_pk_fma_f32 v[90:91], v[86:87], s[38:39], v[90:91] op_sel_hi:[0,1,1] neg_lo:[0,0,1] neg_hi:[0,0,1]
; __device__ __forceinline__ void ph1_small(const Args& a, int tid, int wave, int lane, int G, int bid) {
;     ...
; #pragma unroll 8
;             for (int n = 0; n < 64; ++n) { const float cr = cre[((size_t)g * 16 + p) * 64 + n], ci = cim[((size_t)g * 16 + p) * 64 + n];
;                 const float pr = POW[(((size_t)g * 65 + tau) * 64 + n) * 2], pi = POW[(((size_t)g * 65 + tau) * 64 + n) * 2 + 1];
;                 const float er = cr * pr - ci * pi, ei = cr * pi + ci * pr;
;                 const f32x4* bp = (const f32x4*)(BBAR + ((size_t)g * 64 + n) * 32);
; #pragma unroll
;                 for (int q = 0; q < 8; ++q) { const f32x4 bb = bp[q]; s[2 * q] += er * bb[0] - ei * bb[1]; s[2 * q + 1] += er * bb[2] - ei * bb[3]; } }
	v_pk_add_f32 v[54:55], v[54:55], v[90:91]
	v_pk_mul_f32 v[90:91], v[88:89], s[52:53] op_sel_hi:[0,1]
	v_pk_fma_f32 v[90:91], v[86:87], s[42:43], v[90:91] op_sel_hi:[0,1,1] neg_lo:[0,0,1] neg_hi:[0,0,1]
	v_pk_add_f32 v[52:53], v[52:53], v[90:91]
	v_pk_mul_f32 v[90:91], v[88:89], s[56:57] op_sel_hi:[0,1]
	v_pk_fma_f32 v[90:91], v[86:87], s[54:55], v[90:91] op_sel_hi:[0,1,1] neg_lo:[0,0,1] neg_hi:[0,0,1]
	v_pk_add_f32 v[50:51], v[50:51], v[90:91]
	v_pk_mul_f32 v[90:91], v[88:89], s[62:63] op_sel_hi:[0,1]
	v_pk_fma_f32 v[90:91], v[86:87], s[58:59], v[90:91] op_sel_hi:[0,1,1] neg_lo:[0,0,1] neg_hi:[0,0,1]
	v_pk_add_f32 v[58:59], v[58:59], v[90:91]
	v_pk_mul_f32 v[90:91], v[88:89], s[80:81] op_sel_hi:[0,1]
	v_pk_fma_f32 v[90:91], v[86:87], s[64:65], v[90:91] op_sel_hi:[0,1,1] neg_lo:[0,0,1] neg_hi:[0,0,1]
	v_pk_add_f32 v[60:61], v[60:61], v[90:91]
	v_pk_mul_f32 v[90:91], v[88:89], s[84:85] op_sel_hi:[0,1]
	v_pk_fma_f32 v[90:91], v[86:87], s[82:83], v[90:91] op_sel_hi:[0,1,1] neg_lo:[0,0,1] neg_hi:[0,0,1]
	v_pk_add_f32 v[64:65], v[64:65], v[90:91]
	v_pk_mul_f32 v[90:91], v[88:89], s[88:89] op_sel_hi:[0,1]
	v_pk_fma_f32 v[90:91], v[86:87], s[86:87], v[90:91] op_sel_hi:[0,1,1] neg_lo:[0,0,1] neg_hi:[0,0,1]
	v_pk_add_f32 v[62:63], v[62:63], v[90:91]
	v_readlane_b32 s16, v15, 0
	v_readlane_b32 s17, v15, 2
	v_readlane_b32 s36, v15, 1
	v_readlane_b32 s37, v15, 3
	v_readlane_b32 s38, v15, 4
	v_readlane_b32 s39, v15, 6
	v_readlane_b32 s40, v15, 5
	v_readlane_b32 s41, v15, 7
	v_readlane_b32 s42, v15, 8
	v_readlane_b32 s43, v15, 10
	v_readlane_b32 s52, v15, 9
	v_readlane_b32 s53, v15, 11
	v_readlane_b32 s54, v15, 12
	v_readlane_b32 s55, v15, 14
	v_readlane_b32 s56, v15, 13
	v_readlane_b32 s57, v15, 15
	v_readlane_b32 s58, v15, 16
	v_readlane_b32 s59, v15, 18
	v_readlane_b32 s62, v15, 17
	v_readlane_b32 s63, v15, 19
	v_readlane_b32 s64, v15, 20
	v_readlane_b32 s65, v15, 22
	v_readlane_b32 s80, v15, 21
	v_readlane_b32 s81, v15, 23
	v_readlane_b32 s82, v15, 24
	v_readlane_b32 s83, v15, 26
	v_readlane_b32 s84, v15, 25
	v_readlane_b32 s85, v15, 27
	v_readlane_b32 s86, v15, 28
	v_readlane_b32 s87, v15, 30
	v_readlane_b32 s88, v15, 29
	v_readlane_b32 s89, v15, 31
	v_mul_f32_e32 v244, v20, v46
	v_mul_f32_e32 v245, v24, v47
	v_sub_f32_e32 v86, v244, v245
	v_mul_f32_e32 v244, v24, v46
	v_mul_f32_e32 v245, v20, v47
	v_add_f32_e32 v88, v244, v245
	v_pk_mul_f32 v[90:91], v[88:89], s[36:37] op_sel_hi:[0,1]
	v_pk_fma_f32 v[90:91], v[86:87], s[16:17], v[90:91] op_sel_hi:[0,1,1] neg_lo:[0,0,1] neg_hi:[0,0,1]
	v_pk_add_f32 v[56:57], v[56:57], v[90:91]
	v_pk_mul_f32 v[90:91], v[88:89], s[40:41] op_sel_hi:[0,1]
	v_pk_fma_f32 v[90:91], v[86:87], s[38:39], v[90:91] op_sel_hi:[0,1,1] neg_lo:[0,0,1] neg_hi:[0,0,1]
	v_pk_add_f32 v[54:55], v[54:55], v[90:91]
	v_pk_mul_f32 v[90:91], v[88:89], s[52:53] op_sel_hi:[0,1]
	v_pk_fma_f32 v[90:91], v[86:87], s[42:43], v[90:91] op_sel_hi:[0,1,1] neg_lo:[0,0,1] neg_hi:[0,0,1]
	v_pk_add_f32 v[52:53], v[52:53], v[90:91]
	v_pk_mul_f32 v[90:91], v[88:89], s[56:57] op_sel_hi:[0,1]
	v_pk_fma_f32 v[90:91], v[86:87], s[54:55], v[90:91] op_sel_hi:[0,1,1] neg_lo:[0,0,1] neg_hi:[0,0,1]
	v_pk_add_f32 v[50:51], v[50:51], v[90:91]
	v_pk_mul_f32 v[90:91], v[88:89], s[62:63] op_sel_hi:[0,1]
	v_pk_fma_f32 v[90:91], v[86:87], s[58:59], v[90:91] op_sel_hi:[0,1,1] neg_lo:[0,0,1] neg_hi:[0,0,1]
	v_pk_add_f32 v[58:59], v[58:59], v[90:91]
	v_pk_mul_f32 v[90:91], v[88:89], s[80:81] op_sel_hi:[0,1]
	v_pk_fma_f32 v[90:91], v[86:87], s[64:65], v[90:91] op_sel_hi:[0,1,1] neg_lo:[0,0,1] neg_hi:[0,0,1]
	v_pk_add_f32 v[60:61], v[60:61], v[90:91]
	v_pk_mul_f32 v[90:91], v[88:89], s[84:85] op_sel_hi:[0,1]
	v_pk_fma_f32 v[90:91], v[86:87], s[82:83], v[90:91] op_sel_hi:[0,1,1] neg_lo:[0,0,1] neg_hi:[0,0,1]
	v_pk_add_f32 v[64:65], v[64:65], v[90:91]
	v_pk_mul_f32 v[90:91], v[88:89], s[88:89] op_sel_hi:[0,1]
	v_pk_fma_f32 v[90:91], v[86:87], s[86:87], v[90:91] op_sel_hi:[0,1,1] neg_lo:[0,0,1] neg_hi:[0,0,1]
	v_pk_add_f32 v[62:63], v[62:63], v[90:91]
	v_readlane_b32 s16, v15, 32
	v_readlane_b32 s17, v15, 34
	v_readlane_b32 s36, v15, 33
	v_readlane_b32 s37, v15, 35
	v_readlane_b32 s38, v15, 36
	v_readlane_b32 s39, v15, 38
	v_readlane_b32 s40, v15, 37
	v_readlane_b32 s41, v15, 39
	v_readlane_b32 s42, v15, 40
	v_readlane_b32 s43, v15, 42
	v_readlane_b32 s52, v15, 41
	v_readlane_b32 s53, v15, 43
	v_readlane_b32 s54, v15, 44
	v_readlane_b32 s55, v15, 46
	v_readlane_b32 s56, v15, 45
	v_readlane_b32 s57, v15, 47
	v_readlane_b32 s58, v15, 48
	v_readlane_b32 s59, v15, 50
	v_readlane_b32 s62, v15, 49
	v_readlane_b32 s63, v15, 51
	v_readlane_b32 s64, v15, 52
	v_readlane_b32 s65, v15, 54
	v_readlane_b32 s80, v15, 53
	v_readlane_b32 s81, v15, 55
	v_readlane_b32 s82, v15, 56
	v_readlane_b32 s83, v15, 58
	v_readlane_b32 s84, v15, 57
	v_readlane_b32 s85, v15, 59
	v_readlane_b32 s86, v15, 60
	v_readlane_b32 s87, v15, 62
	v_readlane_b32 s88, v15, 61
	v_readlane_b32 s89, v15, 63
	v_mul_f32_e32 v244, v21, v48
	v_mul_f32_e32 v245, v25, v49
	v_sub_f32_e32 v86, v244, v245
	v_mul_f32_e32 v244, v25, v48
	v_mul_f32_e32 v245, v21, v49
	v_add_f32_e32 v88, v244, v245
	v_pk_mul_f32 v[90:91], v[88:89], s[36:37] op_sel_hi:[0,1]
	v_pk_fma_f32 v[90:91], v[86:87], s[16:17], v[90:91] op_sel_hi:[0,1,1] neg_lo:[0,0,1] neg_hi:[0,0,1]
	v_pk_add_f32 v[56:57], v[56:57], v[90:91]
	v_pk_mul_f32 v[90:91], v[88:89], s[40:41] op_sel_hi:[0,1]
	v_pk_fma_f32 v[90:91], v[86:87], s[38:39], v[90:91] op_sel_hi:[0,1,1] neg_lo:[0,0,1] neg_hi:[0,0,1]
	v_pk_add_f32 v[54:55], v[54:55], v[90:91]
	v_pk_mul_f32 v[90:91], v[88:89], s[52:53] op_sel_hi:[0,1]
	v_pk_fma_f32 v[90:91], v[86:87], s[42:43], v[90:91] op_sel_hi:[0,1,1] neg_lo:[0,0,1] neg_hi:[0,0,1]
	v_pk_add_f32 v[52:53], v[52:53], v[90:91]
	v_pk_mul_f32 v[90:91], v[88:89], s[56:57] op_sel_hi:[0,1]
	v_pk_fma_f32 v[90:91], v[86:87], s[54:55], v[90:91] op_sel_hi:[0,1,1] neg_lo:[0,0,1] neg_hi:[0,0,1]
	v_pk_add_f32 v[50:51], v[50:51], v[90:91]
	v_pk_mul_f32 v[90:91], v[88:89], s[62:63] op_sel_hi:[0,1]
	v_pk_fma_f32 v[90:91], v[86:87], s[58:59], v[90:91] op_sel_hi:[0,1,1] neg_lo:[0,0,1] neg_hi:[0,0,1]
	v_pk_add_f32 v[58:59], v[58:59], v[90:91]
	v_pk_mul_f32 v[90:91], v[88:89], s[80:81] op_sel_hi:[0,1]
	v_pk_fma_f32 v[90:91], v[86:87], s[64:65], v[90:91] op_sel_hi:[0,1,1] neg_lo:[0,0,1] neg_hi:[0,0,1]
	v_pk_add_f32 v[60:61], v[60:61], v[90:91]
	v_pk_mul_f32 v[90:91], v[88:89], s[84:85] op_sel_hi:[0,1]
	v_pk_fma_f32 v[90:91], v[86:87], s[82:83], v[90:91] op_sel_hi:[0,1,1] neg_lo:[0,0,1] neg_hi:[0,0,1]
	v_pk_add_f32 v[64:65], v[64:65], v[90:91]
	v_pk_mul_f32 v[90:91], v[88:89], s[88:89] op_sel_hi:[0,1]
	v_pk_fma_f32 v[90:91], v[86:87], s[86:87], v[90:91] op_sel_hi:[0,1,1] neg_lo:[0,0,1] neg_hi:[0,0,1]
	v_pk_add_f32 v[62:63], v[62:63], v[90:91]
	s_waitcnt vmcnt(0)
; __device__ __forceinline__ void ph1_small(const Args& a, int tid, int wave, int lane, int G, int bid) {
;     ...
; #pragma unroll 8
;             for (int n = 0; n < 64; ++n) { const float cr = cre[((size_t)g * 16 + p) * 64 + n], ci = cim[((size_t)g * 16 + p) * 64 + n];
;                 const float pr = POW[(((size_t)g * 65 + tau) * 64 + n) * 2], pi = POW[(((size_t)g * 65 + tau) * 64 + n) * 2 + 1];
;                 const float er = cr * pr - ci * pi, ei = cr * pi + ci * pr;
;                 const f32x4* bp = (const f32x4*)(BBAR + ((size_t)g * 64 + n) * 32);
; #pragma unroll
;                 for (int q = 0; q < 8; ++q) { const f32x4 bb = bp[q]; s[2 * q] += er * bb[0] - ei * bb[1]; s[2 * q + 1] += er * bb[2] - ei * bb[3]; } }
	v_readlane_b32 s16, v16, 0
	v_readlane_b32 s17, v16, 2
	v_readlane_b32 s36, v16, 1
	v_readlane_b32 s37, v16, 3
	v_readlane_b32 s38, v16, 4
	v_readlane_b32 s39, v16, 6
	v_readlane_b32 s40, v16, 5
	v_readlane_b32 s41, v16, 7
	v_readlane_b32 s42, v16, 8
	v_readlane_b32 s43, v16, 10
	v_readlane_b32 s52, v16, 9
	v_readlane_b32 s53, v16, 11
	v_readlane_b32 s54, v16, 12
	v_readlane_b32 s55, v16, 14
	v_readlane_b32 s56, v16, 13
	v_readlane_b32 s57, v16, 15
	v_readlane_b32 s58, v16, 16
	v_readlane_b32 s59, v16, 18
	v_readlane_b32 s62, v16, 17
	v_readlane_b32 s63, v16, 19
	v_readlane_b32 s64, v16, 20
	v_readlane_b32 s65, v16, 22
	v_readlane_b32 s80, v16, 21
	v_readlane_b32 s81, v16, 23
	v_readlane_b32 s82, v16, 24
	v_readlane_b32 s83, v16, 26
	v_readlane_b32 s84, v16, 25
	v_readlane_b32 s85, v16, 27
	v_readlane_b32 s86, v16, 28
	v_readlane_b32 s87, v16, 30
	v_readlane_b32 s88, v16, 29
	v_readlane_b32 s89, v16, 31
	v_mul_f32_e32 v244, v70, v78
	v_mul_f32_e32 v245, v74, v79
	v_sub_f32_e32 v86, v244, v245
	v_mul_f32_e32 v244, v74, v78
	v_mul_f32_e32 v245, v70, v79
	v_add_f32_e32 v88, v244, v245
	v_pk_mul_f32 v[90:91], v[88:89], s[36:37] op_sel_hi:[0,1]
	v_pk_fma_f32 v[90:91], v[86:87], s[16:17], v[90:91] op_sel_hi:[0,1,1] neg_lo:[0,0,1] neg_hi:[0,0,1]
	v_pk_add_f32 v[56:57], v[56:57], v[90:91]
	v_pk_mul_f32 v[90:91], v[88:89], s[40:41] op_sel_hi:[0,1]
	v_pk_fma_f32 v[90:91], v[86:87], s[38:39], v[90:91] op_sel_hi:[0,1,1] neg_lo:[0,0,1] neg_hi:[0,0,1]
	v_pk_add_f32 v[54:55], v[54:55], v[90:91]
	v_pk_mul_f32 v[90:91], v[88:89], s[52:53] op_sel_hi:[0,1]
	v_pk_fma_f32 v[90:91], v[86:87], s[42:43], v[90:91] op_sel_hi:[0,1,1] neg_lo:[0,0,1] neg_hi:[0,0,1]
	v_pk_add_f32 v[52:53], v[52:53], v[90:91]
	v_pk_mul_f32 v[90:91], v[88:89], s[56:57] op_sel_hi:[0,1]
	v_pk_fma_f32 v[90:91], v[86:87], s[54:55], v[90:91] op_sel_hi:[0,1,1] neg_lo:[0,0,1] neg_hi:[0,0,1]
	v_pk_add_f32 v[50:51], v[50:51], v[90:91]
	v_pk_mul_f32 v[90:91], v[88:89], s[62:63] op_sel_hi:[0,1]
	v_pk_fma_f32 v[90:91], v[86:87], s[58:59], v[90:91] op_sel_hi:[0,1,1] neg_lo:[0,0,1] neg_hi:[0,0,1]
	v_pk_add_f32 v[58:59], v[58:59], v[90:91]
	v_pk_mul_f32 v[90:91], v[88:89], s[80:81] op_sel_hi:[0,1]
	v_pk_fma_f32 v[90:91], v[86:87], s[64:65], v[90:91] op_sel_hi:[0,1,1] neg_lo:[0,0,1] neg_hi:[0,0,1]
	v_pk_add_f32 v[60:61], v[60:61], v[90:91]
	v_pk_mul_f32 v[90:91], v[88:89], s[84:85] op_sel_hi:[0,1]
	v_pk_fma_f32 v[90:91], v[86:87], s[82:83], v[90:91] op_sel_hi:[0,1,1] neg_lo:[0,0,1] neg_hi:[0,0,1]
	v_pk_add_f32 v[64:65], v[64:65], v[90:91]
	v_pk_mul_f32 v[90:91], v[88:89], s[88:89] op_sel_hi:[0,1]
	v_pk_fma_f32 v[90:91], v[86:87], s[86:87], v[90:91] op_sel_hi:[0,1,1] neg_lo:[0,0,1] neg_hi:[0,0,1]
	v_pk_add_f32 v[62:63], v[62:63], v[90:91]
	v_readlane_b32 s16, v16, 32
	v_readlane_b32 s17, v16, 34
	v_readlane_b32 s36, v16, 33
	v_readlane_b32 s37, v16, 35
	v_readlane_b32 s38, v16, 36
	v_readlane_b32 s39, v16, 38
	v_readlane_b32 s40, v16, 37
	v_readlane_b32 s41, v16, 39
	v_readlane_b32 s42, v16, 40
	v_readlane_b32 s43, v16, 42
	v_readlane_b32 s52, v16, 41
	v_readlane_b32 s53, v16, 43
	v_readlane_b32 s54, v16, 44
	v_readlane_b32 s55, v16, 46
	v_readlane_b32 s56, v16, 45
	v_readlane_b32 s57, v16, 47
	v_readlane_b32 s58, v16, 48
	v_readlane_b32 s59, v16, 50
	v_readlane_b32 s62, v16, 49
	v_readlane_b32 s63, v16, 51
	v_readlane_b32 s64, v16, 52
	v_readlane_b32 s65, v16, 54
	v_readlane_b32 s80, v16, 53
	v_readlane_b32 s81, v16, 55
	v_readlane_b32 s82, v16, 56
	v_readlane_b32 s83, v16, 58
	v_readlane_b32 s84, v16, 57
	v_readlane_b32 s85, v16, 59
	v_readlane_b32 s86, v16, 60
	v_readlane_b32 s87, v16, 62
	v_readlane_b32 s88, v16, 61
	v_readlane_b32 s89, v16, 63
	v_mul_f32_e32 v244, v71, v80
	v_mul_f32_e32 v245, v75, v81
	v_sub_f32_e32 v86, v244, v245
	v_mul_f32_e32 v244, v75, v80
	v_mul_f32_e32 v245, v71, v81
	v_add_f32_e32 v88, v244, v245
	v_pk_mul_f32 v[90:91], v[88:89], s[36:37] op_sel_hi:[0,1]
	v_pk_fma_f32 v[90:91], v[86:87], s[16:17], v[90:91] op_sel_hi:[0,1,1] neg_lo:[0,0,1] neg_hi:[0,0,1]
	v_pk_add_f32 v[56:57], v[56:57], v[90:91]
	v_pk_mul_f32 v[90:91], v[88:89], s[40:41] op_sel_hi:[0,1]
	v_pk_fma_f32 v[90:91], v[86:87], s[38:39], v[90:91] op_sel_hi:[0,1,1] neg_lo:[0,0,1] neg_hi:[0,0,1]
	v_pk_add_f32 v[54:55], v[54:55], v[90:91]
	v_pk_mul_f32 v[90:91], v[88:89], s[52:53] op_sel_hi:[0,1]
	v_pk_fma_f32 v[90:91], v[86:87], s[42:43], v[90:91] op_sel_hi:[0,1,1] neg_lo:[0,0,1] neg_hi:[0,0,1]
	v_pk_add_f32 v[52:53], v[52:53], v[90:91]
	v_pk_mul_f32 v[90:91], v[88:89], s[56:57] op_sel_hi:[0,1]
	v_pk_fma_f32 v[90:91], v[86:87], s[54:55], v[90:91] op_sel_hi:[0,1,1] neg_lo:[0,0,1] neg_hi:[0,0,1]
	v_pk_add_f32 v[50:51], v[50:51], v[90:91]
	v_pk_mul_f32 v[90:91], v[88:89], s[62:63] op_sel_hi:[0,1]
	v_pk_fma_f32 v[90:91], v[86:87], s[58:59], v[90:91] op_sel_hi:[0,1,1] neg_lo:[0,0,1] neg_hi:[0,0,1]
	v_pk_add_f32 v[58:59], v[58:59], v[90:91]
	v_pk_mul_f32 v[90:91], v[88:89], s[80:81] op_sel_hi:[0,1]
	v_pk_fma_f32 v[90:91], v[86:87], s[64:65], v[90:91] op_sel_hi:[0,1,1] neg_lo:[0,0,1] neg_hi:[0,0,1]
	v_pk_add_f32 v[60:61], v[60:61], v[90:91]
	v_pk_mul_f32 v[90:91], v[88:89], s[84:85] op_sel_hi:[0,1]
	v_pk_fma_f32 v[90:91], v[86:87], s[82:83], v[90:91] op_sel_hi:[0,1,1] neg_lo:[0,0,1] neg_hi:[0,0,1]
	v_pk_add_f32 v[64:65], v[64:65], v[90:91]
	v_pk_mul_f32 v[90:91], v[88:89], s[88:89] op_sel_hi:[0,1]
	v_pk_fma_f32 v[90:91], v[86:87], s[86:87], v[90:91] op_sel_hi:[0,1,1] neg_lo:[0,0,1] neg_hi:[0,0,1]
	v_pk_add_f32 v[62:63], v[62:63], v[90:91]
	v_readlane_b32 s16, v17, 0
	v_readlane_b32 s17, v17, 2
	v_readlane_b32 s36, v17, 1
	v_readlane_b32 s37, v17, 3
	v_readlane_b32 s38, v17, 4
	v_readlane_b32 s39, v17, 6
; __device__ __forceinline__ void ph1_small(const Args& a, int tid, int wave, int lane, int G, int bid) {
;     ...
; #pragma unroll 8
;             for (int n = 0; n < 64; ++n) { const float cr = cre[((size_t)g * 16 + p) * 64 + n], ci = cim[((size_t)g * 16 + p) * 64 + n];
;                 const float pr = POW[(((size_t)g * 65 + tau) * 64 + n) * 2], pi = POW[(((size_t)g * 65 + tau) * 64 + n) * 2 + 1];
;                 const float er = cr * pr - ci * pi, ei = cr * pi + ci * pr;
;                 const f32x4* bp = (const f32x4*)(BBAR + ((size_t)g * 64 + n) * 32);
; #pragma unroll
;                 for (int q = 0; q < 8; ++q) { const f32x4 bb = bp[q]; s[2 * q] += er * bb[0] - ei * bb[1]; s[2 * q + 1] += er * bb[2] - ei * bb[3]; } }
;             { const float dv = (tau == 0) ? a.in[I_SD][g * 16 + p] : 0.0f;
; #pragma unroll
;               for (int q = 0; q < 16; ++q) s[q] += (q == p) ? dv : 0.0f; }
	v_readlane_b32 s40, v17, 5
	v_readlane_b32 s41, v17, 7
	v_readlane_b32 s42, v17, 8
	v_readlane_b32 s43, v17, 10
	v_readlane_b32 s52, v17, 9
	v_readlane_b32 s53, v17, 11
	v_readlane_b32 s54, v17, 12
	v_readlane_b32 s55, v17, 14
	v_readlane_b32 s56, v17, 13
	v_readlane_b32 s57, v17, 15
	v_readlane_b32 s58, v17, 16
	v_readlane_b32 s59, v17, 18
	v_readlane_b32 s62, v17, 17
	v_readlane_b32 s63, v17, 19
	v_readlane_b32 s64, v17, 20
	v_readlane_b32 s65, v17, 22
	v_readlane_b32 s80, v17, 21
	v_readlane_b32 s81, v17, 23
	v_readlane_b32 s82, v17, 24
	v_readlane_b32 s83, v17, 26
	v_readlane_b32 s84, v17, 25
	v_readlane_b32 s85, v17, 27
	v_readlane_b32 s86, v17, 28
	v_readlane_b32 s87, v17, 30
	v_readlane_b32 s88, v17, 29
	v_readlane_b32 s89, v17, 31
	v_mul_f32_e32 v244, v72, v82
	v_mul_f32_e32 v245, v76, v83
	v_sub_f32_e32 v86, v244, v245
	v_mul_f32_e32 v244, v76, v82
	v_mul_f32_e32 v245, v72, v83
	v_add_f32_e32 v88, v244, v245
	v_pk_mul_f32 v[90:91], v[88:89], s[36:37] op_sel_hi:[0,1]
	v_pk_fma_f32 v[90:91], v[86:87], s[16:17], v[90:91] op_sel_hi:[0,1,1] neg_lo:[0,0,1] neg_hi:[0,0,1]
	v_pk_add_f32 v[56:57], v[56:57], v[90:91]
	v_pk_mul_f32 v[90:91], v[88:89], s[40:41] op_sel_hi:[0,1]
	v_pk_fma_f32 v[90:91], v[86:87], s[38:39], v[90:91] op_sel_hi:[0,1,1] neg_lo:[0,0,1] neg_hi:[0,0,1]
	v_pk_add_f32 v[54:55], v[54:55], v[90:91]
	v_pk_mul_f32 v[90:91], v[88:89], s[52:53] op_sel_hi:[0,1]
	v_pk_fma_f32 v[90:91], v[86:87], s[42:43], v[90:91] op_sel_hi:[0,1,1] neg_lo:[0,0,1] neg_hi:[0,0,1]
	v_pk_add_f32 v[52:53], v[52:53], v[90:91]
	v_pk_mul_f32 v[90:91], v[88:89], s[56:57] op_sel_hi:[0,1]
	v_pk_fma_f32 v[90:91], v[86:87], s[54:55], v[90:91] op_sel_hi:[0,1,1] neg_lo:[0,0,1] neg_hi:[0,0,1]
	v_pk_add_f32 v[50:51], v[50:51], v[90:91]
	v_pk_mul_f32 v[90:91], v[88:89], s[62:63] op_sel_hi:[0,1]
	v_pk_fma_f32 v[90:91], v[86:87], s[58:59], v[90:91] op_sel_hi:[0,1,1] neg_lo:[0,0,1] neg_hi:[0,0,1]
	v_pk_add_f32 v[58:59], v[58:59], v[90:91]
	v_pk_mul_f32 v[90:91], v[88:89], s[80:81] op_sel_hi:[0,1]
	v_pk_fma_f32 v[90:91], v[86:87], s[64:65], v[90:91] op_sel_hi:[0,1,1] neg_lo:[0,0,1] neg_hi:[0,0,1]
	v_pk_add_f32 v[60:61], v[60:61], v[90:91]
	v_pk_mul_f32 v[90:91], v[88:89], s[84:85] op_sel_hi:[0,1]
	v_pk_fma_f32 v[90:91], v[86:87], s[82:83], v[90:91] op_sel_hi:[0,1,1] neg_lo:[0,0,1] neg_hi:[0,0,1]
	v_pk_add_f32 v[64:65], v[64:65], v[90:91]
	v_pk_mul_f32 v[90:91], v[88:89], s[88:89] op_sel_hi:[0,1]
	v_pk_fma_f32 v[90:91], v[86:87], s[86:87], v[90:91] op_sel_hi:[0,1,1] neg_lo:[0,0,1] neg_hi:[0,0,1]
	v_pk_add_f32 v[62:63], v[62:63], v[90:91]
	v_readlane_b32 s16, v17, 32
	v_readlane_b32 s17, v17, 34
	v_readlane_b32 s36, v17, 33
	v_readlane_b32 s37, v17, 35
	v_readlane_b32 s38, v17, 36
	v_readlane_b32 s39, v17, 38
	v_readlane_b32 s40, v17, 37
	v_readlane_b32 s41, v17, 39
	v_readlane_b32 s42, v17, 40
	v_readlane_b32 s43, v17, 42
	v_readlane_b32 s52, v17, 41
	v_readlane_b32 s53, v17, 43
	v_readlane_b32 s54, v17, 44
	v_readlane_b32 s55, v17, 46
	v_readlane_b32 s56, v17, 45
	v_readlane_b32 s57, v17, 47
	v_readlane_b32 s58, v17, 48
	v_readlane_b32 s59, v17, 50
	v_readlane_b32 s62, v17, 49
	v_readlane_b32 s63, v17, 51
	v_readlane_b32 s64, v17, 52
	v_readlane_b32 s65, v17, 54
	v_readlane_b32 s80, v17, 53
	v_readlane_b32 s81, v17, 55
	v_readlane_b32 s82, v17, 56
	v_readlane_b32 s83, v17, 58
	v_readlane_b32 s84, v17, 57
	v_readlane_b32 s85, v17, 59
	v_readlane_b32 s86, v17, 60
	v_readlane_b32 s87, v17, 62
	v_readlane_b32 s88, v17, 61
	v_readlane_b32 s89, v17, 63
	v_mul_f32_e32 v244, v73, v84
	v_mul_f32_e32 v245, v77, v85
	v_sub_f32_e32 v86, v244, v245
	v_mul_f32_e32 v244, v77, v84
	v_mul_f32_e32 v245, v73, v85
	v_add_f32_e32 v88, v244, v245
	v_pk_mul_f32 v[90:91], v[88:89], s[36:37] op_sel_hi:[0,1]
	v_pk_fma_f32 v[90:91], v[86:87], s[16:17], v[90:91] op_sel_hi:[0,1,1] neg_lo:[0,0,1] neg_hi:[0,0,1]
	v_pk_add_f32 v[56:57], v[56:57], v[90:91]
	v_pk_mul_f32 v[90:91], v[88:89], s[40:41] op_sel_hi:[0,1]
	v_pk_fma_f32 v[90:91], v[86:87], s[38:39], v[90:91] op_sel_hi:[0,1,1] neg_lo:[0,0,1] neg_hi:[0,0,1]
	v_pk_add_f32 v[54:55], v[54:55], v[90:91]
	v_pk_mul_f32 v[90:91], v[88:89], s[52:53] op_sel_hi:[0,1]
	v_pk_fma_f32 v[90:91], v[86:87], s[42:43], v[90:91] op_sel_hi:[0,1,1] neg_lo:[0,0,1] neg_hi:[0,0,1]
	v_pk_add_f32 v[52:53], v[52:53], v[90:91]
	v_pk_mul_f32 v[90:91], v[88:89], s[56:57] op_sel_hi:[0,1]
	v_pk_fma_f32 v[90:91], v[86:87], s[54:55], v[90:91] op_sel_hi:[0,1,1] neg_lo:[0,0,1] neg_hi:[0,0,1]
	v_pk_add_f32 v[50:51], v[50:51], v[90:91]
	v_pk_mul_f32 v[90:91], v[88:89], s[62:63] op_sel_hi:[0,1]
	v_pk_fma_f32 v[90:91], v[86:87], s[58:59], v[90:91] op_sel_hi:[0,1,1] neg_lo:[0,0,1] neg_hi:[0,0,1]
	v_pk_add_f32 v[58:59], v[58:59], v[90:91]
	v_pk_mul_f32 v[90:91], v[88:89], s[80:81] op_sel_hi:[0,1]
	v_pk_fma_f32 v[90:91], v[86:87], s[64:65], v[90:91] op_sel_hi:[0,1,1] neg_lo:[0,0,1] neg_hi:[0,0,1]
	v_pk_add_f32 v[60:61], v[60:61], v[90:91]
	v_pk_mul_f32 v[90:91], v[88:89], s[84:85] op_sel_hi:[0,1]
	v_pk_fma_f32 v[90:91], v[86:87], s[82:83], v[90:91] op_sel_hi:[0,1,1] neg_lo:[0,0,1] neg_hi:[0,0,1]
	v_pk_add_f32 v[64:65], v[64:65], v[90:91]
	v_pk_mul_f32 v[90:91], v[88:89], s[88:89] op_sel_hi:[0,1]
	v_pk_fma_f32 v[90:91], v[86:87], s[86:87], v[90:91] op_sel_hi:[0,1,1] neg_lo:[0,0,1] neg_hi:[0,0,1]
	v_pk_add_f32 v[62:63], v[62:63], v[90:91]
	s_add_u32 s98, s98, 0x1000
	s_addc_u32 s99, s99, 0
	v_add_co_u32_e32 v44, vcc, 0x80, v44
	s_nop 0
	v_addc_co_u32_e32 v45, vcc, 0, v45, vcc
	v_add_co_u32_e32 v42, vcc, 0x80, v42
	s_nop 0
	v_addc_co_u32_e32 v43, vcc, 0, v43, vcc
	v_add_u32_e32 v40, 0x100, v40
	s_add_i32 s32, s32, -1
	s_cmp_lg_u32 s32, 0
	s_cbranch_scc1 .Lkta_half
	v_and_b32_e32 v2, 31, v69
	v_cmp_eq_u32_e32 vcc, 0, v2
	v_mov_b32_e32 v3, 0
	s_and_saveexec_b64 s[48:49], vcc
	s_cbranch_execz .LBB0_106
	v_lshl_or_b32 v4, v36, 4, v160
	v_readlane_b32 s0, v250, 33
	v_ashrrev_i32_e32 v5, 31, v4
	v_readlane_b32 s14, v250, 47
	v_readlane_b32 s15, v250, 48
	v_readlane_b32 s1, v250, 34
	v_readlane_b32 s2, v250, 35
	v_lshl_add_u64 v[4:5], v[4:5], 2, s[14:15]
	global_load_dword v3, v[4:5], off
	v_readlane_b32 s3, v250, 36
	v_readlane_b32 s4, v250, 37
	v_readlane_b32 s5, v250, 38
	v_readlane_b32 s6, v250, 39
	v_readlane_b32 s7, v250, 40
	v_readlane_b32 s8, v250, 41
	v_readlane_b32 s9, v250, 42
	v_readlane_b32 s10, v250, 43
	v_readlane_b32 s11, v250, 44
	v_readlane_b32 s12, v250, 45
	v_readlane_b32 s13, v250, 46
	s_branch .LBB0_106
; __device__ __forceinline__ void ph1_small(const Args& a, int tid, int wave, int lane, int G, int bid) {
;     ...
;         const float* cre = a.in[I_CRE]; const float* cim = a.in[I_CIM]; const float* BBAR = (const float*)(a.ws + WS_BBAR); const float* POW = (const float*)(a.ws + WS_POW); float* KT = (float*)(a.ws + WS_KT);
;         for (int idx = (tid < 128 ? bid * 128 + tid : SSMG * SL * 16); idx < SSMG * SL * 16; idx += G * 128) {
.Lkta_restore:
	v_readlane_b32 s16, v249, 0
	v_readlane_b32 s17, v249, 1
	v_readlane_b32 s36, v249, 2
	v_readlane_b32 s37, v249, 3
	v_readlane_b32 s38, v249, 4
	v_readlane_b32 s39, v249, 5
	v_readlane_b32 s40, v249, 6
	v_readlane_b32 s41, v249, 7
	v_readlane_b32 s42, v249, 8
	v_readlane_b32 s43, v249, 9
	v_readlane_b32 s52, v249, 10
	v_readlane_b32 s53, v249, 11
	v_readlane_b32 s54, v249, 12
	v_readlane_b32 s55, v249, 13
	v_readlane_b32 s56, v249, 14
	v_readlane_b32 s57, v249, 15
	v_readlane_b32 s58, v249, 16
	v_readlane_b32 s59, v249, 17
	v_readlane_b32 s62, v249, 18
	v_readlane_b32 s63, v249, 19
	v_readlane_b32 s64, v249, 20
	v_readlane_b32 s65, v249, 21
	v_readlane_b32 s80, v249, 22
	v_readlane_b32 s81, v249, 23
	v_readlane_b32 s82, v249, 24
	v_readlane_b32 s83, v249, 25
	v_readlane_b32 s84, v249, 26
	v_readlane_b32 s85, v249, 27
	v_readlane_b32 s86, v249, 28
	v_readlane_b32 s87, v249, 29
	v_readlane_b32 s88, v249, 30
	v_readlane_b32 s89, v249, 31
	s_nop 4

; __device__ __forceinline__ void ph1_small(const Args& a, int tid, int wave, int lane, int G, int bid) {
;     ...
;         const float* cre = a.in[I_CRE]; const float* cim = a.in[I_CIM]; const float* BBAR = (const float*)(a.ws + WS_BBAR); const float* POW = (const float*)(a.ws + WS_POW); float* KT = (float*)(a.ws + WS_KT);
;         for (int idx = (tid < 128 ? bid * 128 + tid : SSMG * SL * 16); idx < SSMG * SL * 16; idx += G * 128) {
.LBB0_320:
	v_readlane_b32 s0, v251, 15
	v_readlane_b32 s1, v251, 16
	s_and_saveexec_b64 s[36:37], s[0:1]
	s_cbranch_execz .LBB0_327
	v_writelane_b32 v249, s16, 0
	v_writelane_b32 v249, s17, 1
	v_writelane_b32 v249, s44, 2
	v_writelane_b32 v249, s45, 3
	v_writelane_b32 v249, s46, 4
	v_writelane_b32 v249, s47, 5
	v_writelane_b32 v249, s48, 6
	v_writelane_b32 v249, s49, 7
	v_writelane_b32 v249, s52, 8
	v_writelane_b32 v249, s53, 9
	v_writelane_b32 v249, s54, 10
	v_writelane_b32 v249, s55, 11
	v_writelane_b32 v249, s56, 12
	v_writelane_b32 v249, s57, 13
	v_writelane_b32 v249, s58, 14
	v_writelane_b32 v249, s59, 15
	v_writelane_b32 v249, s62, 16
	v_writelane_b32 v249, s63, 17
	v_writelane_b32 v249, s64, 18
	v_writelane_b32 v249, s65, 19
	v_writelane_b32 v249, s68, 20
	v_writelane_b32 v249, s69, 21
	v_writelane_b32 v249, s70, 22
	v_writelane_b32 v249, s71, 23
	v_writelane_b32 v249, s72, 24
	v_writelane_b32 v249, s73, 25
	v_writelane_b32 v249, s80, 26
	v_writelane_b32 v249, s81, 27
	v_writelane_b32 v249, s82, 28
	v_writelane_b32 v249, s83, 29
	v_writelane_b32 v249, s84, 30
	v_writelane_b32 v249, s85, 31
	v_readlane_b32 s0, v250, 33
	v_lshlrev_b32_e32 v30, 8, v160
	v_mov_b32_e32 v31, 0
	v_readlane_b32 s10, v250, 43
	v_readlane_b32 s11, v250, 44
	v_readlane_b32 s12, v250, 45
	v_readlane_b32 s13, v250, 46
	v_lshl_add_u64 v[34:35], s[10:11], 0, v[30:31]
	s_mov_b64 s[38:39], 0
	v_lshl_add_u64 v[32:33], s[12:13], 0, v[30:31]
	v_readlane_b32 s1, v250, 34
	v_readlane_b32 s2, v250, 35
	v_readlane_b32 s3, v250, 36
	v_readlane_b32 s4, v250, 37
	v_readlane_b32 s5, v250, 38
	v_readlane_b32 s6, v250, 39
	v_readlane_b32 s7, v250, 40
	v_readlane_b32 s8, v250, 41
	v_readlane_b32 s9, v250, 42
	v_readlane_b32 s14, v250, 47
	v_readlane_b32 s15, v250, 48
	s_branch .LBB0_323

; __device__ __forceinline__ void ph1_small(const Args& a, int tid, int wave, int lane, int G, int bid) {
;     ...
;         for (int idx = (tid < 128 ? bid * 128 + tid : SSMG * SL * 16); idx < SSMG * SL * 16; idx += G * 128) {
;             const int g = idx >> 9, tau = (idx >> 4) & 31, p = idx & 15; float s[16];
; #pragma unroll
;             for (int q = 0; q < 16; ++q) s[q] = 0.f;
; #pragma unroll 8
;             for (int n = 0; n < 64; ++n) { const float cr = cre[((size_t)g * 16 + p) * 64 + n], ci = cim[((size_t)g * 16 + p) * 64 + n];
;                 const float pr = POW[(((size_t)g * 65 + tau) * 64 + n) * 2], pi = POW[(((size_t)g * 65 + tau) * 64 + n) * 2 + 1];
;                 const float er = cr * pr - ci * pi, ei = cr * pi + ci * pr;
;                 const f32x4* bp = (const f32x4*)(BBAR + ((size_t)g * 64 + n) * 32);
; #pragma unroll
;                 for (int q = 0; q < 8; ++q) { const f32x4 bb = bp[q]; s[2 * q] += er * bb[0] - ei * bb[1]; s[2 * q + 1] += er * bb[2] - ei * bb[3]; } }
.LBB0_323:
	v_ashrrev_i32_e32 v36, 9, v159
	v_bfe_u32 v30, v159, 4, 5
	v_mul_hi_i32_i24_e32 v3, 0x41, v36
	v_mul_i32_i24_e32 v2, 0x41, v36
	v_ashrrev_i32_e32 v37, 31, v36
	v_lshl_add_u64 v[2:3], v[2:3], 0, v[30:31]
	v_lshlrev_b64 v[40:41], 9, v[2:3]
	v_lshlrev_b64 v[2:3], 12, v[36:37]
	v_lshrrev_b32_e32 v66, 4, v159
	v_lshlrev_b64 v[38:39], 13, v[36:37]
	v_lshl_add_u64 v[42:43], v[32:33], 0, v[2:3]
	v_lshl_add_u64 v[44:45], v[34:35], 0, v[2:3]
	s_mov_b64 s[40:41], 0
	v_mov_b32_e32 v62, 0
	v_mov_b32_e32 v63, v31
	v_mov_b32_e32 v56, 0
	v_mov_b32_e32 v57, v31
	v_mov_b32_e32 v54, 0
	v_mov_b32_e32 v55, v31
	v_mov_b32_e32 v52, 0
	v_mov_b32_e32 v53, v31
	v_mov_b32_e32 v50, 0
	v_mov_b32_e32 v51, v31
	v_mov_b32_e32 v58, 0
	v_mov_b32_e32 v59, v31
	v_mov_b32_e32 v60, 0
	v_mov_b32_e32 v61, v31
	v_mov_b32_e32 v64, 0
	v_mov_b32_e32 v65, v31
	v_readlane_b32 s98, v250, 53
	v_readlane_b32 s99, v250, 54
	v_readfirstlane_b32 s16, v38
	v_readlane_b32 s100, v250, 53
	v_readlane_b32 s101, v250, 54
	s_add_u32 s98, s98, s16
	s_addc_u32 s99, s99, 0
	s_add_u32 s98, s98, 0x500000
	s_addc_u32 s99, s99, 0
	s_add_u32 s100, s100, 0x600000
	s_addc_u32 s101, s101, 0
	v_mbcnt_lo_u32_b32 v246, -1, 0
	v_mbcnt_hi_u32_b32 v246, -1, v246
	v_lshlrev_b32_e32 v246, 2, v246
	s_mov_b32 s32, 2
.Lktb_half:
	global_load_dword v2, v246, s[98:99] offset:0
	global_load_dword v3, v246, s[98:99] offset:256
	global_load_dword v4, v246, s[98:99] offset:512
	global_load_dword v5, v246, s[98:99] offset:768
	global_load_dword v6, v246, s[98:99] offset:1024
	global_load_dword v7, v246, s[98:99] offset:1280
	global_load_dword v8, v246, s[98:99] offset:1536
	global_load_dword v9, v246, s[98:99] offset:1792
	global_load_dword v10, v246, s[98:99] offset:2048
	global_load_dword v11, v246, s[98:99] offset:2304
	global_load_dword v12, v246, s[98:99] offset:2560
	global_load_dword v13, v246, s[98:99] offset:2816
	global_load_dword v14, v246, s[98:99] offset:3072
	global_load_dword v15, v246, s[98:99] offset:3328
	global_load_dword v16, v246, s[98:99] offset:3584
	global_load_dword v17, v246, s[98:99] offset:3840
	global_load_dwordx4 v[18:21], v[44:45], off offset:0
	global_load_dwordx4 v[22:25], v[42:43], off offset:0
	global_load_dwordx4 v[26:29], v40, s[100:101] offset:0
	global_load_dwordx4 v[46:49], v40, s[100:101] offset:16
	global_load_dwordx4 v[70:73], v[44:45], off offset:16
	global_load_dwordx4 v[74:77], v[42:43], off offset:16
	global_load_dwordx4 v[78:81], v40, s[100:101] offset:32
	global_load_dwordx4 v[82:85], v40, s[100:101] offset:48
	s_waitcnt vmcnt(4)
	v_readlane_b32 s16, v2, 0
	v_readlane_b32 s17, v2, 2
	v_readlane_b32 s44, v2, 1
	v_readlane_b32 s45, v2, 3
	v_readlane_b32 s46, v2, 4
	v_readlane_b32 s47, v2, 6
	v_readlane_b32 s48, v2, 5
	v_readlane_b32 s49, v2, 7
	v_readlane_b32 s52, v2, 8
	v_readlane_b32 s53, v2, 10
	v_readlane_b32 s54, v2, 9
	v_readlane_b32 s55, v2, 11
	v_readlane_b32 s56, v2, 12
	v_readlane_b32 s57, v2, 14
	v_readlane_b32 s58, v2, 13
	v_readlane_b32 s59, v2, 15
	v_readlane_b32 s62, v2, 16
	v_readlane_b32 s63, v2, 18
	v_readlane_b32 s64, v2, 17
	v_readlane_b32 s65, v2, 19
	v_readlane_b32 s68, v2, 20
	v_readlane_b32 s69, v2, 22
	v_readlane_b32 s70, v2, 21
	v_readlane_b32 s71, v2, 23
	v_readlane_b32 s72, v2, 24
	v_readlane_b32 s73, v2, 26
	v_readlane_b32 s80, v2, 25
	v_readlane_b32 s81, v2, 27
	v_readlane_b32 s82, v2, 28
	v_readlane_b32 s83, v2, 30
	v_readlane_b32 s84, v2, 29
	v_readlane_b32 s85, v2, 31
	v_mul_f32_e32 v244, v18, v26
	v_mul_f32_e32 v245, v22, v27
	v_sub_f32_e32 v86, v244, v245
	v_mul_f32_e32 v244, v22, v26
	v_mul_f32_e32 v245, v18, v27
	v_add_f32_e32 v88, v244, v245
	v_pk_mul_f32 v[90:91], v[88:89], s[44:45] op_sel_hi:[0,1]
	v_pk_fma_f32 v[90:91], v[86:87], s[16:17], v[90:91] op_sel_hi:[0,1,1] neg_lo:[0,0,1] neg_hi:[0,0,1]
	v_pk_add_f32 v[56:57], v[56:57], v[90:91]
	v_pk_mul_f32 v[90:91], v[88:89], s[48:49] op_sel_hi:[0,1]
	v_pk_fma_f32 v[90:91], v[86:87], s[46:47], v[90:91] op_sel_hi:[0,1,1] neg_lo:[0,0,1] neg_hi:[0,0,1]
	v_pk_add_f32 v[54:55], v[54:55], v[90:91]
	v_pk_mul_f32 v[90:91], v[88:89], s[54:55] op_sel_hi:[0,1]
	v_pk_fma_f32 v[90:91], v[86:87], s[52:53], v[90:91] op_sel_hi:[0,1,1] neg_lo:[0,0,1] neg_hi:[0,0,1]
	v_pk_add_f32 v[52:53], v[52:53], v[90:91]
	v_pk_mul_f32 v[90:91], v[88:89], s[58:59] op_sel_hi:[0,1]
	v_pk_fma_f32 v[90:91], v[86:87], s[56:57], v[90:91] op_sel_hi:[0,1,1] neg_lo:[0,0,1] neg_hi:[0,0,1]
	v_pk_add_f32 v[50:51], v[50:51], v[90:91]
	v_pk_mul_f32 v[90:91], v[88:89], s[64:65] op_sel_hi:[0,1]
	v_pk_fma_f32 v[90:91], v[86:87], s[62:63], v[90:91] op_sel_hi:[0,1,1] neg_lo:[0,0,1] neg_hi:[0,0,1]
	v_pk_add_f32 v[58:59], v[58:59], v[90:91]
	v_pk_mul_f32 v[90:91], v[88:89], s[70:71] op_sel_hi:[0,1]
	v_pk_fma_f32 v[90:91], v[86:87], s[68:69], v[90:91] op_sel_hi:[0,1,1] neg_lo:[0,0,1] neg_hi:[0,0,1]
	v_pk_add_f32 v[60:61], v[60:61], v[90:91]
	v_pk_mul_f32 v[90:91], v[88:89], s[80:81] op_sel_hi:[0,1]
	v_pk_fma_f32 v[90:91], v[86:87], s[72:73], v[90:91] op_sel_hi:[0,1,1] neg_lo:[0,0,1] neg_hi:[0,0,1]
	v_pk_add_f32 v[64:65], v[64:65], v[90:91]
	v_pk_mul_f32 v[90:91], v[88:89], s[84:85] op_sel_hi:[0,1]
	v_pk_fma_f32 v[90:91], v[86:87], s[82:83], v[90:91] op_sel_hi:[0,1,1] neg_lo:[0,0,1] neg_hi:[0,0,1]
	v_pk_add_f32 v[62:63], v[62:63], v[90:91]
	v_readlane_b32 s16, v2, 32
	v_readlane_b32 s17, v2, 34
	v_readlane_b32 s44, v2, 33
	v_readlane_b32 s45, v2, 35
	v_readlane_b32 s46, v2, 36
	v_readlane_b32 s47, v2, 38
	v_readlane_b32 s48, v2, 37
	v_readlane_b32 s49, v2, 39
	v_readlane_b32 s52, v2, 40
	v_readlane_b32 s53, v2, 42
	v_readlane_b32 s54, v2, 41
	v_readlane_b32 s55, v2, 43
	v_readlane_b32 s56, v2, 44
	v_readlane_b32 s57, v2, 46
; __device__ __forceinline__ void ph1_small(const Args& a, int tid, int wave, int lane, int G, int bid) {
;     ...
; #pragma unroll 8
;             for (int n = 0; n < 64; ++n) { const float cr = cre[((size_t)g * 16 + p) * 64 + n], ci = cim[((size_t)g * 16 + p) * 64 + n];
;                 const float pr = POW[(((size_t)g * 65 + tau) * 64 + n) * 2], pi = POW[(((size_t)g * 65 + tau) * 64 + n) * 2 + 1];
;                 const float er = cr * pr - ci * pi, ei = cr * pi + ci * pr;
;                 const f32x4* bp = (const f32x4*)(BBAR + ((size_t)g * 64 + n) * 32);
; #pragma unroll
;                 for (int q = 0; q < 8; ++q) { const f32x4 bb = bp[q]; s[2 * q] += er * bb[0] - ei * bb[1]; s[2 * q + 1] += er * bb[2] - ei * bb[3]; } }
	v_readlane_b32 s58, v2, 45
	v_readlane_b32 s59, v2, 47
	v_readlane_b32 s62, v2, 48
	v_readlane_b32 s63, v2, 50
	v_readlane_b32 s64, v2, 49
	v_readlane_b32 s65, v2, 51
	v_readlane_b32 s68, v2, 52
	v_readlane_b32 s69, v2, 54
	v_readlane_b32 s70, v2, 53
	v_readlane_b32 s71, v2, 55
	v_readlane_b32 s72, v2, 56
	v_readlane_b32 s73, v2, 58
	v_readlane_b32 s80, v2, 57
	v_readlane_b32 s81, v2, 59
	v_readlane_b32 s82, v2, 60
	v_readlane_b32 s83, v2, 62
	v_readlane_b32 s84, v2, 61
	v_readlane_b32 s85, v2, 63
	v_mul_f32_e32 v244, v19, v28
	v_mul_f32_e32 v245, v23, v29
	v_sub_f32_e32 v86, v244, v245
	v_mul_f32_e32 v244, v23, v28
	v_mul_f32_e32 v245, v19, v29
	v_add_f32_e32 v88, v244, v245
	v_pk_mul_f32 v[90:91], v[88:89], s[44:45] op_sel_hi:[0,1]
	v_pk_fma_f32 v[90:91], v[86:87], s[16:17], v[90:91] op_sel_hi:[0,1,1] neg_lo:[0,0,1] neg_hi:[0,0,1]
	v_pk_add_f32 v[56:57], v[56:57], v[90:91]
	v_pk_mul_f32 v[90:91], v[88:89], s[48:49] op_sel_hi:[0,1]
	v_pk_fma_f32 v[90:91], v[86:87], s[46:47], v[90:91] op_sel_hi:[0,1,1] neg_lo:[0,0,1] neg_hi:[0,0,1]
	v_pk_add_f32 v[54:55], v[54:55], v[90:91]
	v_pk_mul_f32 v[90:91], v[88:89], s[54:55] op_sel_hi:[0,1]
	v_pk_fma_f32 v[90:91], v[86:87], s[52:53], v[90:91] op_sel_hi:[0,1,1] neg_lo:[0,0,1] neg_hi:[0,0,1]
	v_pk_add_f32 v[52:53], v[52:53], v[90:91]
	v_pk_mul_f32 v[90:91], v[88:89], s[58:59] op_sel_hi:[0,1]
	v_pk_fma_f32 v[90:91], v[86:87], s[56:57], v[90:91] op_sel_hi:[0,1,1] neg_lo:[0,0,1] neg_hi:[0,0,1]
	v_pk_add_f32 v[50:51], v[50:51], v[90:91]
	v_pk_mul_f32 v[90:91], v[88:89], s[64:65] op_sel_hi:[0,1]
	v_pk_fma_f32 v[90:91], v[86:87], s[62:63], v[90:91] op_sel_hi:[0,1,1] neg_lo:[0,0,1] neg_hi:[0,0,1]
	v_pk_add_f32 v[58:59], v[58:59], v[90:91]
	v_pk_mul_f32 v[90:91], v[88:89], s[70:71] op_sel_hi:[0,1]
	v_pk_fma_f32 v[90:91], v[86:87], s[68:69], v[90:91] op_sel_hi:[0,1,1] neg_lo:[0,0,1] neg_hi:[0,0,1]
	v_pk_add_f32 v[60:61], v[60:61], v[90:91]
	v_pk_mul_f32 v[90:91], v[88:89], s[80:81] op_sel_hi:[0,1]
	v_pk_fma_f32 v[90:91], v[86:87], s[72:73], v[90:91] op_sel_hi:[0,1,1] neg_lo:[0,0,1] neg_hi:[0,0,1]
	v_pk_add_f32 v[64:65], v[64:65], v[90:91]
	v_pk_mul_f32 v[90:91], v[88:89], s[84:85] op_sel_hi:[0,1]
	v_pk_fma_f32 v[90:91], v[86:87], s[82:83], v[90:91] op_sel_hi:[0,1,1] neg_lo:[0,0,1] neg_hi:[0,0,1]
	v_pk_add_f32 v[62:63], v[62:63], v[90:91]
	v_readlane_b32 s16, v3, 0
	v_readlane_b32 s17, v3, 2
	v_readlane_b32 s44, v3, 1
	v_readlane_b32 s45, v3, 3
	v_readlane_b32 s46, v3, 4
	v_readlane_b32 s47, v3, 6
	v_readlane_b32 s48, v3, 5
	v_readlane_b32 s49, v3, 7
	v_readlane_b32 s52, v3, 8
	v_readlane_b32 s53, v3, 10
	v_readlane_b32 s54, v3, 9
	v_readlane_b32 s55, v3, 11
	v_readlane_b32 s56, v3, 12
	v_readlane_b32 s57, v3, 14
	v_readlane_b32 s58, v3, 13
	v_readlane_b32 s59, v3, 15
	v_readlane_b32 s62, v3, 16
	v_readlane_b32 s63, v3, 18
	v_readlane_b32 s64, v3, 17
	v_readlane_b32 s65, v3, 19
	v_readlane_b32 s68, v3, 20
	v_readlane_b32 s69, v3, 22
	v_readlane_b32 s70, v3, 21
	v_readlane_b32 s71, v3, 23
	v_readlane_b32 s72, v3, 24
	v_readlane_b32 s73, v3, 26
	v_readlane_b32 s80, v3, 25
	v_readlane_b32 s81, v3, 27
	v_readlane_b32 s82, v3, 28
	v_readlane_b32 s83, v3, 30
	v_readlane_b32 s84, v3, 29
	v_readlane_b32 s85, v3, 31
	v_mul_f32_e32 v244, v20, v46
	v_mul_f32_e32 v245, v24, v47
	v_sub_f32_e32 v86, v244, v245
	v_mul_f32_e32 v244, v24, v46
	v_mul_f32_e32 v245, v20, v47
	v_add_f32_e32 v88, v244, v245
	v_pk_mul_f32 v[90:91], v[88:89], s[44:45] op_sel_hi:[0,1]
	v_pk_fma_f32 v[90:91], v[86:87], s[16:17], v[90:91] op_sel_hi:[0,1,1] neg_lo:[0,0,1] neg_hi:[0,0,1]
	v_pk_add_f32 v[56:57], v[56:57], v[90:91]
	v_pk_mul_f32 v[90:91], v[88:89], s[48:49] op_sel_hi:[0,1]
	v_pk_fma_f32 v[90:91], v[86:87], s[46:47], v[90:91] op_sel_hi:[0,1,1] neg_lo:[0,0,1] neg_hi:[0,0,1]
	v_pk_add_f32 v[54:55], v[54:55], v[90:91]
	v_pk_mul_f32 v[90:91], v[88:89], s[54:55] op_sel_hi:[0,1]
	v_pk_fma_f32 v[90:91], v[86:87], s[52:53], v[90:91] op_sel_hi:[0,1,1] neg_lo:[0,0,1] neg_hi:[0,0,1]
	v_pk_add_f32 v[52:53], v[52:53], v[90:91]
	v_pk_mul_f32 v[90:91], v[88:89], s[58:59] op_sel_hi:[0,1]
	v_pk_fma_f32 v[90:91], v[86:87], s[56:57], v[90:91] op_sel_hi:[0,1,1] neg_lo:[0,0,1] neg_hi:[0,0,1]
	v_pk_add_f32 v[50:51], v[50:51], v[90:91]
	v_pk_mul_f32 v[90:91], v[88:89], s[64:65] op_sel_hi:[0,1]
	v_pk_fma_f32 v[90:91], v[86:87], s[62:63], v[90:91] op_sel_hi:[0,1,1] neg_lo:[0,0,1] neg_hi:[0,0,1]
	v_pk_add_f32 v[58:59], v[58:59], v[90:91]
	v_pk_mul_f32 v[90:91], v[88:89], s[70:71] op_sel_hi:[0,1]
	v_pk_fma_f32 v[90:91], v[86:87], s[68:69], v[90:91] op_sel_hi:[0,1,1] neg_lo:[0,0,1] neg_hi:[0,0,1]
	v_pk_add_f32 v[60:61], v[60:61], v[90:91]
	v_pk_mul_f32 v[90:91], v[88:89], s[80:81] op_sel_hi:[0,1]
	v_pk_fma_f32 v[90:91], v[86:87], s[72:73], v[90:91] op_sel_hi:[0,1,1] neg_lo:[0,0,1] neg_hi:[0,0,1]
	v_pk_add_f32 v[64:65], v[64:65], v[90:91]
	v_pk_mul_f32 v[90:91], v[88:89], s[84:85] op_sel_hi:[0,1]
	v_pk_fma_f32 v[90:91], v[86:87], s[82:83], v[90:91] op_sel_hi:[0,1,1] neg_lo:[0,0,1] neg_hi:[0,0,1]
	v_pk_add_f32 v[62:63], v[62:63], v[90:91]
	v_readlane_b32 s16, v3, 32
	v_readlane_b32 s17, v3, 34
	v_readlane_b32 s44, v3, 33
	v_readlane_b32 s45, v3, 35
	v_readlane_b32 s46, v3, 36
	v_readlane_b32 s47, v3, 38
	v_readlane_b32 s48, v3, 37
	v_readlane_b32 s49, v3, 39
	v_readlane_b32 s52, v3, 40
	v_readlane_b32 s53, v3, 42
	v_readlane_b32 s54, v3, 41
	v_readlane_b32 s55, v3, 43
	v_readlane_b32 s56, v3, 44
	v_readlane_b32 s57, v3, 46
	v_readlane_b32 s58, v3, 45
	v_readlane_b32 s59, v3, 47
	v_readlane_b32 s62, v3, 48
	v_readlane_b32 s63, v3, 50
	v_readlane_b32 s64, v3, 49
	v_readlane_b32 s65, v3, 51
	v_readlane_b32 s68, v3, 52
	v_readlane_b32 s69, v3, 54
	v_readlane_b32 s70, v3, 53
; __device__ __forceinline__ void ph1_small(const Args& a, int tid, int wave, int lane, int G, int bid) {
;     ...
; #pragma unroll 8
;             for (int n = 0; n < 64; ++n) { const float cr = cre[((size_t)g * 16 + p) * 64 + n], ci = cim[((size_t)g * 16 + p) * 64 + n];
;                 const float pr = POW[(((size_t)g * 65 + tau) * 64 + n) * 2], pi = POW[(((size_t)g * 65 + tau) * 64 + n) * 2 + 1];
;                 const float er = cr * pr - ci * pi, ei = cr * pi + ci * pr;
;                 const f32x4* bp = (const f32x4*)(BBAR + ((size_t)g * 64 + n) * 32);
; #pragma unroll
;                 for (int q = 0; q < 8; ++q) { const f32x4 bb = bp[q]; s[2 * q] += er * bb[0] - ei * bb[1]; s[2 * q + 1] += er * bb[2] - ei * bb[3]; } }
	v_readlane_b32 s71, v3, 55
	v_readlane_b32 s72, v3, 56
	v_readlane_b32 s73, v3, 58
	v_readlane_b32 s80, v3, 57
	v_readlane_b32 s81, v3, 59
	v_readlane_b32 s82, v3, 60
	v_readlane_b32 s83, v3, 62
	v_readlane_b32 s84, v3, 61
	v_readlane_b32 s85, v3, 63
	v_mul_f32_e32 v244, v21, v48
	v_mul_f32_e32 v245, v25, v49
	v_sub_f32_e32 v86, v244, v245
	v_mul_f32_e32 v244, v25, v48
	v_mul_f32_e32 v245, v21, v49
	v_add_f32_e32 v88, v244, v245
	v_pk_mul_f32 v[90:91], v[88:89], s[44:45] op_sel_hi:[0,1]
	v_pk_fma_f32 v[90:91], v[86:87], s[16:17], v[90:91] op_sel_hi:[0,1,1] neg_lo:[0,0,1] neg_hi:[0,0,1]
	v_pk_add_f32 v[56:57], v[56:57], v[90:91]
	v_pk_mul_f32 v[90:91], v[88:89], s[48:49] op_sel_hi:[0,1]
	v_pk_fma_f32 v[90:91], v[86:87], s[46:47], v[90:91] op_sel_hi:[0,1,1] neg_lo:[0,0,1] neg_hi:[0,0,1]
	v_pk_add_f32 v[54:55], v[54:55], v[90:91]
	v_pk_mul_f32 v[90:91], v[88:89], s[54:55] op_sel_hi:[0,1]
	v_pk_fma_f32 v[90:91], v[86:87], s[52:53], v[90:91] op_sel_hi:[0,1,1] neg_lo:[0,0,1] neg_hi:[0,0,1]
	v_pk_add_f32 v[52:53], v[52:53], v[90:91]
	v_pk_mul_f32 v[90:91], v[88:89], s[58:59] op_sel_hi:[0,1]
	v_pk_fma_f32 v[90:91], v[86:87], s[56:57], v[90:91] op_sel_hi:[0,1,1] neg_lo:[0,0,1] neg_hi:[0,0,1]
	v_pk_add_f32 v[50:51], v[50:51], v[90:91]
	v_pk_mul_f32 v[90:91], v[88:89], s[64:65] op_sel_hi:[0,1]
	v_pk_fma_f32 v[90:91], v[86:87], s[62:63], v[90:91] op_sel_hi:[0,1,1] neg_lo:[0,0,1] neg_hi:[0,0,1]
	v_pk_add_f32 v[58:59], v[58:59], v[90:91]
	v_pk_mul_f32 v[90:91], v[88:89], s[70:71] op_sel_hi:[0,1]
	v_pk_fma_f32 v[90:91], v[86:87], s[68:69], v[90:91] op_sel_hi:[0,1,1] neg_lo:[0,0,1] neg_hi:[0,0,1]
	v_pk_add_f32 v[60:61], v[60:61], v[90:91]
	v_pk_mul_f32 v[90:91], v[88:89], s[80:81] op_sel_hi:[0,1]
	v_pk_fma_f32 v[90:91], v[86:87], s[72:73], v[90:91] op_sel_hi:[0,1,1] neg_lo:[0,0,1] neg_hi:[0,0,1]
	v_pk_add_f32 v[64:65], v[64:65], v[90:91]
	v_pk_mul_f32 v[90:91], v[88:89], s[84:85] op_sel_hi:[0,1]
	v_pk_fma_f32 v[90:91], v[86:87], s[82:83], v[90:91] op_sel_hi:[0,1,1] neg_lo:[0,0,1] neg_hi:[0,0,1]
	v_pk_add_f32 v[62:63], v[62:63], v[90:91]
	global_load_dwordx4 v[18:21], v[44:45], off offset:32
	global_load_dwordx4 v[22:25], v[42:43], off offset:32
	global_load_dwordx4 v[26:29], v40, s[100:101] offset:64
	global_load_dwordx4 v[46:49], v40, s[100:101] offset:80
	s_waitcnt vmcnt(4)
	v_readlane_b32 s16, v4, 0
	v_readlane_b32 s17, v4, 2
	v_readlane_b32 s44, v4, 1
	v_readlane_b32 s45, v4, 3
	v_readlane_b32 s46, v4, 4
	v_readlane_b32 s47, v4, 6
	v_readlane_b32 s48, v4, 5
	v_readlane_b32 s49, v4, 7
	v_readlane_b32 s52, v4, 8
	v_readlane_b32 s53, v4, 10
	v_readlane_b32 s54, v4, 9
	v_readlane_b32 s55, v4, 11
	v_readlane_b32 s56, v4, 12
	v_readlane_b32 s57, v4, 14
	v_readlane_b32 s58, v4, 13
	v_readlane_b32 s59, v4, 15
	v_readlane_b32 s62, v4, 16
	v_readlane_b32 s63, v4, 18
	v_readlane_b32 s64, v4, 17
	v_readlane_b32 s65, v4, 19
	v_readlane_b32 s68, v4, 20
	v_readlane_b32 s69, v4, 22
	v_readlane_b32 s70, v4, 21
	v_readlane_b32 s71, v4, 23
	v_readlane_b32 s72, v4, 24
	v_readlane_b32 s73, v4, 26
	v_readlane_b32 s80, v4, 25
	v_readlane_b32 s81, v4, 27
	v_readlane_b32 s82, v4, 28
	v_readlane_b32 s83, v4, 30
	v_readlane_b32 s84, v4, 29
	v_readlane_b32 s85, v4, 31
	v_mul_f32_e32 v244, v70, v78
	v_mul_f32_e32 v245, v74, v79
	v_sub_f32_e32 v86, v244, v245
	v_mul_f32_e32 v244, v74, v78
	v_mul_f32_e32 v245, v70, v79
	v_add_f32_e32 v88, v244, v245
	v_pk_mul_f32 v[90:91], v[88:89], s[44:45] op_sel_hi:[0,1]
	v_pk_fma_f32 v[90:91], v[86:87], s[16:17], v[90:91] op_sel_hi:[0,1,1] neg_lo:[0,0,1] neg_hi:[0,0,1]
	v_pk_add_f32 v[56:57], v[56:57], v[90:91]
	v_pk_mul_f32 v[90:91], v[88:89], s[48:49] op_sel_hi:[0,1]
	v_pk_fma_f32 v[90:91], v[86:87], s[46:47], v[90:91] op_sel_hi:[0,1,1] neg_lo:[0,0,1] neg_hi:[0,0,1]
	v_pk_add_f32 v[54:55], v[54:55], v[90:91]
	v_pk_mul_f32 v[90:91], v[88:89], s[54:55] op_sel_hi:[0,1]
	v_pk_fma_f32 v[90:91], v[86:87], s[52:53], v[90:91] op_sel_hi:[0,1,1] neg_lo:[0,0,1] neg_hi:[0,0,1]
	v_pk_add_f32 v[52:53], v[52:53], v[90:91]
	v_pk_mul_f32 v[90:91], v[88:89], s[58:59] op_sel_hi:[0,1]
	v_pk_fma_f32 v[90:91], v[86:87], s[56:57], v[90:91] op_sel_hi:[0,1,1] neg_lo:[0,0,1] neg_hi:[0,0,1]
	v_pk_add_f32 v[50:51], v[50:51], v[90:91]
	v_pk_mul_f32 v[90:91], v[88:89], s[64:65] op_sel_hi:[0,1]
	v_pk_fma_f32 v[90:91], v[86:87], s[62:63], v[90:91] op_sel_hi:[0,1,1] neg_lo:[0,0,1] neg_hi:[0,0,1]
	v_pk_add_f32 v[58:59], v[58:59], v[90:91]
	v_pk_mul_f32 v[90:91], v[88:89], s[70:71] op_sel_hi:[0,1]
	v_pk_fma_f32 v[90:91], v[86:87], s[68:69], v[90:91] op_sel_hi:[0,1,1] neg_lo:[0,0,1] neg_hi:[0,0,1]
	v_pk_add_f32 v[60:61], v[60:61], v[90:91]
	v_pk_mul_f32 v[90:91], v[88:89], s[80:81] op_sel_hi:[0,1]
	v_pk_fma_f32 v[90:91], v[86:87], s[72:73], v[90:91] op_sel_hi:[0,1,1] neg_lo:[0,0,1] neg_hi:[0,0,1]
	v_pk_add_f32 v[64:65], v[64:65], v[90:91]
	v_pk_mul_f32 v[90:91], v[88:89], s[84:85] op_sel_hi:[0,1]
	v_pk_fma_f32 v[90:91], v[86:87], s[82:83], v[90:91] op_sel_hi:[0,1,1] neg_lo:[0,0,1] neg_hi:[0,0,1]
	v_pk_add_f32 v[62:63], v[62:63], v[90:91]
	v_readlane_b32 s16, v4, 32
	v_readlane_b32 s17, v4, 34
	v_readlane_b32 s44, v4, 33
	v_readlane_b32 s45, v4, 35
	v_readlane_b32 s46, v4, 36
	v_readlane_b32 s47, v4, 38
	v_readlane_b32 s48, v4, 37
	v_readlane_b32 s49, v4, 39
	v_readlane_b32 s52, v4, 40
	v_readlane_b32 s53, v4, 42
	v_readlane_b32 s54, v4, 41
	v_readlane_b32 s55, v4, 43
	v_readlane_b32 s56, v4, 44
	v_readlane_b32 s57, v4, 46
	v_readlane_b32 s58, v4, 45
	v_readlane_b32 s59, v4, 47
	v_readlane_b32 s62, v4, 48
	v_readlane_b32 s63, v4, 50
	v_readlane_b32 s64, v4, 49
	v_readlane_b32 s65, v4, 51
	v_readlane_b32 s68, v4, 52
	v_readlane_b32 s69, v4, 54
	v_readlane_b32 s70, v4, 53
; __device__ __forceinline__ void ph1_small(const Args& a, int tid, int wave, int lane, int G, int bid) {
;     ...
; #pragma unroll 8
;             for (int n = 0; n < 64; ++n) { const float cr = cre[((size_t)g * 16 + p) * 64 + n], ci = cim[((size_t)g * 16 + p) * 64 + n];
;                 const float pr = POW[(((size_t)g * 65 + tau) * 64 + n) * 2], pi = POW[(((size_t)g * 65 + tau) * 64 + n) * 2 + 1];
;                 const float er = cr * pr - ci * pi, ei = cr * pi + ci * pr;
;                 const f32x4* bp = (const f32x4*)(BBAR + ((size_t)g * 64 + n) * 32);
; #pragma unroll
;                 for (int q = 0; q < 8; ++q) { const f32x4 bb = bp[q]; s[2 * q] += er * bb[0] - ei * bb[1]; s[2 * q + 1] += er * bb[2] - ei * bb[3]; } }
	v_readlane_b32 s71, v4, 55
	v_readlane_b32 s72, v4, 56
	v_readlane_b32 s73, v4, 58
	v_readlane_b32 s80, v4, 57
	v_readlane_b32 s81, v4, 59
	v_readlane_b32 s82, v4, 60
	v_readlane_b32 s83, v4, 62
	v_readlane_b32 s84, v4, 61
	v_readlane_b32 s85, v4, 63
	v_mul_f32_e32 v244, v71, v80
	v_mul_f32_e32 v245, v75, v81
	v_sub_f32_e32 v86, v244, v245
	v_mul_f32_e32 v244, v75, v80
	v_mul_f32_e32 v245, v71, v81
	v_add_f32_e32 v88, v244, v245
	v_pk_mul_f32 v[90:91], v[88:89], s[44:45] op_sel_hi:[0,1]
	v_pk_fma_f32 v[90:91], v[86:87], s[16:17], v[90:91] op_sel_hi:[0,1,1] neg_lo:[0,0,1] neg_hi:[0,0,1]
	v_pk_add_f32 v[56:57], v[56:57], v[90:91]
	v_pk_mul_f32 v[90:91], v[88:89], s[48:49] op_sel_hi:[0,1]
	v_pk_fma_f32 v[90:91], v[86:87], s[46:47], v[90:91] op_sel_hi:[0,1,1] neg_lo:[0,0,1] neg_hi:[0,0,1]
	v_pk_add_f32 v[54:55], v[54:55], v[90:91]
	v_pk_mul_f32 v[90:91], v[88:89], s[54:55] op_sel_hi:[0,1]
	v_pk_fma_f32 v[90:91], v[86:87], s[52:53], v[90:91] op_sel_hi:[0,1,1] neg_lo:[0,0,1] neg_hi:[0,0,1]
	v_pk_add_f32 v[52:53], v[52:53], v[90:91]
	v_pk_mul_f32 v[90:91], v[88:89], s[58:59] op_sel_hi:[0,1]
	v_pk_fma_f32 v[90:91], v[86:87], s[56:57], v[90:91] op_sel_hi:[0,1,1] neg_lo:[0,0,1] neg_hi:[0,0,1]
	v_pk_add_f32 v[50:51], v[50:51], v[90:91]
	v_pk_mul_f32 v[90:91], v[88:89], s[64:65] op_sel_hi:[0,1]
	v_pk_fma_f32 v[90:91], v[86:87], s[62:63], v[90:91] op_sel_hi:[0,1,1] neg_lo:[0,0,1] neg_hi:[0,0,1]
	v_pk_add_f32 v[58:59], v[58:59], v[90:91]
	v_pk_mul_f32 v[90:91], v[88:89], s[70:71] op_sel_hi:[0,1]
	v_pk_fma_f32 v[90:91], v[86:87], s[68:69], v[90:91] op_sel_hi:[0,1,1] neg_lo:[0,0,1] neg_hi:[0,0,1]
	v_pk_add_f32 v[60:61], v[60:61], v[90:91]
	v_pk_mul_f32 v[90:91], v[88:89], s[80:81] op_sel_hi:[0,1]
	v_pk_fma_f32 v[90:91], v[86:87], s[72:73], v[90:91] op_sel_hi:[0,1,1] neg_lo:[0,0,1] neg_hi:[0,0,1]
	v_pk_add_f32 v[64:65], v[64:65], v[90:91]
	v_pk_mul_f32 v[90:91], v[88:89], s[84:85] op_sel_hi:[0,1]
	v_pk_fma_f32 v[90:91], v[86:87], s[82:83], v[90:91] op_sel_hi:[0,1,1] neg_lo:[0,0,1] neg_hi:[0,0,1]
	v_pk_add_f32 v[62:63], v[62:63], v[90:91]
	v_readlane_b32 s16, v5, 0
	v_readlane_b32 s17, v5, 2
	v_readlane_b32 s44, v5, 1
	v_readlane_b32 s45, v5, 3
	v_readlane_b32 s46, v5, 4
	v_readlane_b32 s47, v5, 6
	v_readlane_b32 s48, v5, 5
	v_readlane_b32 s49, v5, 7
	v_readlane_b32 s52, v5, 8
	v_readlane_b32 s53, v5, 10
	v_readlane_b32 s54, v5, 9
	v_readlane_b32 s55, v5, 11
	v_readlane_b32 s56, v5, 12
	v_readlane_b32 s57, v5, 14
	v_readlane_b32 s58, v5, 13
	v_readlane_b32 s59, v5, 15
	v_readlane_b32 s62, v5, 16
	v_readlane_b32 s63, v5, 18
	v_readlane_b32 s64, v5, 17
	v_readlane_b32 s65, v5, 19
	v_readlane_b32 s68, v5, 20
	v_readlane_b32 s69, v5, 22
	v_readlane_b32 s70, v5, 21
	v_readlane_b32 s71, v5, 23
	v_readlane_b32 s72, v5, 24
	v_readlane_b32 s73, v5, 26
	v_readlane_b32 s80, v5, 25
	v_readlane_b32 s81, v5, 27
	v_readlane_b32 s82, v5, 28
	v_readlane_b32 s83, v5, 30
	v_readlane_b32 s84, v5, 29
	v_readlane_b32 s85, v5, 31
	v_mul_f32_e32 v244, v72, v82
	v_mul_f32_e32 v245, v76, v83
	v_sub_f32_e32 v86, v244, v245
	v_mul_f32_e32 v244, v76, v82
	v_mul_f32_e32 v245, v72, v83
	v_add_f32_e32 v88, v244, v245
	v_pk_mul_f32 v[90:91], v[88:89], s[44:45] op_sel_hi:[0,1]
	v_pk_fma_f32 v[90:91], v[86:87], s[16:17], v[90:91] op_sel_hi:[0,1,1] neg_lo:[0,0,1] neg_hi:[0,0,1]
	v_pk_add_f32 v[56:57], v[56:57], v[90:91]
	v_pk_mul_f32 v[90:91], v[88:89], s[48:49] op_sel_hi:[0,1]
	v_pk_fma_f32 v[90:91], v[86:87], s[46:47], v[90:91] op_sel_hi:[0,1,1] neg_lo:[0,0,1] neg_hi:[0,0,1]
	v_pk_add_f32 v[54:55], v[54:55], v[90:91]
	v_pk_mul_f32 v[90:91], v[88:89], s[54:55] op_sel_hi:[0,1]
	v_pk_fma_f32 v[90:91], v[86:87], s[52:53], v[90:91] op_sel_hi:[0,1,1] neg_lo:[0,0,1] neg_hi:[0,0,1]
	v_pk_add_f32 v[52:53], v[52:53], v[90:91]
	v_pk_mul_f32 v[90:91], v[88:89], s[58:59] op_sel_hi:[0,1]
	v_pk_fma_f32 v[90:91], v[86:87], s[56:57], v[90:91] op_sel_hi:[0,1,1] neg_lo:[0,0,1] neg_hi:[0,0,1]
	v_pk_add_f32 v[50:51], v[50:51], v[90:91]
	v_pk_mul_f32 v[90:91], v[88:89], s[64:65] op_sel_hi:[0,1]
	v_pk_fma_f32 v[90:91], v[86:87], s[62:63], v[90:91] op_sel_hi:[0,1,1] neg_lo:[0,0,1] neg_hi:[0,0,1]
	v_pk_add_f32 v[58:59], v[58:59], v[90:91]
	v_pk_mul_f32 v[90:91], v[88:89], s[70:71] op_sel_hi:[0,1]
	v_pk_fma_f32 v[90:91], v[86:87], s[68:69], v[90:91] op_sel_hi:[0,1,1] neg_lo:[0,0,1] neg_hi:[0,0,1]
	v_pk_add_f32 v[60:61], v[60:61], v[90:91]
	v_pk_mul_f32 v[90:91], v[88:89], s[80:81] op_sel_hi:[0,1]
	v_pk_fma_f32 v[90:91], v[86:87], s[72:73], v[90:91] op_sel_hi:[0,1,1] neg_lo:[0,0,1] neg_hi:[0,0,1]
	v_pk_add_f32 v[64:65], v[64:65], v[90:91]
	v_pk_mul_f32 v[90:91], v[88:89], s[84:85] op_sel_hi:[0,1]
	v_pk_fma_f32 v[90:91], v[86:87], s[82:83], v[90:91] op_sel_hi:[0,1,1] neg_lo:[0,0,1] neg_hi:[0,0,1]
	v_pk_add_f32 v[62:63], v[62:63], v[90:91]
	v_readlane_b32 s16, v5, 32
	v_readlane_b32 s17, v5, 34
	v_readlane_b32 s44, v5, 33
	v_readlane_b32 s45, v5, 35
	v_readlane_b32 s46, v5, 36
	v_readlane_b32 s47, v5, 38
	v_readlane_b32 s48, v5, 37
	v_readlane_b32 s49, v5, 39
	v_readlane_b32 s52, v5, 40
	v_readlane_b32 s53, v5, 42
	v_readlane_b32 s54, v5, 41
	v_readlane_b32 s55, v5, 43
	v_readlane_b32 s56, v5, 44
	v_readlane_b32 s57, v5, 46
	v_readlane_b32 s58, v5, 45
	v_readlane_b32 s59, v5, 47
	v_readlane_b32 s62, v5, 48
	v_readlane_b32 s63, v5, 50
	v_readlane_b32 s64, v5, 49
	v_readlane_b32 s65, v5, 51
	v_readlane_b32 s68, v5, 52
	v_readlane_b32 s69, v5, 54
	v_readlane_b32 s70, v5, 53
	v_readlane_b32 s71, v5, 55
	v_readlane_b32 s72, v5, 56
	v_readlane_b32 s73, v5, 58
	v_readlane_b32 s80, v5, 57
	v_readlane_b32 s81, v5, 59
	v_readlane_b32 s82, v5, 60
	v_readlane_b32 s83, v5, 62
	v_readlane_b32 s84, v5, 61
	v_readlane_b32 s85, v5, 63
; __device__ __forceinline__ void ph1_small(const Args& a, int tid, int wave, int lane, int G, int bid) {
;     ...
; #pragma unroll 8
;             for (int n = 0; n < 64; ++n) { const float cr = cre[((size_t)g * 16 + p) * 64 + n], ci = cim[((size_t)g * 16 + p) * 64 + n];
;                 const float pr = POW[(((size_t)g * 65 + tau) * 64 + n) * 2], pi = POW[(((size_t)g * 65 + tau) * 64 + n) * 2 + 1];
;                 const float er = cr * pr - ci * pi, ei = cr * pi + ci * pr;
;                 const f32x4* bp = (const f32x4*)(BBAR + ((size_t)g * 64 + n) * 32);
; #pragma unroll
;                 for (int q = 0; q < 8; ++q) { const f32x4 bb = bp[q]; s[2 * q] += er * bb[0] - ei * bb[1]; s[2 * q + 1] += er * bb[2] - ei * bb[3]; } }
	v_mul_f32_e32 v244, v73, v84
	v_mul_f32_e32 v245, v77, v85
	v_sub_f32_e32 v86, v244, v245
	v_mul_f32_e32 v244, v77, v84
	v_mul_f32_e32 v245, v73, v85
	v_add_f32_e32 v88, v244, v245
	v_pk_mul_f32 v[90:91], v[88:89], s[44:45] op_sel_hi:[0,1]
	v_pk_fma_f32 v[90:91], v[86:87], s[16:17], v[90:91] op_sel_hi:[0,1,1] neg_lo:[0,0,1] neg_hi:[0,0,1]
	v_pk_add_f32 v[56:57], v[56:57], v[90:91]
	v_pk_mul_f32 v[90:91], v[88:89], s[48:49] op_sel_hi:[0,1]
	v_pk_fma_f32 v[90:91], v[86:87], s[46:47], v[90:91] op_sel_hi:[0,1,1] neg_lo:[0,0,1] neg_hi:[0,0,1]
	v_pk_add_f32 v[54:55], v[54:55], v[90:91]
	v_pk_mul_f32 v[90:91], v[88:89], s[54:55] op_sel_hi:[0,1]
	v_pk_fma_f32 v[90:91], v[86:87], s[52:53], v[90:91] op_sel_hi:[0,1,1] neg_lo:[0,0,1] neg_hi:[0,0,1]
	v_pk_add_f32 v[52:53], v[52:53], v[90:91]
	v_pk_mul_f32 v[90:91], v[88:89], s[58:59] op_sel_hi:[0,1]
	v_pk_fma_f32 v[90:91], v[86:87], s[56:57], v[90:91] op_sel_hi:[0,1,1] neg_lo:[0,0,1] neg_hi:[0,0,1]
	v_pk_add_f32 v[50:51], v[50:51], v[90:91]
	v_pk_mul_f32 v[90:91], v[88:89], s[64:65] op_sel_hi:[0,1]
	v_pk_fma_f32 v[90:91], v[86:87], s[62:63], v[90:91] op_sel_hi:[0,1,1] neg_lo:[0,0,1] neg_hi:[0,0,1]
	v_pk_add_f32 v[58:59], v[58:59], v[90:91]
	v_pk_mul_f32 v[90:91], v[88:89], s[70:71] op_sel_hi:[0,1]
	v_pk_fma_f32 v[90:91], v[86:87], s[68:69], v[90:91] op_sel_hi:[0,1,1] neg_lo:[0,0,1] neg_hi:[0,0,1]
	v_pk_add_f32 v[60:61], v[60:61], v[90:91]
	v_pk_mul_f32 v[90:91], v[88:89], s[80:81] op_sel_hi:[0,1]
	v_pk_fma_f32 v[90:91], v[86:87], s[72:73], v[90:91] op_sel_hi:[0,1,1] neg_lo:[0,0,1] neg_hi:[0,0,1]
	v_pk_add_f32 v[64:65], v[64:65], v[90:91]
	v_pk_mul_f32 v[90:91], v[88:89], s[84:85] op_sel_hi:[0,1]
	v_pk_fma_f32 v[90:91], v[86:87], s[82:83], v[90:91] op_sel_hi:[0,1,1] neg_lo:[0,0,1] neg_hi:[0,0,1]
	v_pk_add_f32 v[62:63], v[62:63], v[90:91]
	global_load_dwordx4 v[70:73], v[44:45], off offset:48
	global_load_dwordx4 v[74:77], v[42:43], off offset:48
	global_load_dwordx4 v[78:81], v40, s[100:101] offset:96
	global_load_dwordx4 v[82:85], v40, s[100:101] offset:112
	s_waitcnt vmcnt(4)
	v_readlane_b32 s16, v6, 0
	v_readlane_b32 s17, v6, 2
	v_readlane_b32 s44, v6, 1
	v_readlane_b32 s45, v6, 3
	v_readlane_b32 s46, v6, 4
	v_readlane_b32 s47, v6, 6
	v_readlane_b32 s48, v6, 5
	v_readlane_b32 s49, v6, 7
	v_readlane_b32 s52, v6, 8
	v_readlane_b32 s53, v6, 10
	v_readlane_b32 s54, v6, 9
	v_readlane_b32 s55, v6, 11
	v_readlane_b32 s56, v6, 12
	v_readlane_b32 s57, v6, 14
	v_readlane_b32 s58, v6, 13
	v_readlane_b32 s59, v6, 15
	v_readlane_b32 s62, v6, 16
	v_readlane_b32 s63, v6, 18
	v_readlane_b32 s64, v6, 17
	v_readlane_b32 s65, v6, 19
	v_readlane_b32 s68, v6, 20
	v_readlane_b32 s69, v6, 22
	v_readlane_b32 s70, v6, 21
	v_readlane_b32 s71, v6, 23
	v_readlane_b32 s72, v6, 24
	v_readlane_b32 s73, v6, 26
	v_readlane_b32 s80, v6, 25
	v_readlane_b32 s81, v6, 27
	v_readlane_b32 s82, v6, 28
	v_readlane_b32 s83, v6, 30
	v_readlane_b32 s84, v6, 29
	v_readlane_b32 s85, v6, 31
	v_mul_f32_e32 v244, v18, v26
	v_mul_f32_e32 v245, v22, v27
	v_sub_f32_e32 v86, v244, v245
	v_mul_f32_e32 v244, v22, v26
	v_mul_f32_e32 v245, v18, v27
	v_add_f32_e32 v88, v244, v245
	v_pk_mul_f32 v[90:91], v[88:89], s[44:45] op_sel_hi:[0,1]
	v_pk_fma_f32 v[90:91], v[86:87], s[16:17], v[90:91] op_sel_hi:[0,1,1] neg_lo:[0,0,1] neg_hi:[0,0,1]
	v_pk_add_f32 v[56:57], v[56:57], v[90:91]
	v_pk_mul_f32 v[90:91], v[88:89], s[48:49] op_sel_hi:[0,1]
	v_pk_fma_f32 v[90:91], v[86:87], s[46:47], v[90:91] op_sel_hi:[0,1,1] neg_lo:[0,0,1] neg_hi:[0,0,1]
	v_pk_add_f32 v[54:55], v[54:55], v[90:91]
	v_pk_mul_f32 v[90:91], v[88:89], s[54:55] op_sel_hi:[0,1]
	v_pk_fma_f32 v[90:91], v[86:87], s[52:53], v[90:91] op_sel_hi:[0,1,1] neg_lo:[0,0,1] neg_hi:[0,0,1]
	v_pk_add_f32 v[52:53], v[52:53], v[90:91]
	v_pk_mul_f32 v[90:91], v[88:89], s[58:59] op_sel_hi:[0,1]
	v_pk_fma_f32 v[90:91], v[86:87], s[56:57], v[90:91] op_sel_hi:[0,1,1] neg_lo:[0,0,1] neg_hi:[0,0,1]
	v_pk_add_f32 v[50:51], v[50:51], v[90:91]
	v_pk_mul_f32 v[90:91], v[88:89], s[64:65] op_sel_hi:[0,1]
	v_pk_fma_f32 v[90:91], v[86:87], s[62:63], v[90:91] op_sel_hi:[0,1,1] neg_lo:[0,0,1] neg_hi:[0,0,1]
	v_pk_add_f32 v[58:59], v[58:59], v[90:91]
	v_pk_mul_f32 v[90:91], v[88:89], s[70:71] op_sel_hi:[0,1]
	v_pk_fma_f32 v[90:91], v[86:87], s[68:69], v[90:91] op_sel_hi:[0,1,1] neg_lo:[0,0,1] neg_hi:[0,0,1]
	v_pk_add_f32 v[60:61], v[60:61], v[90:91]
	v_pk_mul_f32 v[90:91], v[88:89], s[80:81] op_sel_hi:[0,1]
	v_pk_fma_f32 v[90:91], v[86:87], s[72:73], v[90:91] op_sel_hi:[0,1,1] neg_lo:[0,0,1] neg_hi:[0,0,1]
	v_pk_add_f32 v[64:65], v[64:65], v[90:91]
	v_pk_mul_f32 v[90:91], v[88:89], s[84:85] op_sel_hi:[0,1]
	v_pk_fma_f32 v[90:91], v[86:87], s[82:83], v[90:91] op_sel_hi:[0,1,1] neg_lo:[0,0,1] neg_hi:[0,0,1]
	v_pk_add_f32 v[62:63], v[62:63], v[90:91]
	v_readlane_b32 s16, v6, 32
	v_readlane_b32 s17, v6, 34
	v_readlane_b32 s44, v6, 33
	v_readlane_b32 s45, v6, 35
	v_readlane_b32 s46, v6, 36
	v_readlane_b32 s47, v6, 38
	v_readlane_b32 s48, v6, 37
	v_readlane_b32 s49, v6, 39
	v_readlane_b32 s52, v6, 40
	v_readlane_b32 s53, v6, 42
	v_readlane_b32 s54, v6, 41
	v_readlane_b32 s55, v6, 43
	v_readlane_b32 s56, v6, 44
	v_readlane_b32 s57, v6, 46
	v_readlane_b32 s58, v6, 45
	v_readlane_b32 s59, v6, 47
	v_readlane_b32 s62, v6, 48
	v_readlane_b32 s63, v6, 50
	v_readlane_b32 s64, v6, 49
	v_readlane_b32 s65, v6, 51
	v_readlane_b32 s68, v6, 52
	v_readlane_b32 s69, v6, 54
	v_readlane_b32 s70, v6, 53
	v_readlane_b32 s71, v6, 55
	v_readlane_b32 s72, v6, 56
	v_readlane_b32 s73, v6, 58
	v_readlane_b32 s80, v6, 57
	v_readlane_b32 s81, v6, 59
	v_readlane_b32 s82, v6, 60
	v_readlane_b32 s83, v6, 62
	v_readlane_b32 s84, v6, 61
	v_readlane_b32 s85, v6, 63
; __device__ __forceinline__ void ph1_small(const Args& a, int tid, int wave, int lane, int G, int bid) {
;     ...
; #pragma unroll 8
;             for (int n = 0; n < 64; ++n) { const float cr = cre[((size_t)g * 16 + p) * 64 + n], ci = cim[((size_t)g * 16 + p) * 64 + n];
;                 const float pr = POW[(((size_t)g * 65 + tau) * 64 + n) * 2], pi = POW[(((size_t)g * 65 + tau) * 64 + n) * 2 + 1];
;                 const float er = cr * pr - ci * pi, ei = cr * pi + ci * pr;
;                 const f32x4* bp = (const f32x4*)(BBAR + ((size_t)g * 64 + n) * 32);
; #pragma unroll
;                 for (int q = 0; q < 8; ++q) { const f32x4 bb = bp[q]; s[2 * q] += er * bb[0] - ei * bb[1]; s[2 * q + 1] += er * bb[2] - ei * bb[3]; } }
	v_mul_f32_e32 v244, v19, v28
	v_mul_f32_e32 v245, v23, v29
	v_sub_f32_e32 v86, v244, v245
	v_mul_f32_e32 v244, v23, v28
	v_mul_f32_e32 v245, v19, v29
	v_add_f32_e32 v88, v244, v245
	v_pk_mul_f32 v[90:91], v[88:89], s[44:45] op_sel_hi:[0,1]
	v_pk_fma_f32 v[90:91], v[86:87], s[16:17], v[90:91] op_sel_hi:[0,1,1] neg_lo:[0,0,1] neg_hi:[0,0,1]
	v_pk_add_f32 v[56:57], v[56:57], v[90:91]
	v_pk_mul_f32 v[90:91], v[88:89], s[48:49] op_sel_hi:[0,1]
	v_pk_fma_f32 v[90:91], v[86:87], s[46:47], v[90:91] op_sel_hi:[0,1,1] neg_lo:[0,0,1] neg_hi:[0,0,1]
	v_pk_add_f32 v[54:55], v[54:55], v[90:91]
	v_pk_mul_f32 v[90:91], v[88:89], s[54:55] op_sel_hi:[0,1]
	v_pk_fma_f32 v[90:91], v[86:87], s[52:53], v[90:91] op_sel_hi:[0,1,1] neg_lo:[0,0,1] neg_hi:[0,0,1]
	v_pk_add_f32 v[52:53], v[52:53], v[90:91]
	v_pk_mul_f32 v[90:91], v[88:89], s[58:59] op_sel_hi:[0,1]
	v_pk_fma_f32 v[90:91], v[86:87], s[56:57], v[90:91] op_sel_hi:[0,1,1] neg_lo:[0,0,1] neg_hi:[0,0,1]
	v_pk_add_f32 v[50:51], v[50:51], v[90:91]
	v_pk_mul_f32 v[90:91], v[88:89], s[64:65] op_sel_hi:[0,1]
	v_pk_fma_f32 v[90:91], v[86:87], s[62:63], v[90:91] op_sel_hi:[0,1,1] neg_lo:[0,0,1] neg_hi:[0,0,1]
	v_pk_add_f32 v[58:59], v[58:59], v[90:91]
	v_pk_mul_f32 v[90:91], v[88:89], s[70:71] op_sel_hi:[0,1]
	v_pk_fma_f32 v[90:91], v[86:87], s[68:69], v[90:91] op_sel_hi:[0,1,1] neg_lo:[0,0,1] neg_hi:[0,0,1]
	v_pk_add_f32 v[60:61], v[60:61], v[90:91]
	v_pk_mul_f32 v[90:91], v[88:89], s[80:81] op_sel_hi:[0,1]
	v_pk_fma_f32 v[90:91], v[86:87], s[72:73], v[90:91] op_sel_hi:[0,1,1] neg_lo:[0,0,1] neg_hi:[0,0,1]
	v_pk_add_f32 v[64:65], v[64:65], v[90:91]
	v_pk_mul_f32 v[90:91], v[88:89], s[84:85] op_sel_hi:[0,1]
	v_pk_fma_f32 v[90:91], v[86:87], s[82:83], v[90:91] op_sel_hi:[0,1,1] neg_lo:[0,0,1] neg_hi:[0,0,1]
	v_pk_add_f32 v[62:63], v[62:63], v[90:91]
	v_readlane_b32 s16, v7, 0
	v_readlane_b32 s17, v7, 2
	v_readlane_b32 s44, v7, 1
	v_readlane_b32 s45, v7, 3
	v_readlane_b32 s46, v7, 4
	v_readlane_b32 s47, v7, 6
	v_readlane_b32 s48, v7, 5
	v_readlane_b32 s49, v7, 7
	v_readlane_b32 s52, v7, 8
	v_readlane_b32 s53, v7, 10
	v_readlane_b32 s54, v7, 9
	v_readlane_b32 s55, v7, 11
	v_readlane_b32 s56, v7, 12
	v_readlane_b32 s57, v7, 14
	v_readlane_b32 s58, v7, 13
	v_readlane_b32 s59, v7, 15
	v_readlane_b32 s62, v7, 16
	v_readlane_b32 s63, v7, 18
	v_readlane_b32 s64, v7, 17
	v_readlane_b32 s65, v7, 19
	v_readlane_b32 s68, v7, 20
	v_readlane_b32 s69, v7, 22
	v_readlane_b32 s70, v7, 21
	v_readlane_b32 s71, v7, 23
	v_readlane_b32 s72, v7, 24
	v_readlane_b32 s73, v7, 26
	v_readlane_b32 s80, v7, 25
	v_readlane_b32 s81, v7, 27
	v_readlane_b32 s82, v7, 28
	v_readlane_b32 s83, v7, 30
	v_readlane_b32 s84, v7, 29
	v_readlane_b32 s85, v7, 31
	v_mul_f32_e32 v244, v20, v46
	v_mul_f32_e32 v245, v24, v47
	v_sub_f32_e32 v86, v244, v245
	v_mul_f32_e32 v244, v24, v46
	v_mul_f32_e32 v245, v20, v47
	v_add_f32_e32 v88, v244, v245
	v_pk_mul_f32 v[90:91], v[88:89], s[44:45] op_sel_hi:[0,1]
	v_pk_fma_f32 v[90:91], v[86:87], s[16:17], v[90:91] op_sel_hi:[0,1,1] neg_lo:[0,0,1] neg_hi:[0,0,1]
	v_pk_add_f32 v[56:57], v[56:57], v[90:91]
	v_pk_mul_f32 v[90:91], v[88:89], s[48:49] op_sel_hi:[0,1]
	v_pk_fma_f32 v[90:91], v[86:87], s[46:47], v[90:91] op_sel_hi:[0,1,1] neg_lo:[0,0,1] neg_hi:[0,0,1]
	v_pk_add_f32 v[54:55], v[54:55], v[90:91]
	v_pk_mul_f32 v[90:91], v[88:89], s[54:55] op_sel_hi:[0,1]
	v_pk_fma_f32 v[90:91], v[86:87], s[52:53], v[90:91] op_sel_hi:[0,1,1] neg_lo:[0,0,1] neg_hi:[0,0,1]
	v_pk_add_f32 v[52:53], v[52:53], v[90:91]
	v_pk_mul_f32 v[90:91], v[88:89], s[58:59] op_sel_hi:[0,1]
	v_pk_fma_f32 v[90:91], v[86:87], s[56:57], v[90:91] op_sel_hi:[0,1,1] neg_lo:[0,0,1] neg_hi:[0,0,1]
	v_pk_add_f32 v[50:51], v[50:51], v[90:91]
	v_pk_mul_f32 v[90:91], v[88:89], s[64:65] op_sel_hi:[0,1]
	v_pk_fma_f32 v[90:91], v[86:87], s[62:63], v[90:91] op_sel_hi:[0,1,1] neg_lo:[0,0,1] neg_hi:[0,0,1]
	v_pk_add_f32 v[58:59], v[58:59], v[90:91]
	v_pk_mul_f32 v[90:91], v[88:89], s[70:71] op_sel_hi:[0,1]
	v_pk_fma_f32 v[90:91], v[86:87], s[68:69], v[90:91] op_sel_hi:[0,1,1] neg_lo:[0,0,1] neg_hi:[0,0,1]
	v_pk_add_f32 v[60:61], v[60:61], v[90:91]
	v_pk_mul_f32 v[90:91], v[88:89], s[80:81] op_sel_hi:[0,1]
	v_pk_fma_f32 v[90:91], v[86:87], s[72:73], v[90:91] op_sel_hi:[0,1,1] neg_lo:[0,0,1] neg_hi:[0,0,1]
	v_pk_add_f32 v[64:65], v[64:65], v[90:91]
	v_pk_mul_f32 v[90:91], v[88:89], s[84:85] op_sel_hi:[0,1]
	v_pk_fma_f32 v[90:91], v[86:87], s[82:83], v[90:91] op_sel_hi:[0,1,1] neg_lo:[0,0,1] neg_hi:[0,0,1]
	v_pk_add_f32 v[62:63], v[62:63], v[90:91]
	v_readlane_b32 s16, v7, 32
	v_readlane_b32 s17, v7, 34
	v_readlane_b32 s44, v7, 33
	v_readlane_b32 s45, v7, 35
	v_readlane_b32 s46, v7, 36
	v_readlane_b32 s47, v7, 38
	v_readlane_b32 s48, v7, 37
	v_readlane_b32 s49, v7, 39
	v_readlane_b32 s52, v7, 40
	v_readlane_b32 s53, v7, 42
	v_readlane_b32 s54, v7, 41
	v_readlane_b32 s55, v7, 43
	v_readlane_b32 s56, v7, 44
	v_readlane_b32 s57, v7, 46
	v_readlane_b32 s58, v7, 45
	v_readlane_b32 s59, v7, 47
	v_readlane_b32 s62, v7, 48
	v_readlane_b32 s63, v7, 50
	v_readlane_b32 s64, v7, 49
	v_readlane_b32 s65, v7, 51
	v_readlane_b32 s68, v7, 52
	v_readlane_b32 s69, v7, 54
	v_readlane_b32 s70, v7, 53
	v_readlane_b32 s71, v7, 55
	v_readlane_b32 s72, v7, 56
	v_readlane_b32 s73, v7, 58
	v_readlane_b32 s80, v7, 57
	v_readlane_b32 s81, v7, 59
	v_readlane_b32 s82, v7, 60
	v_readlane_b32 s83, v7, 62
	v_readlane_b32 s84, v7, 61
	v_readlane_b32 s85, v7, 63
	v_mul_f32_e32 v244, v21, v48
	v_mul_f32_e32 v245, v25, v49
	v_sub_f32_e32 v86, v244, v245
	v_mul_f32_e32 v244, v25, v48
	v_mul_f32_e32 v245, v21, v49
	v_add_f32_e32 v88, v244, v245
	v_pk_mul_f32 v[90:91], v[88:89], s[44:45] op_sel_hi:[0,1]
; __device__ __forceinline__ void ph1_small(const Args& a, int tid, int wave, int lane, int G, int bid) {
;     ...
; #pragma unroll 8
;             for (int n = 0; n < 64; ++n) { const float cr = cre[((size_t)g * 16 + p) * 64 + n], ci = cim[((size_t)g * 16 + p) * 64 + n];
;                 const float pr = POW[(((size_t)g * 65 + tau) * 64 + n) * 2], pi = POW[(((size_t)g * 65 + tau) * 64 + n) * 2 + 1];
;                 const float er = cr * pr - ci * pi, ei = cr * pi + ci * pr;
;                 const f32x4* bp = (const f32x4*)(BBAR + ((size_t)g * 64 + n) * 32);
; #pragma unroll
;                 for (int q = 0; q < 8; ++q) { const f32x4 bb = bp[q]; s[2 * q] += er * bb[0] - ei * bb[1]; s[2 * q + 1] += er * bb[2] - ei * bb[3]; } }
	v_pk_fma_f32 v[90:91], v[86:87], s[16:17], v[90:91] op_sel_hi:[0,1,1] neg_lo:[0,0,1] neg_hi:[0,0,1]
	v_pk_add_f32 v[56:57], v[56:57], v[90:91]
	v_pk_mul_f32 v[90:91], v[88:89], s[48:49] op_sel_hi:[0,1]
	v_pk_fma_f32 v[90:91], v[86:87], s[46:47], v[90:91] op_sel_hi:[0,1,1] neg_lo:[0,0,1] neg_hi:[0,0,1]
	v_pk_add_f32 v[54:55], v[54:55], v[90:91]
	v_pk_mul_f32 v[90:91], v[88:89], s[54:55] op_sel_hi:[0,1]
	v_pk_fma_f32 v[90:91], v[86:87], s[52:53], v[90:91] op_sel_hi:[0,1,1] neg_lo:[0,0,1] neg_hi:[0,0,1]
	v_pk_add_f32 v[52:53], v[52:53], v[90:91]
	v_pk_mul_f32 v[90:91], v[88:89], s[58:59] op_sel_hi:[0,1]
	v_pk_fma_f32 v[90:91], v[86:87], s[56:57], v[90:91] op_sel_hi:[0,1,1] neg_lo:[0,0,1] neg_hi:[0,0,1]
	v_pk_add_f32 v[50:51], v[50:51], v[90:91]
	v_pk_mul_f32 v[90:91], v[88:89], s[64:65] op_sel_hi:[0,1]
	v_pk_fma_f32 v[90:91], v[86:87], s[62:63], v[90:91] op_sel_hi:[0,1,1] neg_lo:[0,0,1] neg_hi:[0,0,1]
	v_pk_add_f32 v[58:59], v[58:59], v[90:91]
	v_pk_mul_f32 v[90:91], v[88:89], s[70:71] op_sel_hi:[0,1]
	v_pk_fma_f32 v[90:91], v[86:87], s[68:69], v[90:91] op_sel_hi:[0,1,1] neg_lo:[0,0,1] neg_hi:[0,0,1]
	v_pk_add_f32 v[60:61], v[60:61], v[90:91]
	v_pk_mul_f32 v[90:91], v[88:89], s[80:81] op_sel_hi:[0,1]
	v_pk_fma_f32 v[90:91], v[86:87], s[72:73], v[90:91] op_sel_hi:[0,1,1] neg_lo:[0,0,1] neg_hi:[0,0,1]
	v_pk_add_f32 v[64:65], v[64:65], v[90:91]
	v_pk_mul_f32 v[90:91], v[88:89], s[84:85] op_sel_hi:[0,1]
	v_pk_fma_f32 v[90:91], v[86:87], s[82:83], v[90:91] op_sel_hi:[0,1,1] neg_lo:[0,0,1] neg_hi:[0,0,1]
	v_pk_add_f32 v[62:63], v[62:63], v[90:91]
	global_load_dwordx4 v[18:21], v[44:45], off offset:64
	global_load_dwordx4 v[22:25], v[42:43], off offset:64
	global_load_dwordx4 v[26:29], v40, s[100:101] offset:128
	global_load_dwordx4 v[46:49], v40, s[100:101] offset:144
	s_waitcnt vmcnt(4)
	v_readlane_b32 s16, v8, 0
	v_readlane_b32 s17, v8, 2
	v_readlane_b32 s44, v8, 1
	v_readlane_b32 s45, v8, 3
	v_readlane_b32 s46, v8, 4
	v_readlane_b32 s47, v8, 6
	v_readlane_b32 s48, v8, 5
	v_readlane_b32 s49, v8, 7
	v_readlane_b32 s52, v8, 8
	v_readlane_b32 s53, v8, 10
	v_readlane_b32 s54, v8, 9
	v_readlane_b32 s55, v8, 11
	v_readlane_b32 s56, v8, 12
	v_readlane_b32 s57, v8, 14
	v_readlane_b32 s58, v8, 13
	v_readlane_b32 s59, v8, 15
	v_readlane_b32 s62, v8, 16
	v_readlane_b32 s63, v8, 18
	v_readlane_b32 s64, v8, 17
	v_readlane_b32 s65, v8, 19
	v_readlane_b32 s68, v8, 20
	v_readlane_b32 s69, v8, 22
	v_readlane_b32 s70, v8, 21
	v_readlane_b32 s71, v8, 23
	v_readlane_b32 s72, v8, 24
	v_readlane_b32 s73, v8, 26
	v_readlane_b32 s80, v8, 25
	v_readlane_b32 s81, v8, 27
	v_readlane_b32 s82, v8, 28
	v_readlane_b32 s83, v8, 30
	v_readlane_b32 s84, v8, 29
	v_readlane_b32 s85, v8, 31
	v_mul_f32_e32 v244, v70, v78
	v_mul_f32_e32 v245, v74, v79
	v_sub_f32_e32 v86, v244, v245
	v_mul_f32_e32 v244, v74, v78
	v_mul_f32_e32 v245, v70, v79
	v_add_f32_e32 v88, v244, v245
	v_pk_mul_f32 v[90:91], v[88:89], s[44:45] op_sel_hi:[0,1]
	v_pk_fma_f32 v[90:91], v[86:87], s[16:17], v[90:91] op_sel_hi:[0,1,1] neg_lo:[0,0,1] neg_hi:[0,0,1]
	v_pk_add_f32 v[56:57], v[56:57], v[90:91]
	v_pk_mul_f32 v[90:91], v[88:89], s[48:49] op_sel_hi:[0,1]
	v_pk_fma_f32 v[90:91], v[86:87], s[46:47], v[90:91] op_sel_hi:[0,1,1] neg_lo:[0,0,1] neg_hi:[0,0,1]
	v_pk_add_f32 v[54:55], v[54:55], v[90:91]
	v_pk_mul_f32 v[90:91], v[88:89], s[54:55] op_sel_hi:[0,1]
	v_pk_fma_f32 v[90:91], v[86:87], s[52:53], v[90:91] op_sel_hi:[0,1,1] neg_lo:[0,0,1] neg_hi:[0,0,1]
	v_pk_add_f32 v[52:53], v[52:53], v[90:91]
	v_pk_mul_f32 v[90:91], v[88:89], s[58:59] op_sel_hi:[0,1]
	v_pk_fma_f32 v[90:91], v[86:87], s[56:57], v[90:91] op_sel_hi:[0,1,1] neg_lo:[0,0,1] neg_hi:[0,0,1]
	v_pk_add_f32 v[50:51], v[50:51], v[90:91]
	v_pk_mul_f32 v[90:91], v[88:89], s[64:65] op_sel_hi:[0,1]
	v_pk_fma_f32 v[90:91], v[86:87], s[62:63], v[90:91] op_sel_hi:[0,1,1] neg_lo:[0,0,1] neg_hi:[0,0,1]
	v_pk_add_f32 v[58:59], v[58:59], v[90:91]
	v_pk_mul_f32 v[90:91], v[88:89], s[70:71] op_sel_hi:[0,1]
	v_pk_fma_f32 v[90:91], v[86:87], s[68:69], v[90:91] op_sel_hi:[0,1,1] neg_lo:[0,0,1] neg_hi:[0,0,1]
	v_pk_add_f32 v[60:61], v[60:61], v[90:91]
	v_pk_mul_f32 v[90:91], v[88:89], s[80:81] op_sel_hi:[0,1]
	v_pk_fma_f32 v[90:91], v[86:87], s[72:73], v[90:91] op_sel_hi:[0,1,1] neg_lo:[0,0,1] neg_hi:[0,0,1]
	v_pk_add_f32 v[64:65], v[64:65], v[90:91]
	v_pk_mul_f32 v[90:91], v[88:89], s[84:85] op_sel_hi:[0,1]
	v_pk_fma_f32 v[90:91], v[86:87], s[82:83], v[90:91] op_sel_hi:[0,1,1] neg_lo:[0,0,1] neg_hi:[0,0,1]
	v_pk_add_f32 v[62:63], v[62:63], v[90:91]
	v_readlane_b32 s16, v8, 32
	v_readlane_b32 s17, v8, 34
	v_readlane_b32 s44, v8, 33
	v_readlane_b32 s45, v8, 35
	v_readlane_b32 s46, v8, 36
	v_readlane_b32 s47, v8, 38
	v_readlane_b32 s48, v8, 37
	v_readlane_b32 s49, v8, 39
	v_readlane_b32 s52, v8, 40
	v_readlane_b32 s53, v8, 42
	v_readlane_b32 s54, v8, 41
	v_readlane_b32 s55, v8, 43
	v_readlane_b32 s56, v8, 44
	v_readlane_b32 s57, v8, 46
	v_readlane_b32 s58, v8, 45
	v_readlane_b32 s59, v8, 47
	v_readlane_b32 s62, v8, 48
	v_readlane_b32 s63, v8, 50
	v_readlane_b32 s64, v8, 49
	v_readlane_b32 s65, v8, 51
	v_readlane_b32 s68, v8, 52
	v_readlane_b32 s69, v8, 54
	v_readlane_b32 s70, v8, 53
	v_readlane_b32 s71, v8, 55
	v_readlane_b32 s72, v8, 56
	v_readlane_b32 s73, v8, 58
	v_readlane_b32 s80, v8, 57
	v_readlane_b32 s81, v8, 59
	v_readlane_b32 s82, v8, 60
	v_readlane_b32 s83, v8, 62
	v_readlane_b32 s84, v8, 61
	v_readlane_b32 s85, v8, 63
	v_mul_f32_e32 v244, v71, v80
	v_mul_f32_e32 v245, v75, v81
	v_sub_f32_e32 v86, v244, v245
	v_mul_f32_e32 v244, v75, v80
	v_mul_f32_e32 v245, v71, v81
	v_add_f32_e32 v88, v244, v245
	v_pk_mul_f32 v[90:91], v[88:89], s[44:45] op_sel_hi:[0,1]
; __device__ __forceinline__ void ph1_small(const Args& a, int tid, int wave, int lane, int G, int bid) {
;     ...
; #pragma unroll 8
;             for (int n = 0; n < 64; ++n) { const float cr = cre[((size_t)g * 16 + p) * 64 + n], ci = cim[((size_t)g * 16 + p) * 64 + n];
;                 const float pr = POW[(((size_t)g * 65 + tau) * 64 + n) * 2], pi = POW[(((size_t)g * 65 + tau) * 64 + n) * 2 + 1];
;                 const float er = cr * pr - ci * pi, ei = cr * pi + ci * pr;
;                 const f32x4* bp = (const f32x4*)(BBAR + ((size_t)g * 64 + n) * 32);
; #pragma unroll
;                 for (int q = 0; q < 8; ++q) { const f32x4 bb = bp[q]; s[2 * q] += er * bb[0] - ei * bb[1]; s[2 * q + 1] += er * bb[2] - ei * bb[3]; } }
	v_pk_fma_f32 v[90:91], v[86:87], s[16:17], v[90:91] op_sel_hi:[0,1,1] neg_lo:[0,0,1] neg_hi:[0,0,1]
	v_pk_add_f32 v[56:57], v[56:57], v[90:91]
	v_pk_mul_f32 v[90:91], v[88:89], s[48:49] op_sel_hi:[0,1]
	v_pk_fma_f32 v[90:91], v[86:87], s[46:47], v[90:91] op_sel_hi:[0,1,1] neg_lo:[0,0,1] neg_hi:[0,0,1]
	v_pk_add_f32 v[54:55], v[54:55], v[90:91]
	v_pk_mul_f32 v[90:91], v[88:89], s[54:55] op_sel_hi:[0,1]
	v_pk_fma_f32 v[90:91], v[86:87], s[52:53], v[90:91] op_sel_hi:[0,1,1] neg_lo:[0,0,1] neg_hi:[0,0,1]
	v_pk_add_f32 v[52:53], v[52:53], v[90:91]
	v_pk_mul_f32 v[90:91], v[88:89], s[58:59] op_sel_hi:[0,1]
	v_pk_fma_f32 v[90:91], v[86:87], s[56:57], v[90:91] op_sel_hi:[0,1,1] neg_lo:[0,0,1] neg_hi:[0,0,1]
	v_pk_add_f32 v[50:51], v[50:51], v[90:91]
	v_pk_mul_f32 v[90:91], v[88:89], s[64:65] op_sel_hi:[0,1]
	v_pk_fma_f32 v[90:91], v[86:87], s[62:63], v[90:91] op_sel_hi:[0,1,1] neg_lo:[0,0,1] neg_hi:[0,0,1]
	v_pk_add_f32 v[58:59], v[58:59], v[90:91]
	v_pk_mul_f32 v[90:91], v[88:89], s[70:71] op_sel_hi:[0,1]
	v_pk_fma_f32 v[90:91], v[86:87], s[68:69], v[90:91] op_sel_hi:[0,1,1] neg_lo:[0,0,1] neg_hi:[0,0,1]
	v_pk_add_f32 v[60:61], v[60:61], v[90:91]
	v_pk_mul_f32 v[90:91], v[88:89], s[80:81] op_sel_hi:[0,1]
	v_pk_fma_f32 v[90:91], v[86:87], s[72:73], v[90:91] op_sel_hi:[0,1,1] neg_lo:[0,0,1] neg_hi:[0,0,1]
	v_pk_add_f32 v[64:65], v[64:65], v[90:91]
	v_pk_mul_f32 v[90:91], v[88:89], s[84:85] op_sel_hi:[0,1]
	v_pk_fma_f32 v[90:91], v[86:87], s[82:83], v[90:91] op_sel_hi:[0,1,1] neg_lo:[0,0,1] neg_hi:[0,0,1]
	v_pk_add_f32 v[62:63], v[62:63], v[90:91]
	v_readlane_b32 s16, v9, 0
	v_readlane_b32 s17, v9, 2
	v_readlane_b32 s44, v9, 1
	v_readlane_b32 s45, v9, 3
	v_readlane_b32 s46, v9, 4
	v_readlane_b32 s47, v9, 6
	v_readlane_b32 s48, v9, 5
	v_readlane_b32 s49, v9, 7
	v_readlane_b32 s52, v9, 8
	v_readlane_b32 s53, v9, 10
	v_readlane_b32 s54, v9, 9
	v_readlane_b32 s55, v9, 11
	v_readlane_b32 s56, v9, 12
	v_readlane_b32 s57, v9, 14
	v_readlane_b32 s58, v9, 13
	v_readlane_b32 s59, v9, 15
	v_readlane_b32 s62, v9, 16
	v_readlane_b32 s63, v9, 18
	v_readlane_b32 s64, v9, 17
	v_readlane_b32 s65, v9, 19
	v_readlane_b32 s68, v9, 20
	v_readlane_b32 s69, v9, 22
	v_readlane_b32 s70, v9, 21
	v_readlane_b32 s71, v9, 23
	v_readlane_b32 s72, v9, 24
	v_readlane_b32 s73, v9, 26
	v_readlane_b32 s80, v9, 25
	v_readlane_b32 s81, v9, 27
	v_readlane_b32 s82, v9, 28
	v_readlane_b32 s83, v9, 30
	v_readlane_b32 s84, v9, 29
	v_readlane_b32 s85, v9, 31
	v_mul_f32_e32 v244, v72, v82
	v_mul_f32_e32 v245, v76, v83
	v_sub_f32_e32 v86, v244, v245
	v_mul_f32_e32 v244, v76, v82
	v_mul_f32_e32 v245, v72, v83
	v_add_f32_e32 v88, v244, v245
	v_pk_mul_f32 v[90:91], v[88:89], s[44:45] op_sel_hi:[0,1]
	v_pk_fma_f32 v[90:91], v[86:87], s[16:17], v[90:91] op_sel_hi:[0,1,1] neg_lo:[0,0,1] neg_hi:[0,0,1]
	v_pk_add_f32 v[56:57], v[56:57], v[90:91]
	v_pk_mul_f32 v[90:91], v[88:89], s[48:49] op_sel_hi:[0,1]
	v_pk_fma_f32 v[90:91], v[86:87], s[46:47], v[90:91] op_sel_hi:[0,1,1] neg_lo:[0,0,1] neg_hi:[0,0,1]
	v_pk_add_f32 v[54:55], v[54:55], v[90:91]
	v_pk_mul_f32 v[90:91], v[88:89], s[54:55] op_sel_hi:[0,1]
	v_pk_fma_f32 v[90:91], v[86:87], s[52:53], v[90:91] op_sel_hi:[0,1,1] neg_lo:[0,0,1] neg_hi:[0,0,1]
	v_pk_add_f32 v[52:53], v[52:53], v[90:91]
	v_pk_mul_f32 v[90:91], v[88:89], s[58:59] op_sel_hi:[0,1]
	v_pk_fma_f32 v[90:91], v[86:87], s[56:57], v[90:91] op_sel_hi:[0,1,1] neg_lo:[0,0,1] neg_hi:[0,0,1]
	v_pk_add_f32 v[50:51], v[50:51], v[90:91]
	v_pk_mul_f32 v[90:91], v[88:89], s[64:65] op_sel_hi:[0,1]
	v_pk_fma_f32 v[90:91], v[86:87], s[62:63], v[90:91] op_sel_hi:[0,1,1] neg_lo:[0,0,1] neg_hi:[0,0,1]
	v_pk_add_f32 v[58:59], v[58:59], v[90:91]
	v_pk_mul_f32 v[90:91], v[88:89], s[70:71] op_sel_hi:[0,1]
	v_pk_fma_f32 v[90:91], v[86:87], s[68:69], v[90:91] op_sel_hi:[0,1,1] neg_lo:[0,0,1] neg_hi:[0,0,1]
	v_pk_add_f32 v[60:61], v[60:61], v[90:91]
	v_pk_mul_f32 v[90:91], v[88:89], s[80:81] op_sel_hi:[0,1]
	v_pk_fma_f32 v[90:91], v[86:87], s[72:73], v[90:91] op_sel_hi:[0,1,1] neg_lo:[0,0,1] neg_hi:[0,0,1]
	v_pk_add_f32 v[64:65], v[64:65], v[90:91]
	v_pk_mul_f32 v[90:91], v[88:89], s[84:85] op_sel_hi:[0,1]
	v_pk_fma_f32 v[90:91], v[86:87], s[82:83], v[90:91] op_sel_hi:[0,1,1] neg_lo:[0,0,1] neg_hi:[0,0,1]
	v_pk_add_f32 v[62:63], v[62:63], v[90:91]
	v_readlane_b32 s16, v9, 32
	v_readlane_b32 s17, v9, 34
	v_readlane_b32 s44, v9, 33
	v_readlane_b32 s45, v9, 35
	v_readlane_b32 s46, v9, 36
	v_readlane_b32 s47, v9, 38
	v_readlane_b32 s48, v9, 37
	v_readlane_b32 s49, v9, 39
	v_readlane_b32 s52, v9, 40
	v_readlane_b32 s53, v9, 42
	v_readlane_b32 s54, v9, 41
	v_readlane_b32 s55, v9, 43
	v_readlane_b32 s56, v9, 44
	v_readlane_b32 s57, v9, 46
	v_readlane_b32 s58, v9, 45
	v_readlane_b32 s59, v9, 47
	v_readlane_b32 s62, v9, 48
	v_readlane_b32 s63, v9, 50
	v_readlane_b32 s64, v9, 49
	v_readlane_b32 s65, v9, 51
	v_readlane_b32 s68, v9, 52
	v_readlane_b32 s69, v9, 54
	v_readlane_b32 s70, v9, 53
	v_readlane_b32 s71, v9, 55
	v_readlane_b32 s72, v9, 56
	v_readlane_b32 s73, v9, 58
	v_readlane_b32 s80, v9, 57
	v_readlane_b32 s81, v9, 59
	v_readlane_b32 s82, v9, 60
	v_readlane_b32 s83, v9, 62
	v_readlane_b32 s84, v9, 61
	v_readlane_b32 s85, v9, 63
	v_mul_f32_e32 v244, v73, v84
	v_mul_f32_e32 v245, v77, v85
	v_sub_f32_e32 v86, v244, v245
	v_mul_f32_e32 v244, v77, v84
	v_mul_f32_e32 v245, v73, v85
	v_add_f32_e32 v88, v244, v245
	v_pk_mul_f32 v[90:91], v[88:89], s[44:45] op_sel_hi:[0,1]
	v_pk_fma_f32 v[90:91], v[86:87], s[16:17], v[90:91] op_sel_hi:[0,1,1] neg_lo:[0,0,1] neg_hi:[0,0,1]
	v_pk_add_f32 v[56:57], v[56:57], v[90:91]
	v_pk_mul_f32 v[90:91], v[88:89], s[48:49] op_sel_hi:[0,1]
; __device__ __forceinline__ void ph1_small(const Args& a, int tid, int wave, int lane, int G, int bid) {
;     ...
; #pragma unroll 8
;             for (int n = 0; n < 64; ++n) { const float cr = cre[((size_t)g * 16 + p) * 64 + n], ci = cim[((size_t)g * 16 + p) * 64 + n];
;                 const float pr = POW[(((size_t)g * 65 + tau) * 64 + n) * 2], pi = POW[(((size_t)g * 65 + tau) * 64 + n) * 2 + 1];
;                 const float er = cr * pr - ci * pi, ei = cr * pi + ci * pr;
;                 const f32x4* bp = (const f32x4*)(BBAR + ((size_t)g * 64 + n) * 32);
; #pragma unroll
;                 for (int q = 0; q < 8; ++q) { const f32x4 bb = bp[q]; s[2 * q] += er * bb[0] - ei * bb[1]; s[2 * q + 1] += er * bb[2] - ei * bb[3]; } }
	v_pk_fma_f32 v[90:91], v[86:87], s[46:47], v[90:91] op_sel_hi:[0,1,1] neg_lo:[0,0,1] neg_hi:[0,0,1]
	v_pk_add_f32 v[54:55], v[54:55], v[90:91]
	v_pk_mul_f32 v[90:91], v[88:89], s[54:55] op_sel_hi:[0,1]
	v_pk_fma_f32 v[90:91], v[86:87], s[52:53], v[90:91] op_sel_hi:[0,1,1] neg_lo:[0,0,1] neg_hi:[0,0,1]
	v_pk_add_f32 v[52:53], v[52:53], v[90:91]
	v_pk_mul_f32 v[90:91], v[88:89], s[58:59] op_sel_hi:[0,1]
	v_pk_fma_f32 v[90:91], v[86:87], s[56:57], v[90:91] op_sel_hi:[0,1,1] neg_lo:[0,0,1] neg_hi:[0,0,1]
	v_pk_add_f32 v[50:51], v[50:51], v[90:91]
	v_pk_mul_f32 v[90:91], v[88:89], s[64:65] op_sel_hi:[0,1]
	v_pk_fma_f32 v[90:91], v[86:87], s[62:63], v[90:91] op_sel_hi:[0,1,1] neg_lo:[0,0,1] neg_hi:[0,0,1]
	v_pk_add_f32 v[58:59], v[58:59], v[90:91]
	v_pk_mul_f32 v[90:91], v[88:89], s[70:71] op_sel_hi:[0,1]
	v_pk_fma_f32 v[90:91], v[86:87], s[68:69], v[90:91] op_sel_hi:[0,1,1] neg_lo:[0,0,1] neg_hi:[0,0,1]
	v_pk_add_f32 v[60:61], v[60:61], v[90:91]
	v_pk_mul_f32 v[90:91], v[88:89], s[80:81] op_sel_hi:[0,1]
	v_pk_fma_f32 v[90:91], v[86:87], s[72:73], v[90:91] op_sel_hi:[0,1,1] neg_lo:[0,0,1] neg_hi:[0,0,1]
	v_pk_add_f32 v[64:65], v[64:65], v[90:91]
	v_pk_mul_f32 v[90:91], v[88:89], s[84:85] op_sel_hi:[0,1]
	v_pk_fma_f32 v[90:91], v[86:87], s[82:83], v[90:91] op_sel_hi:[0,1,1] neg_lo:[0,0,1] neg_hi:[0,0,1]
	v_pk_add_f32 v[62:63], v[62:63], v[90:91]
	global_load_dwordx4 v[70:73], v[44:45], off offset:80
	global_load_dwordx4 v[74:77], v[42:43], off offset:80
	global_load_dwordx4 v[78:81], v40, s[100:101] offset:160
	global_load_dwordx4 v[82:85], v40, s[100:101] offset:176
	s_waitcnt vmcnt(4)
	v_readlane_b32 s16, v10, 0
	v_readlane_b32 s17, v10, 2
	v_readlane_b32 s44, v10, 1
	v_readlane_b32 s45, v10, 3
	v_readlane_b32 s46, v10, 4
	v_readlane_b32 s47, v10, 6
	v_readlane_b32 s48, v10, 5
	v_readlane_b32 s49, v10, 7
	v_readlane_b32 s52, v10, 8
	v_readlane_b32 s53, v10, 10
	v_readlane_b32 s54, v10, 9
	v_readlane_b32 s55, v10, 11
	v_readlane_b32 s56, v10, 12
	v_readlane_b32 s57, v10, 14
	v_readlane_b32 s58, v10, 13
	v_readlane_b32 s59, v10, 15
	v_readlane_b32 s62, v10, 16
	v_readlane_b32 s63, v10, 18
	v_readlane_b32 s64, v10, 17
	v_readlane_b32 s65, v10, 19
	v_readlane_b32 s68, v10, 20
	v_readlane_b32 s69, v10, 22
	v_readlane_b32 s70, v10, 21
	v_readlane_b32 s71, v10, 23
	v_readlane_b32 s72, v10, 24
	v_readlane_b32 s73, v10, 26
	v_readlane_b32 s80, v10, 25
	v_readlane_b32 s81, v10, 27
	v_readlane_b32 s82, v10, 28
	v_readlane_b32 s83, v10, 30
	v_readlane_b32 s84, v10, 29
	v_readlane_b32 s85, v10, 31
	v_mul_f32_e32 v244, v18, v26
	v_mul_f32_e32 v245, v22, v27
	v_sub_f32_e32 v86, v244, v245
	v_mul_f32_e32 v244, v22, v26
	v_mul_f32_e32 v245, v18, v27
	v_add_f32_e32 v88, v244, v245
	v_pk_mul_f32 v[90:91], v[88:89], s[44:45] op_sel_hi:[0,1]
	v_pk_fma_f32 v[90:91], v[86:87], s[16:17], v[90:91] op_sel_hi:[0,1,1] neg_lo:[0,0,1] neg_hi:[0,0,1]
	v_pk_add_f32 v[56:57], v[56:57], v[90:91]
	v_pk_mul_f32 v[90:91], v[88:89], s[48:49] op_sel_hi:[0,1]
	v_pk_fma_f32 v[90:91], v[86:87], s[46:47], v[90:91] op_sel_hi:[0,1,1] neg_lo:[0,0,1] neg_hi:[0,0,1]
	v_pk_add_f32 v[54:55], v[54:55], v[90:91]
	v_pk_mul_f32 v[90:91], v[88:89], s[54:55] op_sel_hi:[0,1]
	v_pk_fma_f32 v[90:91], v[86:87], s[52:53], v[90:91] op_sel_hi:[0,1,1] neg_lo:[0,0,1] neg_hi:[0,0,1]
	v_pk_add_f32 v[52:53], v[52:53], v[90:91]
	v_pk_mul_f32 v[90:91], v[88:89], s[58:59] op_sel_hi:[0,1]
	v_pk_fma_f32 v[90:91], v[86:87], s[56:57], v[90:91] op_sel_hi:[0,1,1] neg_lo:[0,0,1] neg_hi:[0,0,1]
	v_pk_add_f32 v[50:51], v[50:51], v[90:91]
	v_pk_mul_f32 v[90:91], v[88:89], s[64:65] op_sel_hi:[0,1]
	v_pk_fma_f32 v[90:91], v[86:87], s[62:63], v[90:91] op_sel_hi:[0,1,1] neg_lo:[0,0,1] neg_hi:[0,0,1]
	v_pk_add_f32 v[58:59], v[58:59], v[90:91]
	v_pk_mul_f32 v[90:91], v[88:89], s[70:71] op_sel_hi:[0,1]
	v_pk_fma_f32 v[90:91], v[86:87], s[68:69], v[90:91] op_sel_hi:[0,1,1] neg_lo:[0,0,1] neg_hi:[0,0,1]
	v_pk_add_f32 v[60:61], v[60:61], v[90:91]
	v_pk_mul_f32 v[90:91], v[88:89], s[80:81] op_sel_hi:[0,1]
	v_pk_fma_f32 v[90:91], v[86:87], s[72:73], v[90:91] op_sel_hi:[0,1,1] neg_lo:[0,0,1] neg_hi:[0,0,1]
	v_pk_add_f32 v[64:65], v[64:65], v[90:91]
	v_pk_mul_f32 v[90:91], v[88:89], s[84:85] op_sel_hi:[0,1]
	v_pk_fma_f32 v[90:91], v[86:87], s[82:83], v[90:91] op_sel_hi:[0,1,1] neg_lo:[0,0,1] neg_hi:[0,0,1]
	v_pk_add_f32 v[62:63], v[62:63], v[90:91]
	v_readlane_b32 s16, v10, 32
	v_readlane_b32 s17, v10, 34
	v_readlane_b32 s44, v10, 33
	v_readlane_b32 s45, v10, 35
	v_readlane_b32 s46, v10, 36
	v_readlane_b32 s47, v10, 38
	v_readlane_b32 s48, v10, 37
	v_readlane_b32 s49, v10, 39
	v_readlane_b32 s52, v10, 40
	v_readlane_b32 s53, v10, 42
	v_readlane_b32 s54, v10, 41
	v_readlane_b32 s55, v10, 43
	v_readlane_b32 s56, v10, 44
	v_readlane_b32 s57, v10, 46
	v_readlane_b32 s58, v10, 45
	v_readlane_b32 s59, v10, 47
	v_readlane_b32 s62, v10, 48
	v_readlane_b32 s63, v10, 50
	v_readlane_b32 s64, v10, 49
	v_readlane_b32 s65, v10, 51
	v_readlane_b32 s68, v10, 52
	v_readlane_b32 s69, v10, 54
	v_readlane_b32 s70, v10, 53
	v_readlane_b32 s71, v10, 55
	v_readlane_b32 s72, v10, 56
	v_readlane_b32 s73, v10, 58
	v_readlane_b32 s80, v10, 57
	v_readlane_b32 s81, v10, 59
	v_readlane_b32 s82, v10, 60
	v_readlane_b32 s83, v10, 62
	v_readlane_b32 s84, v10, 61
	v_readlane_b32 s85, v10, 63
	v_mul_f32_e32 v244, v19, v28
	v_mul_f32_e32 v245, v23, v29
	v_sub_f32_e32 v86, v244, v245
	v_mul_f32_e32 v244, v23, v28
	v_mul_f32_e32 v245, v19, v29
	v_add_f32_e32 v88, v244, v245
	v_pk_mul_f32 v[90:91], v[88:89], s[44:45] op_sel_hi:[0,1]
	v_pk_fma_f32 v[90:91], v[86:87], s[16:17], v[90:91] op_sel_hi:[0,1,1] neg_lo:[0,0,1] neg_hi:[0,0,1]
	v_pk_add_f32 v[56:57], v[56:57], v[90:91]
; __device__ __forceinline__ void ph1_small(const Args& a, int tid, int wave, int lane, int G, int bid) {
;     ...
; #pragma unroll 8
;             for (int n = 0; n < 64; ++n) { const float cr = cre[((size_t)g * 16 + p) * 64 + n], ci = cim[((size_t)g * 16 + p) * 64 + n];
;                 const float pr = POW[(((size_t)g * 65 + tau) * 64 + n) * 2], pi = POW[(((size_t)g * 65 + tau) * 64 + n) * 2 + 1];
;                 const float er = cr * pr - ci * pi, ei = cr * pi + ci * pr;
;                 const f32x4* bp = (const f32x4*)(BBAR + ((size_t)g * 64 + n) * 32);
; #pragma unroll
;                 for (int q = 0; q < 8; ++q) { const f32x4 bb = bp[q]; s[2 * q] += er * bb[0] - ei * bb[1]; s[2 * q + 1] += er * bb[2] - ei * bb[3]; } }
	v_pk_mul_f32 v[90:91], v[88:89], s[48:49] op_sel_hi:[0,1]
	v_pk_fma_f32 v[90:91], v[86:87], s[46:47], v[90:91] op_sel_hi:[0,1,1] neg_lo:[0,0,1] neg_hi:[0,0,1]
	v_pk_add_f32 v[54:55], v[54:55], v[90:91]
	v_pk_mul_f32 v[90:91], v[88:89], s[54:55] op_sel_hi:[0,1]
	v_pk_fma_f32 v[90:91], v[86:87], s[52:53], v[90:91] op_sel_hi:[0,1,1] neg_lo:[0,0,1] neg_hi:[0,0,1]
	v_pk_add_f32 v[52:53], v[52:53], v[90:91]
	v_pk_mul_f32 v[90:91], v[88:89], s[58:59] op_sel_hi:[0,1]
	v_pk_fma_f32 v[90:91], v[86:87], s[56:57], v[90:91] op_sel_hi:[0,1,1] neg_lo:[0,0,1] neg_hi:[0,0,1]
	v_pk_add_f32 v[50:51], v[50:51], v[90:91]
	v_pk_mul_f32 v[90:91], v[88:89], s[64:65] op_sel_hi:[0,1]
	v_pk_fma_f32 v[90:91], v[86:87], s[62:63], v[90:91] op_sel_hi:[0,1,1] neg_lo:[0,0,1] neg_hi:[0,0,1]
	v_pk_add_f32 v[58:59], v[58:59], v[90:91]
	v_pk_mul_f32 v[90:91], v[88:89], s[70:71] op_sel_hi:[0,1]
	v_pk_fma_f32 v[90:91], v[86:87], s[68:69], v[90:91] op_sel_hi:[0,1,1] neg_lo:[0,0,1] neg_hi:[0,0,1]
	v_pk_add_f32 v[60:61], v[60:61], v[90:91]
	v_pk_mul_f32 v[90:91], v[88:89], s[80:81] op_sel_hi:[0,1]
	v_pk_fma_f32 v[90:91], v[86:87], s[72:73], v[90:91] op_sel_hi:[0,1,1] neg_lo:[0,0,1] neg_hi:[0,0,1]
	v_pk_add_f32 v[64:65], v[64:65], v[90:91]
	v_pk_mul_f32 v[90:91], v[88:89], s[84:85] op_sel_hi:[0,1]
	v_pk_fma_f32 v[90:91], v[86:87], s[82:83], v[90:91] op_sel_hi:[0,1,1] neg_lo:[0,0,1] neg_hi:[0,0,1]
	v_pk_add_f32 v[62:63], v[62:63], v[90:91]
	v_readlane_b32 s16, v11, 0
	v_readlane_b32 s17, v11, 2
	v_readlane_b32 s44, v11, 1
	v_readlane_b32 s45, v11, 3
	v_readlane_b32 s46, v11, 4
	v_readlane_b32 s47, v11, 6
	v_readlane_b32 s48, v11, 5
	v_readlane_b32 s49, v11, 7
	v_readlane_b32 s52, v11, 8
	v_readlane_b32 s53, v11, 10
	v_readlane_b32 s54, v11, 9
	v_readlane_b32 s55, v11, 11
	v_readlane_b32 s56, v11, 12
	v_readlane_b32 s57, v11, 14
	v_readlane_b32 s58, v11, 13
	v_readlane_b32 s59, v11, 15
	v_readlane_b32 s62, v11, 16
	v_readlane_b32 s63, v11, 18
	v_readlane_b32 s64, v11, 17
	v_readlane_b32 s65, v11, 19
	v_readlane_b32 s68, v11, 20
	v_readlane_b32 s69, v11, 22
	v_readlane_b32 s70, v11, 21
	v_readlane_b32 s71, v11, 23
	v_readlane_b32 s72, v11, 24
	v_readlane_b32 s73, v11, 26
	v_readlane_b32 s80, v11, 25
	v_readlane_b32 s81, v11, 27
	v_readlane_b32 s82, v11, 28
	v_readlane_b32 s83, v11, 30
	v_readlane_b32 s84, v11, 29
	v_readlane_b32 s85, v11, 31
	v_mul_f32_e32 v244, v20, v46
	v_mul_f32_e32 v245, v24, v47
	v_sub_f32_e32 v86, v244, v245
	v_mul_f32_e32 v244, v24, v46
	v_mul_f32_e32 v245, v20, v47
	v_add_f32_e32 v88, v244, v245
	v_pk_mul_f32 v[90:91], v[88:89], s[44:45] op_sel_hi:[0,1]
	v_pk_fma_f32 v[90:91], v[86:87], s[16:17], v[90:91] op_sel_hi:[0,1,1] neg_lo:[0,0,1] neg_hi:[0,0,1]
	v_pk_add_f32 v[56:57], v[56:57], v[90:91]
	v_pk_mul_f32 v[90:91], v[88:89], s[48:49] op_sel_hi:[0,1]
	v_pk_fma_f32 v[90:91], v[86:87], s[46:47], v[90:91] op_sel_hi:[0,1,1] neg_lo:[0,0,1] neg_hi:[0,0,1]
	v_pk_add_f32 v[54:55], v[54:55], v[90:91]
	v_pk_mul_f32 v[90:91], v[88:89], s[54:55] op_sel_hi:[0,1]
	v_pk_fma_f32 v[90:91], v[86:87], s[52:53], v[90:91] op_sel_hi:[0,1,1] neg_lo:[0,0,1] neg_hi:[0,0,1]
	v_pk_add_f32 v[52:53], v[52:53], v[90:91]
	v_pk_mul_f32 v[90:91], v[88:89], s[58:59] op_sel_hi:[0,1]
	v_pk_fma_f32 v[90:91], v[86:87], s[56:57], v[90:91] op_sel_hi:[0,1,1] neg_lo:[0,0,1] neg_hi:[0,0,1]
	v_pk_add_f32 v[50:51], v[50:51], v[90:91]
	v_pk_mul_f32 v[90:91], v[88:89], s[64:65] op_sel_hi:[0,1]
	v_pk_fma_f32 v[90:91], v[86:87], s[62:63], v[90:91] op_sel_hi:[0,1,1] neg_lo:[0,0,1] neg_hi:[0,0,1]
	v_pk_add_f32 v[58:59], v[58:59], v[90:91]
	v_pk_mul_f32 v[90:91], v[88:89], s[70:71] op_sel_hi:[0,1]
	v_pk_fma_f32 v[90:91], v[86:87], s[68:69], v[90:91] op_sel_hi:[0,1,1] neg_lo:[0,0,1] neg_hi:[0,0,1]
	v_pk_add_f32 v[60:61], v[60:61], v[90:91]
	v_pk_mul_f32 v[90:91], v[88:89], s[80:81] op_sel_hi:[0,1]
	v_pk_fma_f32 v[90:91], v[86:87], s[72:73], v[90:91] op_sel_hi:[0,1,1] neg_lo:[0,0,1] neg_hi:[0,0,1]
	v_pk_add_f32 v[64:65], v[64:65], v[90:91]
	v_pk_mul_f32 v[90:91], v[88:89], s[84:85] op_sel_hi:[0,1]
	v_pk_fma_f32 v[90:91], v[86:87], s[82:83], v[90:91] op_sel_hi:[0,1,1] neg_lo:[0,0,1] neg_hi:[0,0,1]
	v_pk_add_f32 v[62:63], v[62:63], v[90:91]
	v_readlane_b32 s16, v11, 32
	v_readlane_b32 s17, v11, 34
	v_readlane_b32 s44, v11, 33
	v_readlane_b32 s45, v11, 35
	v_readlane_b32 s46, v11, 36
	v_readlane_b32 s47, v11, 38
	v_readlane_b32 s48, v11, 37
	v_readlane_b32 s49, v11, 39
	v_readlane_b32 s52, v11, 40
	v_readlane_b32 s53, v11, 42
	v_readlane_b32 s54, v11, 41
	v_readlane_b32 s55, v11, 43
	v_readlane_b32 s56, v11, 44
	v_readlane_b32 s57, v11, 46
	v_readlane_b32 s58, v11, 45
	v_readlane_b32 s59, v11, 47
	v_readlane_b32 s62, v11, 48
	v_readlane_b32 s63, v11, 50
	v_readlane_b32 s64, v11, 49
	v_readlane_b32 s65, v11, 51
	v_readlane_b32 s68, v11, 52
	v_readlane_b32 s69, v11, 54
	v_readlane_b32 s70, v11, 53
	v_readlane_b32 s71, v11, 55
	v_readlane_b32 s72, v11, 56
	v_readlane_b32 s73, v11, 58
	v_readlane_b32 s80, v11, 57
	v_readlane_b32 s81, v11, 59
	v_readlane_b32 s82, v11, 60
	v_readlane_b32 s83, v11, 62
	v_readlane_b32 s84, v11, 61
	v_readlane_b32 s85, v11, 63
	v_mul_f32_e32 v244, v21, v48
	v_mul_f32_e32 v245, v25, v49
	v_sub_f32_e32 v86, v244, v245
	v_mul_f32_e32 v244, v25, v48
	v_mul_f32_e32 v245, v21, v49
	v_add_f32_e32 v88, v244, v245
	v_pk_mul_f32 v[90:91], v[88:89], s[44:45] op_sel_hi:[0,1]
	v_pk_fma_f32 v[90:91], v[86:87], s[16:17], v[90:91] op_sel_hi:[0,1,1] neg_lo:[0,0,1] neg_hi:[0,0,1]
	v_pk_add_f32 v[56:57], v[56:57], v[90:91]
	v_pk_mul_f32 v[90:91], v[88:89], s[48:49] op_sel_hi:[0,1]
	v_pk_fma_f32 v[90:91], v[86:87], s[46:47], v[90:91] op_sel_hi:[0,1,1] neg_lo:[0,0,1] neg_hi:[0,0,1]
	v_pk_add_f32 v[54:55], v[54:55], v[90:91]
; __device__ __forceinline__ void ph1_small(const Args& a, int tid, int wave, int lane, int G, int bid) {
;     ...
; #pragma unroll 8
;             for (int n = 0; n < 64; ++n) { const float cr = cre[((size_t)g * 16 + p) * 64 + n], ci = cim[((size_t)g * 16 + p) * 64 + n];
;                 const float pr = POW[(((size_t)g * 65 + tau) * 64 + n) * 2], pi = POW[(((size_t)g * 65 + tau) * 64 + n) * 2 + 1];
;                 const float er = cr * pr - ci * pi, ei = cr * pi + ci * pr;
;                 const f32x4* bp = (const f32x4*)(BBAR + ((size_t)g * 64 + n) * 32);
; #pragma unroll
;                 for (int q = 0; q < 8; ++q) { const f32x4 bb = bp[q]; s[2 * q] += er * bb[0] - ei * bb[1]; s[2 * q + 1] += er * bb[2] - ei * bb[3]; } }
	v_pk_mul_f32 v[90:91], v[88:89], s[54:55] op_sel_hi:[0,1]
	v_pk_fma_f32 v[90:91], v[86:87], s[52:53], v[90:91] op_sel_hi:[0,1,1] neg_lo:[0,0,1] neg_hi:[0,0,1]
	v_pk_add_f32 v[52:53], v[52:53], v[90:91]
	v_pk_mul_f32 v[90:91], v[88:89], s[58:59] op_sel_hi:[0,1]
	v_pk_fma_f32 v[90:91], v[86:87], s[56:57], v[90:91] op_sel_hi:[0,1,1] neg_lo:[0,0,1] neg_hi:[0,0,1]
	v_pk_add_f32 v[50:51], v[50:51], v[90:91]
	v_pk_mul_f32 v[90:91], v[88:89], s[64:65] op_sel_hi:[0,1]
	v_pk_fma_f32 v[90:91], v[86:87], s[62:63], v[90:91] op_sel_hi:[0,1,1] neg_lo:[0,0,1] neg_hi:[0,0,1]
	v_pk_add_f32 v[58:59], v[58:59], v[90:91]
	v_pk_mul_f32 v[90:91], v[88:89], s[70:71] op_sel_hi:[0,1]
	v_pk_fma_f32 v[90:91], v[86:87], s[68:69], v[90:91] op_sel_hi:[0,1,1] neg_lo:[0,0,1] neg_hi:[0,0,1]
	v_pk_add_f32 v[60:61], v[60:61], v[90:91]
	v_pk_mul_f32 v[90:91], v[88:89], s[80:81] op_sel_hi:[0,1]
	v_pk_fma_f32 v[90:91], v[86:87], s[72:73], v[90:91] op_sel_hi:[0,1,1] neg_lo:[0,0,1] neg_hi:[0,0,1]
	v_pk_add_f32 v[64:65], v[64:65], v[90:91]
	v_pk_mul_f32 v[90:91], v[88:89], s[84:85] op_sel_hi:[0,1]
	v_pk_fma_f32 v[90:91], v[86:87], s[82:83], v[90:91] op_sel_hi:[0,1,1] neg_lo:[0,0,1] neg_hi:[0,0,1]
	v_pk_add_f32 v[62:63], v[62:63], v[90:91]
	global_load_dwordx4 v[18:21], v[44:45], off offset:96
	global_load_dwordx4 v[22:25], v[42:43], off offset:96
	global_load_dwordx4 v[26:29], v40, s[100:101] offset:192
	global_load_dwordx4 v[46:49], v40, s[100:101] offset:208
	s_waitcnt vmcnt(4)
	v_readlane_b32 s16, v12, 0
	v_readlane_b32 s17, v12, 2
	v_readlane_b32 s44, v12, 1
	v_readlane_b32 s45, v12, 3
	v_readlane_b32 s46, v12, 4
	v_readlane_b32 s47, v12, 6
	v_readlane_b32 s48, v12, 5
	v_readlane_b32 s49, v12, 7
	v_readlane_b32 s52, v12, 8
	v_readlane_b32 s53, v12, 10
	v_readlane_b32 s54, v12, 9
	v_readlane_b32 s55, v12, 11
	v_readlane_b32 s56, v12, 12
	v_readlane_b32 s57, v12, 14
	v_readlane_b32 s58, v12, 13
	v_readlane_b32 s59, v12, 15
	v_readlane_b32 s62, v12, 16
	v_readlane_b32 s63, v12, 18
	v_readlane_b32 s64, v12, 17
	v_readlane_b32 s65, v12, 19
	v_readlane_b32 s68, v12, 20
	v_readlane_b32 s69, v12, 22
	v_readlane_b32 s70, v12, 21
	v_readlane_b32 s71, v12, 23
	v_readlane_b32 s72, v12, 24
	v_readlane_b32 s73, v12, 26
	v_readlane_b32 s80, v12, 25
	v_readlane_b32 s81, v12, 27
	v_readlane_b32 s82, v12, 28
	v_readlane_b32 s83, v12, 30
	v_readlane_b32 s84, v12, 29
	v_readlane_b32 s85, v12, 31
	v_mul_f32_e32 v244, v70, v78
	v_mul_f32_e32 v245, v74, v79
	v_sub_f32_e32 v86, v244, v245
	v_mul_f32_e32 v244, v74, v78
	v_mul_f32_e32 v245, v70, v79
	v_add_f32_e32 v88, v244, v245
	v_pk_mul_f32 v[90:91], v[88:89], s[44:45] op_sel_hi:[0,1]
	v_pk_fma_f32 v[90:91], v[86:87], s[16:17], v[90:91] op_sel_hi:[0,1,1] neg_lo:[0,0,1] neg_hi:[0,0,1]
	v_pk_add_f32 v[56:57], v[56:57], v[90:91]
	v_pk_mul_f32 v[90:91], v[88:89], s[48:49] op_sel_hi:[0,1]
	v_pk_fma_f32 v[90:91], v[86:87], s[46:47], v[90:91] op_sel_hi:[0,1,1] neg_lo:[0,0,1] neg_hi:[0,0,1]
	v_pk_add_f32 v[54:55], v[54:55], v[90:91]
	v_pk_mul_f32 v[90:91], v[88:89], s[54:55] op_sel_hi:[0,1]
	v_pk_fma_f32 v[90:91], v[86:87], s[52:53], v[90:91] op_sel_hi:[0,1,1] neg_lo:[0,0,1] neg_hi:[0,0,1]
	v_pk_add_f32 v[52:53], v[52:53], v[90:91]
	v_pk_mul_f32 v[90:91], v[88:89], s[58:59] op_sel_hi:[0,1]
	v_pk_fma_f32 v[90:91], v[86:87], s[56:57], v[90:91] op_sel_hi:[0,1,1] neg_lo:[0,0,1] neg_hi:[0,0,1]
	v_pk_add_f32 v[50:51], v[50:51], v[90:91]
	v_pk_mul_f32 v[90:91], v[88:89], s[64:65] op_sel_hi:[0,1]
	v_pk_fma_f32 v[90:91], v[86:87], s[62:63], v[90:91] op_sel_hi:[0,1,1] neg_lo:[0,0,1] neg_hi:[0,0,1]
	v_pk_add_f32 v[58:59], v[58:59], v[90:91]
	v_pk_mul_f32 v[90:91], v[88:89], s[70:71] op_sel_hi:[0,1]
	v_pk_fma_f32 v[90:91], v[86:87], s[68:69], v[90:91] op_sel_hi:[0,1,1] neg_lo:[0,0,1] neg_hi:[0,0,1]
	v_pk_add_f32 v[60:61], v[60:61], v[90:91]
	v_pk_mul_f32 v[90:91], v[88:89], s[80:81] op_sel_hi:[0,1]
	v_pk_fma_f32 v[90:91], v[86:87], s[72:73], v[90:91] op_sel_hi:[0,1,1] neg_lo:[0,0,1] neg_hi:[0,0,1]
	v_pk_add_f32 v[64:65], v[64:65], v[90:91]
	v_pk_mul_f32 v[90:91], v[88:89], s[84:85] op_sel_hi:[0,1]
	v_pk_fma_f32 v[90:91], v[86:87], s[82:83], v[90:91] op_sel_hi:[0,1,1] neg_lo:[0,0,1] neg_hi:[0,0,1]
	v_pk_add_f32 v[62:63], v[62:63], v[90:91]
	v_readlane_b32 s16, v12, 32
	v_readlane_b32 s17, v12, 34
	v_readlane_b32 s44, v12, 33
	v_readlane_b32 s45, v12, 35
	v_readlane_b32 s46, v12, 36
	v_readlane_b32 s47, v12, 38
	v_readlane_b32 s48, v12, 37
	v_readlane_b32 s49, v12, 39
	v_readlane_b32 s52, v12, 40
	v_readlane_b32 s53, v12, 42
	v_readlane_b32 s54, v12, 41
	v_readlane_b32 s55, v12, 43
	v_readlane_b32 s56, v12, 44
	v_readlane_b32 s57, v12, 46
	v_readlane_b32 s58, v12, 45
	v_readlane_b32 s59, v12, 47
	v_readlane_b32 s62, v12, 48
	v_readlane_b32 s63, v12, 50
	v_readlane_b32 s64, v12, 49
	v_readlane_b32 s65, v12, 51
	v_readlane_b32 s68, v12, 52
	v_readlane_b32 s69, v12, 54
	v_readlane_b32 s70, v12, 53
	v_readlane_b32 s71, v12, 55
	v_readlane_b32 s72, v12, 56
	v_readlane_b32 s73, v12, 58
	v_readlane_b32 s80, v12, 57
	v_readlane_b32 s81, v12, 59
	v_readlane_b32 s82, v12, 60
	v_readlane_b32 s83, v12, 62
	v_readlane_b32 s84, v12, 61
	v_readlane_b32 s85, v12, 63
	v_mul_f32_e32 v244, v71, v80
	v_mul_f32_e32 v245, v75, v81
	v_sub_f32_e32 v86, v244, v245
	v_mul_f32_e32 v244, v75, v80
	v_mul_f32_e32 v245, v71, v81
	v_add_f32_e32 v88, v244, v245
	v_pk_mul_f32 v[90:91], v[88:89], s[44:45] op_sel_hi:[0,1]
	v_pk_fma_f32 v[90:91], v[86:87], s[16:17], v[90:91] op_sel_hi:[0,1,1] neg_lo:[0,0,1] neg_hi:[0,0,1]
	v_pk_add_f32 v[56:57], v[56:57], v[90:91]
	v_pk_mul_f32 v[90:91], v[88:89], s[48:49] op_sel_hi:[0,1]
	v_pk_fma_f32 v[90:91], v[86:87], s[46:47], v[90:91] op_sel_hi:[0,1,1] neg_lo:[0,0,1] neg_hi:[0,0,1]
; __device__ __forceinline__ void ph1_small(const Args& a, int tid, int wave, int lane, int G, int bid) {
;     ...
; #pragma unroll 8
;             for (int n = 0; n < 64; ++n) { const float cr = cre[((size_t)g * 16 + p) * 64 + n], ci = cim[((size_t)g * 16 + p) * 64 + n];
;                 const float pr = POW[(((size_t)g * 65 + tau) * 64 + n) * 2], pi = POW[(((size_t)g * 65 + tau) * 64 + n) * 2 + 1];
;                 const float er = cr * pr - ci * pi, ei = cr * pi + ci * pr;
;                 const f32x4* bp = (const f32x4*)(BBAR + ((size_t)g * 64 + n) * 32);
; #pragma unroll
;                 for (int q = 0; q < 8; ++q) { const f32x4 bb = bp[q]; s[2 * q] += er * bb[0] - ei * bb[1]; s[2 * q + 1] += er * bb[2] - ei * bb[3]; } }
	v_pk_add_f32 v[54:55], v[54:55], v[90:91]
	v_pk_mul_f32 v[90:91], v[88:89], s[54:55] op_sel_hi:[0,1]
	v_pk_fma_f32 v[90:91], v[86:87], s[52:53], v[90:91] op_sel_hi:[0,1,1] neg_lo:[0,0,1] neg_hi:[0,0,1]
	v_pk_add_f32 v[52:53], v[52:53], v[90:91]
	v_pk_mul_f32 v[90:91], v[88:89], s[58:59] op_sel_hi:[0,1]
	v_pk_fma_f32 v[90:91], v[86:87], s[56:57], v[90:91] op_sel_hi:[0,1,1] neg_lo:[0,0,1] neg_hi:[0,0,1]
	v_pk_add_f32 v[50:51], v[50:51], v[90:91]
	v_pk_mul_f32 v[90:91], v[88:89], s[64:65] op_sel_hi:[0,1]
	v_pk_fma_f32 v[90:91], v[86:87], s[62:63], v[90:91] op_sel_hi:[0,1,1] neg_lo:[0,0,1] neg_hi:[0,0,1]
	v_pk_add_f32 v[58:59], v[58:59], v[90:91]
	v_pk_mul_f32 v[90:91], v[88:89], s[70:71] op_sel_hi:[0,1]
	v_pk_fma_f32 v[90:91], v[86:87], s[68:69], v[90:91] op_sel_hi:[0,1,1] neg_lo:[0,0,1] neg_hi:[0,0,1]
	v_pk_add_f32 v[60:61], v[60:61], v[90:91]
	v_pk_mul_f32 v[90:91], v[88:89], s[80:81] op_sel_hi:[0,1]
	v_pk_fma_f32 v[90:91], v[86:87], s[72:73], v[90:91] op_sel_hi:[0,1,1] neg_lo:[0,0,1] neg_hi:[0,0,1]
	v_pk_add_f32 v[64:65], v[64:65], v[90:91]
	v_pk_mul_f32 v[90:91], v[88:89], s[84:85] op_sel_hi:[0,1]
	v_pk_fma_f32 v[90:91], v[86:87], s[82:83], v[90:91] op_sel_hi:[0,1,1] neg_lo:[0,0,1] neg_hi:[0,0,1]
	v_pk_add_f32 v[62:63], v[62:63], v[90:91]
	v_readlane_b32 s16, v13, 0
	v_readlane_b32 s17, v13, 2
	v_readlane_b32 s44, v13, 1
	v_readlane_b32 s45, v13, 3
	v_readlane_b32 s46, v13, 4
	v_readlane_b32 s47, v13, 6
	v_readlane_b32 s48, v13, 5
	v_readlane_b32 s49, v13, 7
	v_readlane_b32 s52, v13, 8
	v_readlane_b32 s53, v13, 10
	v_readlane_b32 s54, v13, 9
	v_readlane_b32 s55, v13, 11
	v_readlane_b32 s56, v13, 12
	v_readlane_b32 s57, v13, 14
	v_readlane_b32 s58, v13, 13
	v_readlane_b32 s59, v13, 15
	v_readlane_b32 s62, v13, 16
	v_readlane_b32 s63, v13, 18
	v_readlane_b32 s64, v13, 17
	v_readlane_b32 s65, v13, 19
	v_readlane_b32 s68, v13, 20
	v_readlane_b32 s69, v13, 22
	v_readlane_b32 s70, v13, 21
	v_readlane_b32 s71, v13, 23
	v_readlane_b32 s72, v13, 24
	v_readlane_b32 s73, v13, 26
	v_readlane_b32 s80, v13, 25
	v_readlane_b32 s81, v13, 27
	v_readlane_b32 s82, v13, 28
	v_readlane_b32 s83, v13, 30
	v_readlane_b32 s84, v13, 29
	v_readlane_b32 s85, v13, 31
	v_mul_f32_e32 v244, v72, v82
	v_mul_f32_e32 v245, v76, v83
	v_sub_f32_e32 v86, v244, v245
	v_mul_f32_e32 v244, v76, v82
	v_mul_f32_e32 v245, v72, v83
	v_add_f32_e32 v88, v244, v245
	v_pk_mul_f32 v[90:91], v[88:89], s[44:45] op_sel_hi:[0,1]
	v_pk_fma_f32 v[90:91], v[86:87], s[16:17], v[90:91] op_sel_hi:[0,1,1] neg_lo:[0,0,1] neg_hi:[0,0,1]
	v_pk_add_f32 v[56:57], v[56:57], v[90:91]
	v_pk_mul_f32 v[90:91], v[88:89], s[48:49] op_sel_hi:[0,1]
	v_pk_fma_f32 v[90:91], v[86:87], s[46:47], v[90:91] op_sel_hi:[0,1,1] neg_lo:[0,0,1] neg_hi:[0,0,1]
	v_pk_add_f32 v[54:55], v[54:55], v[90:91]
	v_pk_mul_f32 v[90:91], v[88:89], s[54:55] op_sel_hi:[0,1]
	v_pk_fma_f32 v[90:91], v[86:87], s[52:53], v[90:91] op_sel_hi:[0,1,1] neg_lo:[0,0,1] neg_hi:[0,0,1]
	v_pk_add_f32 v[52:53], v[52:53], v[90:91]
	v_pk_mul_f32 v[90:91], v[88:89], s[58:59] op_sel_hi:[0,1]
	v_pk_fma_f32 v[90:91], v[86:87], s[56:57], v[90:91] op_sel_hi:[0,1,1] neg_lo:[0,0,1] neg_hi:[0,0,1]
	v_pk_add_f32 v[50:51], v[50:51], v[90:91]
	v_pk_mul_f32 v[90:91], v[88:89], s[64:65] op_sel_hi:[0,1]
	v_pk_fma_f32 v[90:91], v[86:87], s[62:63], v[90:91] op_sel_hi:[0,1,1] neg_lo:[0,0,1] neg_hi:[0,0,1]
	v_pk_add_f32 v[58:59], v[58:59], v[90:91]
	v_pk_mul_f32 v[90:91], v[88:89], s[70:71] op_sel_hi:[0,1]
	v_pk_fma_f32 v[90:91], v[86:87], s[68:69], v[90:91] op_sel_hi:[0,1,1] neg_lo:[0,0,1] neg_hi:[0,0,1]
	v_pk_add_f32 v[60:61], v[60:61], v[90:91]
	v_pk_mul_f32 v[90:91], v[88:89], s[80:81] op_sel_hi:[0,1]
	v_pk_fma_f32 v[90:91], v[86:87], s[72:73], v[90:91] op_sel_hi:[0,1,1] neg_lo:[0,0,1] neg_hi:[0,0,1]
	v_pk_add_f32 v[64:65], v[64:65], v[90:91]
	v_pk_mul_f32 v[90:91], v[88:89], s[84:85] op_sel_hi:[0,1]
	v_pk_fma_f32 v[90:91], v[86:87], s[82:83], v[90:91] op_sel_hi:[0,1,1] neg_lo:[0,0,1] neg_hi:[0,0,1]
	v_pk_add_f32 v[62:63], v[62:63], v[90:91]
	v_readlane_b32 s16, v13, 32
	v_readlane_b32 s17, v13, 34
	v_readlane_b32 s44, v13, 33
	v_readlane_b32 s45, v13, 35
	v_readlane_b32 s46, v13, 36
	v_readlane_b32 s47, v13, 38
	v_readlane_b32 s48, v13, 37
	v_readlane_b32 s49, v13, 39
	v_readlane_b32 s52, v13, 40
	v_readlane_b32 s53, v13, 42
	v_readlane_b32 s54, v13, 41
	v_readlane_b32 s55, v13, 43
	v_readlane_b32 s56, v13, 44
	v_readlane_b32 s57, v13, 46
	v_readlane_b32 s58, v13, 45
	v_readlane_b32 s59, v13, 47
	v_readlane_b32 s62, v13, 48
	v_readlane_b32 s63, v13, 50
	v_readlane_b32 s64, v13, 49
	v_readlane_b32 s65, v13, 51
	v_readlane_b32 s68, v13, 52
	v_readlane_b32 s69, v13, 54
	v_readlane_b32 s70, v13, 53
	v_readlane_b32 s71, v13, 55
	v_readlane_b32 s72, v13, 56
	v_readlane_b32 s73, v13, 58
	v_readlane_b32 s80, v13, 57
	v_readlane_b32 s81, v13, 59
	v_readlane_b32 s82, v13, 60
	v_readlane_b32 s83, v13, 62
	v_readlane_b32 s84, v13, 61
	v_readlane_b32 s85, v13, 63
	v_mul_f32_e32 v244, v73, v84
	v_mul_f32_e32 v245, v77, v85
	v_sub_f32_e32 v86, v244, v245
	v_mul_f32_e32 v244, v77, v84
	v_mul_f32_e32 v245, v73, v85
	v_add_f32_e32 v88, v244, v245
	v_pk_mul_f32 v[90:91], v[88:89], s[44:45] op_sel_hi:[0,1]
	v_pk_fma_f32 v[90:91], v[86:87], s[16:17], v[90:91] op_sel_hi:[0,1,1] neg_lo:[0,0,1] neg_hi:[0,0,1]
	v_pk_add_f32 v[56:57], v[56:57], v[90:91]
	v_pk_mul_f32 v[90:91], v[88:89], s[48:49] op_sel_hi:[0,1]
	v_pk_fma_f32 v[90:91], v[86:87], s[46:47], v[90:91] op_sel_hi:[0,1,1] neg_lo:[0,0,1] neg_hi:[0,0,1]
	v_pk_add_f32 v[54:55], v[54:55], v[90:91]
	v_pk_mul_f32 v[90:91], v[88:89], s[54:55] op_sel_hi:[0,1]
	v_pk_fma_f32 v[90:91], v[86:87], s[52:53], v[90:91] op_sel_hi:[0,1,1] neg_lo:[0,0,1] neg_hi:[0,0,1]
	v_pk_add_f32 v[52:53], v[52:53], v[90:91]
	v_pk_mul_f32 v[90:91], v[88:89], s[58:59] op_sel_hi:[0,1]
	v_pk_fma_f32 v[90:91], v[86:87], s[56:57], v[90:91] op_sel_hi:[0,1,1] neg_lo:[0,0,1] neg_hi:[0,0,1]
	v_pk_add_f32 v[50:51], v[50:51], v[90:91]
	v_pk_mul_f32 v[90:91], v[88:89], s[64:65] op_sel_hi:[0,1]
	v_pk_fma_f32 v[90:91], v[86:87], s[62:63], v[90:91] op_sel_hi:[0,1,1] neg_lo:[0,0,1] neg_hi:[0,0,1]
	v_pk_add_f32 v[58:59], v[58:59], v[90:91]
	v_pk_mul_f32 v[90:91], v[88:89], s[70:71] op_sel_hi:[0,1]
	v_pk_fma_f32 v[90:91], v[86:87], s[68:69], v[90:91] op_sel_hi:[0,1,1] neg_lo:[0,0,1] neg_hi:[0,0,1]
	v_pk_add_f32 v[60:61], v[60:61], v[90:91]
	v_pk_mul_f32 v[90:91], v[88:89], s[80:81] op_sel_hi:[0,1]
	v_pk_fma_f32 v[90:91], v[86:87], s[72:73], v[90:91] op_sel_hi:[0,1,1] neg_lo:[0,0,1] neg_hi:[0,0,1]
	v_pk_add_f32 v[64:65], v[64:65], v[90:91]
	v_pk_mul_f32 v[90:91], v[88:89], s[84:85] op_sel_hi:[0,1]
	v_pk_fma_f32 v[90:91], v[86:87], s[82:83], v[90:91] op_sel_hi:[0,1,1] neg_lo:[0,0,1] neg_hi:[0,0,1]
	v_pk_add_f32 v[62:63], v[62:63], v[90:91]
	global_load_dwordx4 v[70:73], v[44:45], off offset:112
	global_load_dwordx4 v[74:77], v[42:43], off offset:112
	global_load_dwordx4 v[78:81], v40, s[100:101] offset:224
	global_load_dwordx4 v[82:85], v40, s[100:101] offset:240
	s_waitcnt vmcnt(4)
; __device__ __forceinline__ void ph1_small(const Args& a, int tid, int wave, int lane, int G, int bid) {
;     ...
; #pragma unroll 8
;             for (int n = 0; n < 64; ++n) { const float cr = cre[((size_t)g * 16 + p) * 64 + n], ci = cim[((size_t)g * 16 + p) * 64 + n];
;                 const float pr = POW[(((size_t)g * 65 + tau) * 64 + n) * 2], pi = POW[(((size_t)g * 65 + tau) * 64 + n) * 2 + 1];
;                 const float er = cr * pr - ci * pi, ei = cr * pi + ci * pr;
;                 const f32x4* bp = (const f32x4*)(BBAR + ((size_t)g * 64 + n) * 32);
; #pragma unroll
;                 for (int q = 0; q < 8; ++q) { const f32x4 bb = bp[q]; s[2 * q] += er * bb[0] - ei * bb[1]; s[2 * q + 1] += er * bb[2] - ei * bb[3]; } }
	v_readlane_b32 s16, v14, 0
	v_readlane_b32 s17, v14, 2
	v_readlane_b32 s44, v14, 1
	v_readlane_b32 s45, v14, 3
	v_readlane_b32 s46, v14, 4
	v_readlane_b32 s47, v14, 6
	v_readlane_b32 s48, v14, 5
	v_readlane_b32 s49, v14, 7
	v_readlane_b32 s52, v14, 8
	v_readlane_b32 s53, v14, 10
	v_readlane_b32 s54, v14, 9
	v_readlane_b32 s55, v14, 11
	v_readlane_b32 s56, v14, 12
	v_readlane_b32 s57, v14, 14
	v_readlane_b32 s58, v14, 13
	v_readlane_b32 s59, v14, 15
	v_readlane_b32 s62, v14, 16
	v_readlane_b32 s63, v14, 18
	v_readlane_b32 s64, v14, 17
	v_readlane_b32 s65, v14, 19
	v_readlane_b32 s68, v14, 20
	v_readlane_b32 s69, v14, 22
	v_readlane_b32 s70, v14, 21
	v_readlane_b32 s71, v14, 23
	v_readlane_b32 s72, v14, 24
	v_readlane_b32 s73, v14, 26
	v_readlane_b32 s80, v14, 25
	v_readlane_b32 s81, v14, 27
	v_readlane_b32 s82, v14, 28
	v_readlane_b32 s83, v14, 30
	v_readlane_b32 s84, v14, 29
	v_readlane_b32 s85, v14, 31
	v_mul_f32_e32 v244, v18, v26
	v_mul_f32_e32 v245, v22, v27
	v_sub_f32_e32 v86, v244, v245
	v_mul_f32_e32 v244, v22, v26
	v_mul_f32_e32 v245, v18, v27
	v_add_f32_e32 v88, v244, v245
	v_pk_mul_f32 v[90:91], v[88:89], s[44:45] op_sel_hi:[0,1]
	v_pk_fma_f32 v[90:91], v[86:87], s[16:17], v[90:91] op_sel_hi:[0,1,1] neg_lo:[0,0,1] neg_hi:[0,0,1]
	v_pk_add_f32 v[56:57], v[56:57], v[90:91]
	v_pk_mul_f32 v[90:91], v[88:89], s[48:49] op_sel_hi:[0,1]
	v_pk_fma_f32 v[90:91], v[86:87], s[46:47], v[90:91] op_sel_hi:[0,1,1] neg_lo:[0,0,1] neg_hi:[0,0,1]
	v_pk_add_f32 v[54:55], v[54:55], v[90:91]
	v_pk_mul_f32 v[90:91], v[88:89], s[54:55] op_sel_hi:[0,1]
	v_pk_fma_f32 v[90:91], v[86:87], s[52:53], v[90:91] op_sel_hi:[0,1,1] neg_lo:[0,0,1] neg_hi:[0,0,1]
	v_pk_add_f32 v[52:53], v[52:53], v[90:91]
	v_pk_mul_f32 v[90:91], v[88:89], s[58:59] op_sel_hi:[0,1]
	v_pk_fma_f32 v[90:91], v[86:87], s[56:57], v[90:91] op_sel_hi:[0,1,1] neg_lo:[0,0,1] neg_hi:[0,0,1]
	v_pk_add_f32 v[50:51], v[50:51], v[90:91]
	v_pk_mul_f32 v[90:91], v[88:89], s[64:65] op_sel_hi:[0,1]
	v_pk_fma_f32 v[90:91], v[86:87], s[62:63], v[90:91] op_sel_hi:[0,1,1] neg_lo:[0,0,1] neg_hi:[0,0,1]
	v_pk_add_f32 v[58:59], v[58:59], v[90:91]
	v_pk_mul_f32 v[90:91], v[88:89], s[70:71] op_sel_hi:[0,1]
	v_pk_fma_f32 v[90:91], v[86:87], s[68:69], v[90:91] op_sel_hi:[0,1,1] neg_lo:[0,0,1] neg_hi:[0,0,1]
	v_pk_add_f32 v[60:61], v[60:61], v[90:91]
	v_pk_mul_f32 v[90:91], v[88:89], s[80:81] op_sel_hi:[0,1]
	v_pk_fma_f32 v[90:91], v[86:87], s[72:73], v[90:91] op_sel_hi:[0,1,1] neg_lo:[0,0,1] neg_hi:[0,0,1]
	v_pk_add_f32 v[64:65], v[64:65], v[90:91]
	v_pk_mul_f32 v[90:91], v[88:89], s[84:85] op_sel_hi:[0,1]
	v_pk_fma_f32 v[90:91], v[86:87], s[82:83], v[90:91] op_sel_hi:[0,1,1] neg_lo:[0,0,1] neg_hi:[0,0,1]
	v_pk_add_f32 v[62:63], v[62:63], v[90:91]
	v_readlane_b32 s16, v14, 32
	v_readlane_b32 s17, v14, 34
	v_readlane_b32 s44, v14, 33
	v_readlane_b32 s45, v14, 35
	v_readlane_b32 s46, v14, 36
	v_readlane_b32 s47, v14, 38
	v_readlane_b32 s48, v14, 37
	v_readlane_b32 s49, v14, 39
	v_readlane_b32 s52, v14, 40
	v_readlane_b32 s53, v14, 42
	v_readlane_b32 s54, v14, 41
	v_readlane_b32 s55, v14, 43
	v_readlane_b32 s56, v14, 44
	v_readlane_b32 s57, v14, 46
	v_readlane_b32 s58, v14, 45
	v_readlane_b32 s59, v14, 47
	v_readlane_b32 s62, v14, 48
	v_readlane_b32 s63, v14, 50
	v_readlane_b32 s64, v14, 49
	v_readlane_b32 s65, v14, 51
	v_readlane_b32 s68, v14, 52
	v_readlane_b32 s69, v14, 54
	v_readlane_b32 s70, v14, 53
	v_readlane_b32 s71, v14, 55
	v_readlane_b32 s72, v14, 56
	v_readlane_b32 s73, v14, 58
	v_readlane_b32 s80, v14, 57
	v_readlane_b32 s81, v14, 59
	v_readlane_b32 s82, v14, 60
	v_readlane_b32 s83, v14, 62
	v_readlane_b32 s84, v14, 61
	v_readlane_b32 s85, v14, 63
	v_mul_f32_e32 v244, v19, v28
	v_mul_f32_e32 v245, v23, v29
	v_sub_f32_e32 v86, v244, v245
	v_mul_f32_e32 v244, v23, v28
	v_mul_f32_e32 v245, v19, v29
	v_add_f32_e32 v88, v244, v245
	v_pk_mul_f32 v[90:91], v[88:89], s[44:45] op_sel_hi:[0,1]
	v_pk_fma_f32 v[90:91], v[86:87], s[16:17], v[90:91] op_sel_hi:[0,1,1] neg_lo:[0,0,1] neg_hi:[0,0,1]
	v_pk_add_f32 v[56:57], v[56:57], v[90:91]
	v_pk_mul_f32 v[90:91], v[88:89], s[48:49] op_sel_hi:[0,1]
	v_pk_fma_f32 v[90:91], v[86:87], s[46:47], v[90:91] op_sel_hi:[0,1,1] neg_lo:[0,0,1] neg_hi:[0,0,1]
	v_pk_add_f32 v[54:55], v[54:55], v[90:91]
	v_pk_mul_f32 v[90:91], v[88:89], s[54:55] op_sel_hi:[0,1]
	v_pk_fma_f32 v[90:91], v[86:87], s[52:53], v[90:91] op_sel_hi:[0,1,1] neg_lo:[0,0,1] neg_hi:[0,0,1]
	v_pk_add_f32 v[52:53], v[52:53], v[90:91]
	v_pk_mul_f32 v[90:91], v[88:89], s[58:59] op_sel_hi:[0,1]
	v_pk_fma_f32 v[90:91], v[86:87], s[56:57], v[90:91] op_sel_hi:[0,1,1] neg_lo:[0,0,1] neg_hi:[0,0,1]
	v_pk_add_f32 v[50:51], v[50:51], v[90:91]
	v_pk_mul_f32 v[90:91], v[88:89], s[64:65] op_sel_hi:[0,1]
	v_pk_fma_f32 v[90:91], v[86:87], s[62:63], v[90:91] op_sel_hi:[0,1,1] neg_lo:[0,0,1] neg_hi:[0,0,1]
	v_pk_add_f32 v[58:59], v[58:59], v[90:91]
	v_pk_mul_f32 v[90:91], v[88:89], s[70:71] op_sel_hi:[0,1]
	v_pk_fma_f32 v[90:91], v[86:87], s[68:69], v[90:91] op_sel_hi:[0,1,1] neg_lo:[0,0,1] neg_hi:[0,0,1]
	v_pk_add_f32 v[60:61], v[60:61], v[90:91]
	v_pk_mul_f32 v[90:91], v[88:89], s[80:81] op_sel_hi:[0,1]
	v_pk_fma_f32 v[90:91], v[86:87], s[72:73], v[90:91] op_sel_hi:[0,1,1] neg_lo:[0,0,1] neg_hi:[0,0,1]
	v_pk_add_f32 v[64:65], v[64:65], v[90:91]
	v_pk_mul_f32 v[90:91], v[88:89], s[84:85] op_sel_hi:[0,1]
	v_pk_fma_f32 v[90:91], v[86:87], s[82:83], v[90:91] op_sel_hi:[0,1,1] neg_lo:[0,0,1] neg_hi:[0,0,1]
	v_pk_add_f32 v[62:63], v[62:63], v[90:91]
	v_readlane_b32 s16, v15, 0
	v_readlane_b32 s17, v15, 2
	v_readlane_b32 s44, v15, 1
	v_readlane_b32 s45, v15, 3
	v_readlane_b32 s46, v15, 4
	v_readlane_b32 s47, v15, 6
; __device__ __forceinline__ void ph1_small(const Args& a, int tid, int wave, int lane, int G, int bid) {
;     ...
; #pragma unroll 8
;             for (int n = 0; n < 64; ++n) { const float cr = cre[((size_t)g * 16 + p) * 64 + n], ci = cim[((size_t)g * 16 + p) * 64 + n];
;                 const float pr = POW[(((size_t)g * 65 + tau) * 64 + n) * 2], pi = POW[(((size_t)g * 65 + tau) * 64 + n) * 2 + 1];
;                 const float er = cr * pr - ci * pi, ei = cr * pi + ci * pr;
;                 const f32x4* bp = (const f32x4*)(BBAR + ((size_t)g * 64 + n) * 32);
; #pragma unroll
;                 for (int q = 0; q < 8; ++q) { const f32x4 bb = bp[q]; s[2 * q] += er * bb[0] - ei * bb[1]; s[2 * q + 1] += er * bb[2] - ei * bb[3]; } }
	v_readlane_b32 s48, v15, 5
	v_readlane_b32 s49, v15, 7
	v_readlane_b32 s52, v15, 8
	v_readlane_b32 s53, v15, 10
	v_readlane_b32 s54, v15, 9
	v_readlane_b32 s55, v15, 11
	v_readlane_b32 s56, v15, 12
	v_readlane_b32 s57, v15, 14
	v_readlane_b32 s58, v15, 13
	v_readlane_b32 s59, v15, 15
	v_readlane_b32 s62, v15, 16
	v_readlane_b32 s63, v15, 18
	v_readlane_b32 s64, v15, 17
	v_readlane_b32 s65, v15, 19
	v_readlane_b32 s68, v15, 20
	v_readlane_b32 s69, v15, 22
	v_readlane_b32 s70, v15, 21
	v_readlane_b32 s71, v15, 23
	v_readlane_b32 s72, v15, 24
	v_readlane_b32 s73, v15, 26
	v_readlane_b32 s80, v15, 25
	v_readlane_b32 s81, v15, 27
	v_readlane_b32 s82, v15, 28
	v_readlane_b32 s83, v15, 30
	v_readlane_b32 s84, v15, 29
	v_readlane_b32 s85, v15, 31
	v_mul_f32_e32 v244, v20, v46
	v_mul_f32_e32 v245, v24, v47
	v_sub_f32_e32 v86, v244, v245
	v_mul_f32_e32 v244, v24, v46
	v_mul_f32_e32 v245, v20, v47
	v_add_f32_e32 v88, v244, v245
	v_pk_mul_f32 v[90:91], v[88:89], s[44:45] op_sel_hi:[0,1]
	v_pk_fma_f32 v[90:91], v[86:87], s[16:17], v[90:91] op_sel_hi:[0,1,1] neg_lo:[0,0,1] neg_hi:[0,0,1]
	v_pk_add_f32 v[56:57], v[56:57], v[90:91]
	v_pk_mul_f32 v[90:91], v[88:89], s[48:49] op_sel_hi:[0,1]
	v_pk_fma_f32 v[90:91], v[86:87], s[46:47], v[90:91] op_sel_hi:[0,1,1] neg_lo:[0,0,1] neg_hi:[0,0,1]
	v_pk_add_f32 v[54:55], v[54:55], v[90:91]
	v_pk_mul_f32 v[90:91], v[88:89], s[54:55] op_sel_hi:[0,1]
	v_pk_fma_f32 v[90:91], v[86:87], s[52:53], v[90:91] op_sel_hi:[0,1,1] neg_lo:[0,0,1] neg_hi:[0,0,1]
	v_pk_add_f32 v[52:53], v[52:53], v[90:91]
	v_pk_mul_f32 v[90:91], v[88:89], s[58:59] op_sel_hi:[0,1]
	v_pk_fma_f32 v[90:91], v[86:87], s[56:57], v[90:91] op_sel_hi:[0,1,1] neg_lo:[0,0,1] neg_hi:[0,0,1]
	v_pk_add_f32 v[50:51], v[50:51], v[90:91]
	v_pk_mul_f32 v[90:91], v[88:89], s[64:65] op_sel_hi:[0,1]
	v_pk_fma_f32 v[90:91], v[86:87], s[62:63], v[90:91] op_sel_hi:[0,1,1] neg_lo:[0,0,1] neg_hi:[0,0,1]
	v_pk_add_f32 v[58:59], v[58:59], v[90:91]
	v_pk_mul_f32 v[90:91], v[88:89], s[70:71] op_sel_hi:[0,1]
	v_pk_fma_f32 v[90:91], v[86:87], s[68:69], v[90:91] op_sel_hi:[0,1,1] neg_lo:[0,0,1] neg_hi:[0,0,1]
	v_pk_add_f32 v[60:61], v[60:61], v[90:91]
	v_pk_mul_f32 v[90:91], v[88:89], s[80:81] op_sel_hi:[0,1]
	v_pk_fma_f32 v[90:91], v[86:87], s[72:73], v[90:91] op_sel_hi:[0,1,1] neg_lo:[0,0,1] neg_hi:[0,0,1]
	v_pk_add_f32 v[64:65], v[64:65], v[90:91]
	v_pk_mul_f32 v[90:91], v[88:89], s[84:85] op_sel_hi:[0,1]
	v_pk_fma_f32 v[90:91], v[86:87], s[82:83], v[90:91] op_sel_hi:[0,1,1] neg_lo:[0,0,1] neg_hi:[0,0,1]
	v_pk_add_f32 v[62:63], v[62:63], v[90:91]
	v_readlane_b32 s16, v15, 32
	v_readlane_b32 s17, v15, 34
	v_readlane_b32 s44, v15, 33
	v_readlane_b32 s45, v15, 35
	v_readlane_b32 s46, v15, 36
	v_readlane_b32 s47, v15, 38
	v_readlane_b32 s48, v15, 37
	v_readlane_b32 s49, v15, 39
	v_readlane_b32 s52, v15, 40
	v_readlane_b32 s53, v15, 42
	v_readlane_b32 s54, v15, 41
	v_readlane_b32 s55, v15, 43
	v_readlane_b32 s56, v15, 44
	v_readlane_b32 s57, v15, 46
	v_readlane_b32 s58, v15, 45
	v_readlane_b32 s59, v15, 47
	v_readlane_b32 s62, v15, 48
	v_readlane_b32 s63, v15, 50
	v_readlane_b32 s64, v15, 49
	v_readlane_b32 s65, v15, 51
	v_readlane_b32 s68, v15, 52
	v_readlane_b32 s69, v15, 54
	v_readlane_b32 s70, v15, 53
	v_readlane_b32 s71, v15, 55
	v_readlane_b32 s72, v15, 56
	v_readlane_b32 s73, v15, 58
	v_readlane_b32 s80, v15, 57
	v_readlane_b32 s81, v15, 59
	v_readlane_b32 s82, v15, 60
	v_readlane_b32 s83, v15, 62
	v_readlane_b32 s84, v15, 61
	v_readlane_b32 s85, v15, 63
	v_mul_f32_e32 v244, v21, v48
	v_mul_f32_e32 v245, v25, v49
	v_sub_f32_e32 v86, v244, v245
	v_mul_f32_e32 v244, v25, v48
	v_mul_f32_e32 v245, v21, v49
	v_add_f32_e32 v88, v244, v245
	v_pk_mul_f32 v[90:91], v[88:89], s[44:45] op_sel_hi:[0,1]
	v_pk_fma_f32 v[90:91], v[86:87], s[16:17], v[90:91] op_sel_hi:[0,1,1] neg_lo:[0,0,1] neg_hi:[0,0,1]
	v_pk_add_f32 v[56:57], v[56:57], v[90:91]
	v_pk_mul_f32 v[90:91], v[88:89], s[48:49] op_sel_hi:[0,1]
	v_pk_fma_f32 v[90:91], v[86:87], s[46:47], v[90:91] op_sel_hi:[0,1,1] neg_lo:[0,0,1] neg_hi:[0,0,1]
	v_pk_add_f32 v[54:55], v[54:55], v[90:91]
	v_pk_mul_f32 v[90:91], v[88:89], s[54:55] op_sel_hi:[0,1]
	v_pk_fma_f32 v[90:91], v[86:87], s[52:53], v[90:91] op_sel_hi:[0,1,1] neg_lo:[0,0,1] neg_hi:[0,0,1]
	v_pk_add_f32 v[52:53], v[52:53], v[90:91]
	v_pk_mul_f32 v[90:91], v[88:89], s[58:59] op_sel_hi:[0,1]
	v_pk_fma_f32 v[90:91], v[86:87], s[56:57], v[90:91] op_sel_hi:[0,1,1] neg_lo:[0,0,1] neg_hi:[0,0,1]
	v_pk_add_f32 v[50:51], v[50:51], v[90:91]
	v_pk_mul_f32 v[90:91], v[88:89], s[64:65] op_sel_hi:[0,1]
	v_pk_fma_f32 v[90:91], v[86:87], s[62:63], v[90:91] op_sel_hi:[0,1,1] neg_lo:[0,0,1] neg_hi:[0,0,1]
	v_pk_add_f32 v[58:59], v[58:59], v[90:91]
	v_pk_mul_f32 v[90:91], v[88:89], s[70:71] op_sel_hi:[0,1]
	v_pk_fma_f32 v[90:91], v[86:87], s[68:69], v[90:91] op_sel_hi:[0,1,1] neg_lo:[0,0,1] neg_hi:[0,0,1]
	v_pk_add_f32 v[60:61], v[60:61], v[90:91]
	v_pk_mul_f32 v[90:91], v[88:89], s[80:81] op_sel_hi:[0,1]
	v_pk_fma_f32 v[90:91], v[86:87], s[72:73], v[90:91] op_sel_hi:[0,1,1] neg_lo:[0,0,1] neg_hi:[0,0,1]
	v_pk_add_f32 v[64:65], v[64:65], v[90:91]
	v_pk_mul_f32 v[90:91], v[88:89], s[84:85] op_sel_hi:[0,1]
	v_pk_fma_f32 v[90:91], v[86:87], s[82:83], v[90:91] op_sel_hi:[0,1,1] neg_lo:[0,0,1] neg_hi:[0,0,1]
	v_pk_add_f32 v[62:63], v[62:63], v[90:91]
	s_waitcnt vmcnt(0)
; __device__ __forceinline__ void ph1_small(const Args& a, int tid, int wave, int lane, int G, int bid) {
;     ...
; #pragma unroll 8
;             for (int n = 0; n < 64; ++n) { const float cr = cre[((size_t)g * 16 + p) * 64 + n], ci = cim[((size_t)g * 16 + p) * 64 + n];
;                 const float pr = POW[(((size_t)g * 65 + tau) * 64 + n) * 2], pi = POW[(((size_t)g * 65 + tau) * 64 + n) * 2 + 1];
;                 const float er = cr * pr - ci * pi, ei = cr * pi + ci * pr;
;                 const f32x4* bp = (const f32x4*)(BBAR + ((size_t)g * 64 + n) * 32);
; #pragma unroll
;                 for (int q = 0; q < 8; ++q) { const f32x4 bb = bp[q]; s[2 * q] += er * bb[0] - ei * bb[1]; s[2 * q + 1] += er * bb[2] - ei * bb[3]; } }
	v_readlane_b32 s16, v16, 0
	v_readlane_b32 s17, v16, 2
	v_readlane_b32 s44, v16, 1
	v_readlane_b32 s45, v16, 3
	v_readlane_b32 s46, v16, 4
	v_readlane_b32 s47, v16, 6
	v_readlane_b32 s48, v16, 5
	v_readlane_b32 s49, v16, 7
	v_readlane_b32 s52, v16, 8
	v_readlane_b32 s53, v16, 10
	v_readlane_b32 s54, v16, 9
	v_readlane_b32 s55, v16, 11
	v_readlane_b32 s56, v16, 12
	v_readlane_b32 s57, v16, 14
	v_readlane_b32 s58, v16, 13
	v_readlane_b32 s59, v16, 15
	v_readlane_b32 s62, v16, 16
	v_readlane_b32 s63, v16, 18
	v_readlane_b32 s64, v16, 17
	v_readlane_b32 s65, v16, 19
	v_readlane_b32 s68, v16, 20
	v_readlane_b32 s69, v16, 22
	v_readlane_b32 s70, v16, 21
	v_readlane_b32 s71, v16, 23
	v_readlane_b32 s72, v16, 24
	v_readlane_b32 s73, v16, 26
	v_readlane_b32 s80, v16, 25
	v_readlane_b32 s81, v16, 27
	v_readlane_b32 s82, v16, 28
	v_readlane_b32 s83, v16, 30
	v_readlane_b32 s84, v16, 29
	v_readlane_b32 s85, v16, 31
	v_mul_f32_e32 v244, v70, v78
	v_mul_f32_e32 v245, v74, v79
	v_sub_f32_e32 v86, v244, v245
	v_mul_f32_e32 v244, v74, v78
	v_mul_f32_e32 v245, v70, v79
	v_add_f32_e32 v88, v244, v245
	v_pk_mul_f32 v[90:91], v[88:89], s[44:45] op_sel_hi:[0,1]
	v_pk_fma_f32 v[90:91], v[86:87], s[16:17], v[90:91] op_sel_hi:[0,1,1] neg_lo:[0,0,1] neg_hi:[0,0,1]
	v_pk_add_f32 v[56:57], v[56:57], v[90:91]
	v_pk_mul_f32 v[90:91], v[88:89], s[48:49] op_sel_hi:[0,1]
	v_pk_fma_f32 v[90:91], v[86:87], s[46:47], v[90:91] op_sel_hi:[0,1,1] neg_lo:[0,0,1] neg_hi:[0,0,1]
	v_pk_add_f32 v[54:55], v[54:55], v[90:91]
	v_pk_mul_f32 v[90:91], v[88:89], s[54:55] op_sel_hi:[0,1]
	v_pk_fma_f32 v[90:91], v[86:87], s[52:53], v[90:91] op_sel_hi:[0,1,1] neg_lo:[0,0,1] neg_hi:[0,0,1]
	v_pk_add_f32 v[52:53], v[52:53], v[90:91]
	v_pk_mul_f32 v[90:91], v[88:89], s[58:59] op_sel_hi:[0,1]
	v_pk_fma_f32 v[90:91], v[86:87], s[56:57], v[90:91] op_sel_hi:[0,1,1] neg_lo:[0,0,1] neg_hi:[0,0,1]
	v_pk_add_f32 v[50:51], v[50:51], v[90:91]
	v_pk_mul_f32 v[90:91], v[88:89], s[64:65] op_sel_hi:[0,1]
	v_pk_fma_f32 v[90:91], v[86:87], s[62:63], v[90:91] op_sel_hi:[0,1,1] neg_lo:[0,0,1] neg_hi:[0,0,1]
	v_pk_add_f32 v[58:59], v[58:59], v[90:91]
	v_pk_mul_f32 v[90:91], v[88:89], s[70:71] op_sel_hi:[0,1]
	v_pk_fma_f32 v[90:91], v[86:87], s[68:69], v[90:91] op_sel_hi:[0,1,1] neg_lo:[0,0,1] neg_hi:[0,0,1]
	v_pk_add_f32 v[60:61], v[60:61], v[90:91]
	v_pk_mul_f32 v[90:91], v[88:89], s[80:81] op_sel_hi:[0,1]
	v_pk_fma_f32 v[90:91], v[86:87], s[72:73], v[90:91] op_sel_hi:[0,1,1] neg_lo:[0,0,1] neg_hi:[0,0,1]
	v_pk_add_f32 v[64:65], v[64:65], v[90:91]
	v_pk_mul_f32 v[90:91], v[88:89], s[84:85] op_sel_hi:[0,1]
	v_pk_fma_f32 v[90:91], v[86:87], s[82:83], v[90:91] op_sel_hi:[0,1,1] neg_lo:[0,0,1] neg_hi:[0,0,1]
	v_pk_add_f32 v[62:63], v[62:63], v[90:91]
	v_readlane_b32 s16, v16, 32
	v_readlane_b32 s17, v16, 34
	v_readlane_b32 s44, v16, 33
	v_readlane_b32 s45, v16, 35
	v_readlane_b32 s46, v16, 36
	v_readlane_b32 s47, v16, 38
	v_readlane_b32 s48, v16, 37
	v_readlane_b32 s49, v16, 39
	v_readlane_b32 s52, v16, 40
	v_readlane_b32 s53, v16, 42
	v_readlane_b32 s54, v16, 41
	v_readlane_b32 s55, v16, 43
	v_readlane_b32 s56, v16, 44
	v_readlane_b32 s57, v16, 46
	v_readlane_b32 s58, v16, 45
	v_readlane_b32 s59, v16, 47
	v_readlane_b32 s62, v16, 48
	v_readlane_b32 s63, v16, 50
	v_readlane_b32 s64, v16, 49
	v_readlane_b32 s65, v16, 51
	v_readlane_b32 s68, v16, 52
	v_readlane_b32 s69, v16, 54
	v_readlane_b32 s70, v16, 53
	v_readlane_b32 s71, v16, 55
	v_readlane_b32 s72, v16, 56
	v_readlane_b32 s73, v16, 58
	v_readlane_b32 s80, v16, 57
	v_readlane_b32 s81, v16, 59
	v_readlane_b32 s82, v16, 60
	v_readlane_b32 s83, v16, 62
	v_readlane_b32 s84, v16, 61
	v_readlane_b32 s85, v16, 63
	v_mul_f32_e32 v244, v71, v80
	v_mul_f32_e32 v245, v75, v81
	v_sub_f32_e32 v86, v244, v245
	v_mul_f32_e32 v244, v75, v80
	v_mul_f32_e32 v245, v71, v81
	v_add_f32_e32 v88, v244, v245
	v_pk_mul_f32 v[90:91], v[88:89], s[44:45] op_sel_hi:[0,1]
	v_pk_fma_f32 v[90:91], v[86:87], s[16:17], v[90:91] op_sel_hi:[0,1,1] neg_lo:[0,0,1] neg_hi:[0,0,1]
	v_pk_add_f32 v[56:57], v[56:57], v[90:91]
	v_pk_mul_f32 v[90:91], v[88:89], s[48:49] op_sel_hi:[0,1]
	v_pk_fma_f32 v[90:91], v[86:87], s[46:47], v[90:91] op_sel_hi:[0,1,1] neg_lo:[0,0,1] neg_hi:[0,0,1]
	v_pk_add_f32 v[54:55], v[54:55], v[90:91]
	v_pk_mul_f32 v[90:91], v[88:89], s[54:55] op_sel_hi:[0,1]
	v_pk_fma_f32 v[90:91], v[86:87], s[52:53], v[90:91] op_sel_hi:[0,1,1] neg_lo:[0,0,1] neg_hi:[0,0,1]
	v_pk_add_f32 v[52:53], v[52:53], v[90:91]
	v_pk_mul_f32 v[90:91], v[88:89], s[58:59] op_sel_hi:[0,1]
	v_pk_fma_f32 v[90:91], v[86:87], s[56:57], v[90:91] op_sel_hi:[0,1,1] neg_lo:[0,0,1] neg_hi:[0,0,1]
	v_pk_add_f32 v[50:51], v[50:51], v[90:91]
	v_pk_mul_f32 v[90:91], v[88:89], s[64:65] op_sel_hi:[0,1]
	v_pk_fma_f32 v[90:91], v[86:87], s[62:63], v[90:91] op_sel_hi:[0,1,1] neg_lo:[0,0,1] neg_hi:[0,0,1]
	v_pk_add_f32 v[58:59], v[58:59], v[90:91]
	v_pk_mul_f32 v[90:91], v[88:89], s[70:71] op_sel_hi:[0,1]
	v_pk_fma_f32 v[90:91], v[86:87], s[68:69], v[90:91] op_sel_hi:[0,1,1] neg_lo:[0,0,1] neg_hi:[0,0,1]
	v_pk_add_f32 v[60:61], v[60:61], v[90:91]
	v_pk_mul_f32 v[90:91], v[88:89], s[80:81] op_sel_hi:[0,1]
	v_pk_fma_f32 v[90:91], v[86:87], s[72:73], v[90:91] op_sel_hi:[0,1,1] neg_lo:[0,0,1] neg_hi:[0,0,1]
	v_pk_add_f32 v[64:65], v[64:65], v[90:91]
	v_pk_mul_f32 v[90:91], v[88:89], s[84:85] op_sel_hi:[0,1]
	v_pk_fma_f32 v[90:91], v[86:87], s[82:83], v[90:91] op_sel_hi:[0,1,1] neg_lo:[0,0,1] neg_hi:[0,0,1]
	v_pk_add_f32 v[62:63], v[62:63], v[90:91]
	v_readlane_b32 s16, v17, 0
	v_readlane_b32 s17, v17, 2
	v_readlane_b32 s44, v17, 1
	v_readlane_b32 s45, v17, 3
	v_readlane_b32 s46, v17, 4
	v_readlane_b32 s47, v17, 6
; __device__ __forceinline__ void ph1_small(const Args& a, int tid, int wave, int lane, int G, int bid) {
;     ...
; #pragma unroll 8
;             for (int n = 0; n < 64; ++n) { const float cr = cre[((size_t)g * 16 + p) * 64 + n], ci = cim[((size_t)g * 16 + p) * 64 + n];
;                 const float pr = POW[(((size_t)g * 65 + tau) * 64 + n) * 2], pi = POW[(((size_t)g * 65 + tau) * 64 + n) * 2 + 1];
;                 const float er = cr * pr - ci * pi, ei = cr * pi + ci * pr;
;                 const f32x4* bp = (const f32x4*)(BBAR + ((size_t)g * 64 + n) * 32);
; #pragma unroll
;                 for (int q = 0; q < 8; ++q) { const f32x4 bb = bp[q]; s[2 * q] += er * bb[0] - ei * bb[1]; s[2 * q + 1] += er * bb[2] - ei * bb[3]; } }
;             { const float dv = (tau == 0) ? a.in[I_SD][g * 16 + p] : 0.0f;
	v_readlane_b32 s48, v17, 5
	v_readlane_b32 s49, v17, 7
	v_readlane_b32 s52, v17, 8
	v_readlane_b32 s53, v17, 10
	v_readlane_b32 s54, v17, 9
	v_readlane_b32 s55, v17, 11
	v_readlane_b32 s56, v17, 12
	v_readlane_b32 s57, v17, 14
	v_readlane_b32 s58, v17, 13
	v_readlane_b32 s59, v17, 15
	v_readlane_b32 s62, v17, 16
	v_readlane_b32 s63, v17, 18
	v_readlane_b32 s64, v17, 17
	v_readlane_b32 s65, v17, 19
	v_readlane_b32 s68, v17, 20
	v_readlane_b32 s69, v17, 22
	v_readlane_b32 s70, v17, 21
	v_readlane_b32 s71, v17, 23
	v_readlane_b32 s72, v17, 24
	v_readlane_b32 s73, v17, 26
	v_readlane_b32 s80, v17, 25
	v_readlane_b32 s81, v17, 27
	v_readlane_b32 s82, v17, 28
	v_readlane_b32 s83, v17, 30
	v_readlane_b32 s84, v17, 29
	v_readlane_b32 s85, v17, 31
	v_mul_f32_e32 v244, v72, v82
	v_mul_f32_e32 v245, v76, v83
	v_sub_f32_e32 v86, v244, v245
	v_mul_f32_e32 v244, v76, v82
	v_mul_f32_e32 v245, v72, v83
	v_add_f32_e32 v88, v244, v245
	v_pk_mul_f32 v[90:91], v[88:89], s[44:45] op_sel_hi:[0,1]
	v_pk_fma_f32 v[90:91], v[86:87], s[16:17], v[90:91] op_sel_hi:[0,1,1] neg_lo:[0,0,1] neg_hi:[0,0,1]
	v_pk_add_f32 v[56:57], v[56:57], v[90:91]
	v_pk_mul_f32 v[90:91], v[88:89], s[48:49] op_sel_hi:[0,1]
	v_pk_fma_f32 v[90:91], v[86:87], s[46:47], v[90:91] op_sel_hi:[0,1,1] neg_lo:[0,0,1] neg_hi:[0,0,1]
	v_pk_add_f32 v[54:55], v[54:55], v[90:91]
	v_pk_mul_f32 v[90:91], v[88:89], s[54:55] op_sel_hi:[0,1]
	v_pk_fma_f32 v[90:91], v[86:87], s[52:53], v[90:91] op_sel_hi:[0,1,1] neg_lo:[0,0,1] neg_hi:[0,0,1]
	v_pk_add_f32 v[52:53], v[52:53], v[90:91]
	v_pk_mul_f32 v[90:91], v[88:89], s[58:59] op_sel_hi:[0,1]
	v_pk_fma_f32 v[90:91], v[86:87], s[56:57], v[90:91] op_sel_hi:[0,1,1] neg_lo:[0,0,1] neg_hi:[0,0,1]
	v_pk_add_f32 v[50:51], v[50:51], v[90:91]
	v_pk_mul_f32 v[90:91], v[88:89], s[64:65] op_sel_hi:[0,1]
	v_pk_fma_f32 v[90:91], v[86:87], s[62:63], v[90:91] op_sel_hi:[0,1,1] neg_lo:[0,0,1] neg_hi:[0,0,1]
	v_pk_add_f32 v[58:59], v[58:59], v[90:91]
	v_pk_mul_f32 v[90:91], v[88:89], s[70:71] op_sel_hi:[0,1]
	v_pk_fma_f32 v[90:91], v[86:87], s[68:69], v[90:91] op_sel_hi:[0,1,1] neg_lo:[0,0,1] neg_hi:[0,0,1]
	v_pk_add_f32 v[60:61], v[60:61], v[90:91]
	v_pk_mul_f32 v[90:91], v[88:89], s[80:81] op_sel_hi:[0,1]
	v_pk_fma_f32 v[90:91], v[86:87], s[72:73], v[90:91] op_sel_hi:[0,1,1] neg_lo:[0,0,1] neg_hi:[0,0,1]
	v_pk_add_f32 v[64:65], v[64:65], v[90:91]
	v_pk_mul_f32 v[90:91], v[88:89], s[84:85] op_sel_hi:[0,1]
	v_pk_fma_f32 v[90:91], v[86:87], s[82:83], v[90:91] op_sel_hi:[0,1,1] neg_lo:[0,0,1] neg_hi:[0,0,1]
	v_pk_add_f32 v[62:63], v[62:63], v[90:91]
	v_readlane_b32 s16, v17, 32
	v_readlane_b32 s17, v17, 34
	v_readlane_b32 s44, v17, 33
	v_readlane_b32 s45, v17, 35
	v_readlane_b32 s46, v17, 36
	v_readlane_b32 s47, v17, 38
	v_readlane_b32 s48, v17, 37
	v_readlane_b32 s49, v17, 39
	v_readlane_b32 s52, v17, 40
	v_readlane_b32 s53, v17, 42
	v_readlane_b32 s54, v17, 41
	v_readlane_b32 s55, v17, 43
	v_readlane_b32 s56, v17, 44
	v_readlane_b32 s57, v17, 46
	v_readlane_b32 s58, v17, 45
	v_readlane_b32 s59, v17, 47
	v_readlane_b32 s62, v17, 48
	v_readlane_b32 s63, v17, 50
	v_readlane_b32 s64, v17, 49
	v_readlane_b32 s65, v17, 51
	v_readlane_b32 s68, v17, 52
	v_readlane_b32 s69, v17, 54
	v_readlane_b32 s70, v17, 53
	v_readlane_b32 s71, v17, 55
	v_readlane_b32 s72, v17, 56
	v_readlane_b32 s73, v17, 58
	v_readlane_b32 s80, v17, 57
	v_readlane_b32 s81, v17, 59
	v_readlane_b32 s82, v17, 60
	v_readlane_b32 s83, v17, 62
	v_readlane_b32 s84, v17, 61
	v_readlane_b32 s85, v17, 63
	v_mul_f32_e32 v244, v73, v84
	v_mul_f32_e32 v245, v77, v85
	v_sub_f32_e32 v86, v244, v245
	v_mul_f32_e32 v244, v77, v84
	v_mul_f32_e32 v245, v73, v85
	v_add_f32_e32 v88, v244, v245
	v_pk_mul_f32 v[90:91], v[88:89], s[44:45] op_sel_hi:[0,1]
	v_pk_fma_f32 v[90:91], v[86:87], s[16:17], v[90:91] op_sel_hi:[0,1,1] neg_lo:[0,0,1] neg_hi:[0,0,1]
	v_pk_add_f32 v[56:57], v[56:57], v[90:91]
	v_pk_mul_f32 v[90:91], v[88:89], s[48:49] op_sel_hi:[0,1]
	v_pk_fma_f32 v[90:91], v[86:87], s[46:47], v[90:91] op_sel_hi:[0,1,1] neg_lo:[0,0,1] neg_hi:[0,0,1]
	v_pk_add_f32 v[54:55], v[54:55], v[90:91]
	v_pk_mul_f32 v[90:91], v[88:89], s[54:55] op_sel_hi:[0,1]
	v_pk_fma_f32 v[90:91], v[86:87], s[52:53], v[90:91] op_sel_hi:[0,1,1] neg_lo:[0,0,1] neg_hi:[0,0,1]
	v_pk_add_f32 v[52:53], v[52:53], v[90:91]
	v_pk_mul_f32 v[90:91], v[88:89], s[58:59] op_sel_hi:[0,1]
	v_pk_fma_f32 v[90:91], v[86:87], s[56:57], v[90:91] op_sel_hi:[0,1,1] neg_lo:[0,0,1] neg_hi:[0,0,1]
	v_pk_add_f32 v[50:51], v[50:51], v[90:91]
	v_pk_mul_f32 v[90:91], v[88:89], s[64:65] op_sel_hi:[0,1]
	v_pk_fma_f32 v[90:91], v[86:87], s[62:63], v[90:91] op_sel_hi:[0,1,1] neg_lo:[0,0,1] neg_hi:[0,0,1]
	v_pk_add_f32 v[58:59], v[58:59], v[90:91]
	v_pk_mul_f32 v[90:91], v[88:89], s[70:71] op_sel_hi:[0,1]
	v_pk_fma_f32 v[90:91], v[86:87], s[68:69], v[90:91] op_sel_hi:[0,1,1] neg_lo:[0,0,1] neg_hi:[0,0,1]
	v_pk_add_f32 v[60:61], v[60:61], v[90:91]
	v_pk_mul_f32 v[90:91], v[88:89], s[80:81] op_sel_hi:[0,1]
	v_pk_fma_f32 v[90:91], v[86:87], s[72:73], v[90:91] op_sel_hi:[0,1,1] neg_lo:[0,0,1] neg_hi:[0,0,1]
	v_pk_add_f32 v[64:65], v[64:65], v[90:91]
	v_pk_mul_f32 v[90:91], v[88:89], s[84:85] op_sel_hi:[0,1]
	v_pk_fma_f32 v[90:91], v[86:87], s[82:83], v[90:91] op_sel_hi:[0,1,1] neg_lo:[0,0,1] neg_hi:[0,0,1]
	v_pk_add_f32 v[62:63], v[62:63], v[90:91]
	s_add_u32 s98, s98, 0x1000
	s_addc_u32 s99, s99, 0
	v_add_co_u32_e32 v44, vcc, 0x80, v44
	s_nop 0
	v_addc_co_u32_e32 v45, vcc, 0, v45, vcc
	v_add_co_u32_e32 v42, vcc, 0x80, v42
	s_nop 0
	v_addc_co_u32_e32 v43, vcc, 0, v43, vcc
	v_add_u32_e32 v40, 0x100, v40
	s_add_i32 s32, s32, -1
	s_cmp_lg_u32 s32, 0
	s_cbranch_scc1 .Lktb_half
	v_and_b32_e32 v2, 31, v66
	v_cmp_eq_u32_e32 vcc, 0, v2
	v_mov_b32_e32 v3, 0
	s_and_saveexec_b64 s[40:41], vcc
	s_cbranch_execz .LBB0_322
	v_lshl_or_b32 v4, v36, 4, v160
	v_readlane_b32 s0, v250, 33
	v_ashrrev_i32_e32 v5, 31, v4
	v_readlane_b32 s14, v250, 47
	v_readlane_b32 s15, v250, 48
	v_readlane_b32 s1, v250, 34
	v_readlane_b32 s2, v250, 35
	v_lshl_add_u64 v[4:5], v[4:5], 2, s[14:15]
	global_load_dword v3, v[4:5], off
	v_readlane_b32 s3, v250, 36
	v_readlane_b32 s4, v250, 37
	v_readlane_b32 s5, v250, 38
	v_readlane_b32 s6, v250, 39
	v_readlane_b32 s7, v250, 40
	v_readlane_b32 s8, v250, 41
	v_readlane_b32 s9, v250, 42
	v_readlane_b32 s10, v250, 43
	v_readlane_b32 s11, v250, 44
	v_readlane_b32 s12, v250, 45
	v_readlane_b32 s13, v250, 46
	s_branch .LBB0_322
; __device__ __forceinline__ void ph1_small(const Args& a, int tid, int wave, int lane, int G, int bid) {
;     ...
;         for (int idx = (tid < 128 ? bid * 128 + tid : SSMG * SL * 16); idx < SSMG * SL * 16; idx += G * 128) {
;             const int g = idx >> 9, tau = (idx >> 4) & 31, p = idx & 15; float s[16];
; #pragma unroll
;             for (int q = 0; q < 16; ++q) s[q] = 0.f;
; #pragma unroll 8
;             for (int n = 0; n < 64; ++n) { const float cr = cre[((size_t)g * 16 + p) * 64 + n], ci = cim[((size_t)g * 16 + p) * 64 + n];
;                 const float pr = POW[(((size_t)g * 65 + tau) * 64 + n) * 2], pi = POW[(((size_t)g * 65 + tau) * 64 + n) * 2 + 1];
;                 const float er = cr * pr - ci * pi, ei = cr * pi + ci * pr;
;                 const f32x4* bp = (const f32x4*)(BBAR + ((size_t)g * 64 + n) * 32);
; #pragma unroll
;                 for (int q = 0; q < 8; ++q) { const f32x4 bb = bp[q]; s[2 * q] += er * bb[0] - ei * bb[1]; s[2 * q + 1] += er * bb[2] - ei * bb[3]; } }
.Lktb_restore:
	v_readlane_b32 s16, v249, 0
	v_readlane_b32 s17, v249, 1
	v_readlane_b32 s44, v249, 2
	v_readlane_b32 s45, v249, 3
	v_readlane_b32 s46, v249, 4
	v_readlane_b32 s47, v249, 5
	v_readlane_b32 s48, v249, 6
	v_readlane_b32 s49, v249, 7
	v_readlane_b32 s52, v249, 8
	v_readlane_b32 s53, v249, 9
	v_readlane_b32 s54, v249, 10
	v_readlane_b32 s55, v249, 11
	v_readlane_b32 s56, v249, 12
	v_readlane_b32 s57, v249, 13
	v_readlane_b32 s58, v249, 14
	v_readlane_b32 s59, v249, 15
	v_readlane_b32 s62, v249, 16
	v_readlane_b32 s63, v249, 17
	v_readlane_b32 s64, v249, 18
	v_readlane_b32 s65, v249, 19
	v_readlane_b32 s68, v249, 20
	v_readlane_b32 s69, v249, 21
	v_readlane_b32 s70, v249, 22
	v_readlane_b32 s71, v249, 23
	v_readlane_b32 s72, v249, 24
	v_readlane_b32 s73, v249, 25
	v_readlane_b32 s80, v249, 26
	v_readlane_b32 s81, v249, 27
	v_readlane_b32 s82, v249, 28
	v_readlane_b32 s83, v249, 29
	v_readlane_b32 s84, v249, 30
	v_readlane_b32 s85, v249, 31
	s_nop 4
